# speedup vs baseline: 1.0009x; 1.0009x over previous
.LBB6_32:
	s_or_b64 exec, exec, s[2:3]
	s_add_i32 s0, 0, 0x18000
	v_add_u32_e32 v48, s0, v39
	s_mov_b64 s[0:1], 0x80
	v_readfirstlane_b32 s22, v48
	v_add_u32_e32 v49, 0x2000, v48
	v_lshl_add_u64 v[2:3], v[30:31], 0, s[0:1]
	s_mov_b32 m0, s22
	v_readfirstlane_b32 s21, v49
	v_add_u32_e32 v46, 0x8000, v35
	s_waitcnt vmcnt(4)
	s_barrier
	global_load_lds_dwordx4 v[2:3], off
	v_lshl_add_u64 v[2:3], v[32:33], 0, s[0:1]
	s_mov_b32 m0, s21
	v_readfirstlane_b32 s19, v46
	v_add_u32_e32 v47, 0xa000, v35
	s_add_i32 s2, 0, 0x1c000
	global_load_lds_dwordx4 v[2:3], off
	v_lshl_add_u64 v[2:3], v[26:27], 0, s[0:1]
	s_mov_b32 m0, s19
	v_readfirstlane_b32 s17, v47
	v_add_u32_e32 v38, s2, v39
	global_load_lds_dwordx4 v[2:3], off
	v_lshl_add_u64 v[2:3], v[28:29], 0, s[0:1]
	s_mov_b32 m0, s17
	v_readfirstlane_b32 s4, v38
	v_add_u32_e32 v40, 0x2000, v38
	global_load_lds_dwordx4 v[2:3], off
	v_lshl_add_u64 v[2:3], v[22:23], 0, s[0:1]
	s_mov_b32 m0, s4
	v_readfirstlane_b32 s3, v40
	global_load_lds_dwordx4 v[2:3], off
	v_lshl_add_u64 v[2:3], v[24:25], 0, s[0:1]
	s_mov_b32 m0, s3
	v_and_b32_e32 v4, 48, v0
	global_load_lds_dwordx4 v[2:3], off
	v_lshlrev_b32_e32 v2, 6, v0
	v_and_b32_e32 v3, 0x3c0, v2
	v_and_b32_e32 v5, 32, v103
	v_bitop3_b32 v6, v3, v5, v4 bitop3:0x36
	v_and_b32_e32 v2, 0x3000, v2
	v_add3_u32 v234, 0, v2, v6
	v_add_u32_e32 v2, 0x10000, v234
	v_add_u32_e32 v4, 0x10800, v234
	s_waitcnt vmcnt(6)
	s_barrier
	v_add_u32_e32 v3, 0x10400, v234
	ds_read_b128 v[10:13], v2
	ds_read_b128 v[14:17], v3
	v_add_u32_e32 v5, 0x10c00, v234
	ds_read_b128 v[50:53], v4
	ds_read_b128 v[54:57], v5
	v_and_b32_e32 v1, 0x2000, v1
	v_add3_u32 v1, 0, v1, v6
	v_add_u32_e32 v37, 0xc000, v35
	v_add_u32_e32 v39, 0xe000, v35
	v_readfirstlane_b32 s7, v37
	v_lshl_add_u64 v[6:7], v[18:19], 0, s[0:1]
	s_mov_b32 m0, s7
	v_readfirstlane_b32 s2, v39
	global_load_lds_dwordx4 v[6:7], off
	v_lshl_add_u64 v[6:7], v[20:21], 0, s[0:1]
	s_mov_b32 m0, s2
	s_nop 0
	global_load_lds_dwordx4 v[6:7], off
	ds_read_b128 v[42:45], v1
	ds_read_b128 v[58:61], v1 offset:1024
	ds_read_b128 v[62:65], v1 offset:2048
	ds_read_b128 v[66:69], v1 offset:3072
	ds_read_b128 v[70:73], v1 offset:4096
	ds_read_b128 v[74:77], v1 offset:5120
	ds_read_b128 v[78:81], v1 offset:6144
	ds_read_b128 v[82:85], v1 offset:7168
	s_waitcnt lgkmcnt(8)
	s_barrier
	s_waitcnt lgkmcnt(0)
	s_setprio 1
	s_waitcnt lgkmcnt(0)
	v_mfma_f32_16x16x32_f16 v[6:9], v[10:13], v[42:45], 0
	v_mfma_f32_16x16x32_f16 v[86:89], v[14:17], v[58:61], v[6:9]
	v_mfma_f32_16x16x32_f16 v[6:9], v[50:53], v[42:45], 0
	v_mfma_f32_16x16x32_f16 v[90:93], v[54:57], v[58:61], v[6:9]
	v_mfma_f32_16x16x32_f16 v[6:9], v[10:13], v[62:65], 0
	v_mfma_f32_16x16x32_f16 v[94:97], v[14:17], v[66:69], v[6:9]
	v_mfma_f32_16x16x32_f16 v[6:9], v[50:53], v[62:65], 0
	v_mfma_f32_16x16x32_f16 v[98:101], v[54:57], v[66:69], v[6:9]
	v_mfma_f32_16x16x32_f16 v[6:9], v[10:13], v[70:73], 0
	v_mfma_f32_16x16x32_f16 v[102:105], v[14:17], v[74:77], v[6:9]
	v_mfma_f32_16x16x32_f16 v[6:9], v[50:53], v[70:73], 0
	v_mfma_f32_16x16x32_f16 v[106:109], v[54:57], v[74:77], v[6:9]
	v_mfma_f32_16x16x32_f16 v[6:9], v[10:13], v[78:81], 0
	v_mfma_f32_16x16x32_f16 v[110:113], v[14:17], v[82:85], v[6:9]
	v_mfma_f32_16x16x32_f16 v[6:9], v[50:53], v[78:81], 0
	v_mfma_f32_16x16x32_f16 v[114:117], v[54:57], v[82:85], v[6:9]
	s_setprio 0
	s_barrier
	s_mov_b64 s[0:1], 0x100
	v_readfirstlane_b32 s15, v36
	v_add_u32_e32 v41, 0x2000, v36
	s_nop 1
	v_add_u32_e32 v6, 0x14000, v234
	v_add_u32_e32 v8, 0x14800, v234
	v_lshl_add_u64 v[134:135], v[30:31], 0, s[0:1]
	s_mov_b32 m0, s15
	v_readfirstlane_b32 s5, v41
	v_add_u32_e32 v7, 0x14400, v234
	ds_read_b128 v[118:121], v6
	ds_read_b128 v[122:125], v7
	v_add_u32_e32 v9, 0x14c00, v234
	ds_read_b128 v[126:129], v8
	ds_read_b128 v[130:133], v9
	global_load_lds_dwordx4 v[134:135], off
	v_lshl_add_u64 v[134:135], v[32:33], 0, s[0:1]
	s_mov_b32 m0, s5
	s_nop 0
	global_load_lds_dwordx4 v[134:135], off
	s_barrier
	s_waitcnt lgkmcnt(0)
	s_setprio 1
	s_waitcnt lgkmcnt(0)
	v_mfma_f32_16x16x32_f16 v[134:137], v[118:121], v[42:45], 0
	v_mfma_f32_16x16x32_f16 v[42:45], v[126:129], v[42:45], 0
	v_mfma_f32_16x16x32_f16 v[134:137], v[122:125], v[58:61], v[134:137]
	v_mfma_f32_16x16x32_f16 v[58:61], v[130:133], v[58:61], v[42:45]
	v_mfma_f32_16x16x32_f16 v[42:45], v[118:121], v[62:65], 0
	v_mfma_f32_16x16x32_f16 v[138:141], v[122:125], v[66:69], v[42:45]
	v_mfma_f32_16x16x32_f16 v[42:45], v[126:129], v[62:65], 0
	v_mfma_f32_16x16x32_f16 v[62:65], v[130:133], v[66:69], v[42:45]
	v_mfma_f32_16x16x32_f16 v[42:45], v[118:121], v[70:73], 0
	v_mfma_f32_16x16x32_f16 v[66:69], v[122:125], v[74:77], v[42:45]
	v_mfma_f32_16x16x32_f16 v[42:45], v[126:129], v[70:73], 0
	v_mfma_f32_16x16x32_f16 v[70:73], v[130:133], v[74:77], v[42:45]
	v_mfma_f32_16x16x32_f16 v[42:45], v[118:121], v[78:81], 0
	v_mfma_f32_16x16x32_f16 v[74:77], v[122:125], v[82:85], v[42:45]
	v_mfma_f32_16x16x32_f16 v[42:45], v[126:129], v[78:81], 0
	v_mfma_f32_16x16x32_f16 v[78:81], v[130:133], v[82:85], v[42:45]
	s_setprio 0
	v_readfirstlane_b32 s16, v35
	s_nop 4
	v_lshl_add_u64 v[42:43], v[26:27], 0, s[0:1]
	s_mov_b32 m0, s16
	s_barrier
	ds_read_b128 v[82:85], v1 offset:16384
	ds_read_b128 v[142:145], v1 offset:17408
	ds_read_b128 v[146:149], v1 offset:18432
	ds_read_b128 v[150:153], v1 offset:19456
	ds_read_b128 v[154:157], v1 offset:20480
	ds_read_b128 v[158:161], v1 offset:21504
	ds_read_b128 v[162:165], v1 offset:22528
	ds_read_b128 v[166:169], v1 offset:23552
	global_load_lds_dwordx4 v[42:43], off
	v_add_u32_e32 v42, 0x2000, v35
	v_lshl_add_u64 v[44:45], v[28:29], 0, s[0:1]
	v_readfirstlane_b32 s10, v42
	s_mov_b32 m0, s10
	s_nop 0
	global_load_lds_dwordx4 v[44:45], off
	s_barrier
	s_waitcnt lgkmcnt(0)
	s_setprio 1
	s_waitcnt lgkmcnt(0)
	v_mfma_f32_16x16x32_f16 v[170:173], v[10:13], v[82:85], 0
	v_mfma_f32_16x16x32_f16 v[178:181], v[10:13], v[146:149], 0
	v_mfma_f32_16x16x32_f16 v[186:189], v[10:13], v[154:157], 0
	v_mfma_f32_16x16x32_f16 v[10:13], v[10:13], v[162:165], 0
	v_mfma_f32_16x16x32_f16 v[174:177], v[50:53], v[82:85], 0
	v_mfma_f32_16x16x32_f16 v[182:185], v[50:53], v[146:149], 0
	v_mfma_f32_16x16x32_f16 v[190:193], v[50:53], v[154:157], 0
	v_mfma_f32_16x16x32_f16 v[194:197], v[14:17], v[166:169], v[10:13]
	v_mfma_f32_16x16x32_f16 v[10:13], v[50:53], v[162:165], 0
	v_mfma_f32_16x16x32_f16 v[170:173], v[14:17], v[142:145], v[170:173]
	v_mfma_f32_16x16x32_f16 v[174:177], v[54:57], v[142:145], v[174:177]
	v_mfma_f32_16x16x32_f16 v[178:181], v[14:17], v[150:153], v[178:181]
	v_mfma_f32_16x16x32_f16 v[182:185], v[54:57], v[150:153], v[182:185]
	v_mfma_f32_16x16x32_f16 v[186:189], v[14:17], v[158:161], v[186:189]
	v_mfma_f32_16x16x32_f16 v[190:193], v[54:57], v[158:161], v[190:193]
	v_mfma_f32_16x16x32_f16 v[50:53], v[54:57], v[166:169], v[10:13]
	s_setprio 0
	s_barrier
	v_readfirstlane_b32 s14, v34
	v_add_u32_e32 v43, 0x2000, v34
	v_lshl_add_u64 v[10:11], v[22:23], 0, s[0:1]
	s_mov_b32 m0, s14
	v_readfirstlane_b32 s11, v43
	global_load_lds_dwordx4 v[10:11], off
	v_lshl_add_u64 v[10:11], v[24:25], 0, s[0:1]
	s_mov_b32 m0, s11
	s_nop 0
	global_load_lds_dwordx4 v[10:11], off
	s_waitcnt vmcnt(6)
	s_barrier
	s_setprio 1
	v_mfma_f32_16x16x32_f16 v[10:13], v[118:121], v[82:85], 0
	v_mfma_f32_16x16x32_f16 v[54:57], v[122:125], v[142:145], v[10:13]
	v_mfma_f32_16x16x32_f16 v[10:13], v[126:129], v[82:85], 0
	v_mfma_f32_16x16x32_f16 v[82:85], v[130:133], v[142:145], v[10:13]
	v_mfma_f32_16x16x32_f16 v[10:13], v[118:121], v[146:149], 0
	v_mfma_f32_16x16x32_f16 v[142:145], v[122:125], v[150:153], v[10:13]
	v_mfma_f32_16x16x32_f16 v[10:13], v[126:129], v[146:149], 0
	v_mfma_f32_16x16x32_f16 v[146:149], v[130:133], v[150:153], v[10:13]
	v_mfma_f32_16x16x32_f16 v[10:13], v[118:121], v[154:157], 0
	v_mfma_f32_16x16x32_f16 v[150:153], v[122:125], v[158:161], v[10:13]
	v_mfma_f32_16x16x32_f16 v[10:13], v[126:129], v[154:157], 0
	v_mfma_f32_16x16x32_f16 v[154:157], v[130:133], v[158:161], v[10:13]
	v_mfma_f32_16x16x32_f16 v[10:13], v[118:121], v[162:165], 0
	v_mfma_f32_16x16x32_f16 v[118:121], v[122:125], v[166:169], v[10:13]
	v_mfma_f32_16x16x32_f16 v[10:13], v[126:129], v[162:165], 0
	v_mfma_f32_16x16x32_f16 v[122:125], v[130:133], v[166:169], v[10:13]
	s_setprio 0
	s_nop 5
	v_add_u32_e32 v10, 0x18000, v234
	v_add_u32_e32 v12, 0x18800, v234
	s_barrier
	v_add_u32_e32 v11, 0x18400, v234
	ds_read_b128 v[126:129], v10
	ds_read_b128 v[130:133], v11
	v_add_u32_e32 v13, 0x18c00, v234
	ds_read_b128 v[158:161], v12
	ds_read_b128 v[162:165], v13
	v_add_u32_e32 v44, 0x4000, v35
	v_add_u32_e32 v45, 0x6000, v35
	v_readfirstlane_b32 s20, v44
	v_lshl_add_u64 v[14:15], v[18:19], 0, s[0:1]
	s_mov_b32 m0, s20
	v_readfirstlane_b32 s18, v45
	ds_read_b128 v[166:169], v1 offset:32768
	ds_read_b128 v[198:201], v1 offset:33792
	ds_read_b128 v[202:205], v1 offset:34816
	ds_read_b128 v[206:209], v1 offset:35840
	ds_read_b128 v[210:213], v1 offset:36864
	ds_read_b128 v[214:217], v1 offset:37888
	ds_read_b128 v[218:221], v1 offset:38912
	ds_read_b128 v[222:225], v1 offset:39936
	global_load_lds_dwordx4 v[14:15], off
	v_lshl_add_u64 v[14:15], v[20:21], 0, s[0:1]
	s_mov_b32 m0, s18
	s_nop 0
	global_load_lds_dwordx4 v[14:15], off
	s_waitcnt lgkmcnt(8)
	s_barrier
	s_waitcnt lgkmcnt(0)
	s_setprio 1
	s_waitcnt lgkmcnt(0)
	v_mfma_f32_16x16x32_f16 v[14:17], v[126:129], v[166:169], v[86:89]
	v_mfma_f32_16x16x32_f16 v[86:89], v[130:133], v[198:201], v[14:17]
	v_mfma_f32_16x16x32_f16 v[14:17], v[158:161], v[166:169], v[90:93]
	v_mfma_f32_16x16x32_f16 v[90:93], v[162:165], v[198:201], v[14:17]
	v_mfma_f32_16x16x32_f16 v[14:17], v[126:129], v[202:205], v[94:97]
	v_mfma_f32_16x16x32_f16 v[94:97], v[130:133], v[206:209], v[14:17]
	v_mfma_f32_16x16x32_f16 v[14:17], v[158:161], v[202:205], v[98:101]
	v_mfma_f32_16x16x32_f16 v[98:101], v[162:165], v[206:209], v[14:17]
	v_mfma_f32_16x16x32_f16 v[14:17], v[126:129], v[210:213], v[102:105]
	v_mfma_f32_16x16x32_f16 v[102:105], v[130:133], v[214:217], v[14:17]
	v_mfma_f32_16x16x32_f16 v[14:17], v[158:161], v[210:213], v[106:109]
	v_mfma_f32_16x16x32_f16 v[106:109], v[162:165], v[214:217], v[14:17]
	v_mfma_f32_16x16x32_f16 v[14:17], v[126:129], v[218:221], v[110:113]
	v_mfma_f32_16x16x32_f16 v[110:113], v[130:133], v[222:225], v[14:17]
	v_mfma_f32_16x16x32_f16 v[14:17], v[158:161], v[218:221], v[114:117]
	v_mfma_f32_16x16x32_f16 v[114:117], v[162:165], v[222:225], v[14:17]
	s_setprio 0
	s_barrier
	s_mov_b64 s[0:1], 0x180
	s_mov_b32 m0, s22
	s_nop 2
	v_add_u32_e32 v14, 0x1c000, v234
	v_add_u32_e32 v16, 0x1c800, v234
	v_lshl_add_u64 v[242:243], v[30:31], 0, s[0:1]
	v_add_u32_e32 v15, 0x1c400, v234
	ds_read_b128 v[226:229], v14
	ds_read_b128 v[230:233], v15
	v_add_u32_e32 v17, 0x1cc00, v234
	ds_read_b128 v[234:237], v16
	ds_read_b128 v[238:241], v17
	global_load_lds_dwordx4 v[242:243], off
	v_lshl_add_u64 v[242:243], v[32:33], 0, s[0:1]
	s_mov_b32 m0, s21
	s_nop 0
	global_load_lds_dwordx4 v[242:243], off
	s_barrier
	s_waitcnt lgkmcnt(0)
	s_setprio 1
	s_waitcnt lgkmcnt(0)
	v_mfma_f32_16x16x32_f16 v[134:137], v[226:229], v[166:169], v[134:137]
	v_mfma_f32_16x16x32_f16 v[138:141], v[226:229], v[202:205], v[138:141]
	v_mfma_f32_16x16x32_f16 v[66:69], v[226:229], v[210:213], v[66:69]
	v_mfma_f32_16x16x32_f16 v[70:73], v[234:237], v[210:213], v[70:73]
	v_mfma_f32_16x16x32_f16 v[74:77], v[226:229], v[218:221], v[74:77]
	v_mfma_f32_16x16x32_f16 v[78:81], v[234:237], v[218:221], v[78:81]
	v_mfma_f32_16x16x32_f16 v[134:137], v[230:233], v[198:201], v[134:137]
	v_mfma_f32_16x16x32_f16 v[58:61], v[234:237], v[166:169], v[58:61]
	v_mfma_f32_16x16x32_f16 v[138:141], v[230:233], v[206:209], v[138:141]
	v_mfma_f32_16x16x32_f16 v[62:65], v[234:237], v[202:205], v[62:65]
	v_mfma_f32_16x16x32_f16 v[66:69], v[230:233], v[214:217], v[66:69]
	v_mfma_f32_16x16x32_f16 v[70:73], v[238:241], v[214:217], v[70:73]
	v_mfma_f32_16x16x32_f16 v[74:77], v[230:233], v[222:225], v[74:77]
	v_mfma_f32_16x16x32_f16 v[78:81], v[238:241], v[222:225], v[78:81]
	v_mfma_f32_16x16x32_f16 v[58:61], v[238:241], v[198:201], v[58:61]
	v_mfma_f32_16x16x32_f16 v[62:65], v[238:241], v[206:209], v[62:65]
	s_setprio 0
	s_mov_b32 m0, s19
	v_lshl_add_u64 v[242:243], v[26:27], 0, s[0:1]
	s_barrier
	ds_read_b128 v[166:169], v1 offset:49152
	ds_read_b128 v[198:201], v1 offset:50176
	ds_read_b128 v[202:205], v1 offset:51200
	ds_read_b128 v[206:209], v1 offset:52224
	ds_read_b128 v[210:213], v1 offset:53248
	ds_read_b128 v[214:217], v1 offset:54272
	ds_read_b128 v[218:221], v1 offset:55296
	ds_read_b128 v[222:225], v1 offset:56320
	global_load_lds_dwordx4 v[242:243], off
	v_lshl_add_u64 v[242:243], v[28:29], 0, s[0:1]
	s_mov_b32 m0, s17
	s_nop 0
	global_load_lds_dwordx4 v[242:243], off
	s_barrier
	s_waitcnt lgkmcnt(0)
	s_setprio 1
	s_waitcnt lgkmcnt(0)
	v_mfma_f32_16x16x32_f16 v[170:173], v[126:129], v[166:169], v[170:173]
	v_mfma_f32_16x16x32_f16 v[178:181], v[126:129], v[202:205], v[178:181]
	v_mfma_f32_16x16x32_f16 v[186:189], v[126:129], v[210:213], v[186:189]
	v_mfma_f32_16x16x32_f16 v[126:129], v[126:129], v[218:221], v[194:197]
	v_mfma_f32_16x16x32_f16 v[174:177], v[158:161], v[166:169], v[174:177]
	v_mfma_f32_16x16x32_f16 v[182:185], v[158:161], v[202:205], v[182:185]
	v_mfma_f32_16x16x32_f16 v[190:193], v[158:161], v[210:213], v[190:193]
	v_mfma_f32_16x16x32_f16 v[126:129], v[130:133], v[222:225], v[126:129]
	v_mfma_f32_16x16x32_f16 v[50:53], v[158:161], v[218:221], v[50:53]
	v_mfma_f32_16x16x32_f16 v[170:173], v[130:133], v[198:201], v[170:173]
	v_mfma_f32_16x16x32_f16 v[174:177], v[162:165], v[198:201], v[174:177]
	v_mfma_f32_16x16x32_f16 v[178:181], v[130:133], v[206:209], v[178:181]
	v_mfma_f32_16x16x32_f16 v[182:185], v[162:165], v[206:209], v[182:185]
	v_mfma_f32_16x16x32_f16 v[186:189], v[130:133], v[214:217], v[186:189]
	v_mfma_f32_16x16x32_f16 v[190:193], v[162:165], v[214:217], v[190:193]
	v_mfma_f32_16x16x32_f16 v[50:53], v[162:165], v[222:225], v[50:53]
	s_setprio 0
	s_barrier
	s_mov_b32 m0, s4
	v_lshl_add_u64 v[130:131], v[22:23], 0, s[0:1]
	global_load_lds_dwordx4 v[130:131], off
	v_lshl_add_u64 v[130:131], v[24:25], 0, s[0:1]
	s_mov_b32 m0, s3
	s_nop 0
	global_load_lds_dwordx4 v[130:131], off
	s_waitcnt vmcnt(6)
	s_barrier
	s_setprio 1
	v_mfma_f32_16x16x32_f16 v[82:85], v[234:237], v[166:169], v[82:85]
	v_mfma_f32_16x16x32_f16 v[130:133], v[226:229], v[202:205], v[142:145]
	v_mfma_f32_16x16x32_f16 v[142:145], v[234:237], v[202:205], v[146:149]
	v_mfma_f32_16x16x32_f16 v[146:149], v[226:229], v[210:213], v[150:153]
	v_mfma_f32_16x16x32_f16 v[150:153], v[234:237], v[210:213], v[154:157]
	v_mfma_f32_16x16x32_f16 v[118:121], v[226:229], v[218:221], v[118:121]
	v_mfma_f32_16x16x32_f16 v[122:125], v[234:237], v[218:221], v[122:125]
	v_mfma_f32_16x16x32_f16 v[54:57], v[226:229], v[166:169], v[54:57]
	v_mfma_f32_16x16x32_f16 v[82:85], v[238:241], v[198:201], v[82:85]
	v_mfma_f32_16x16x32_f16 v[130:133], v[230:233], v[206:209], v[130:133]
	v_mfma_f32_16x16x32_f16 v[142:145], v[238:241], v[206:209], v[142:145]
	v_mfma_f32_16x16x32_f16 v[150:153], v[238:241], v[214:217], v[150:153]
	v_mfma_f32_16x16x32_f16 v[118:121], v[230:233], v[222:225], v[118:121]
	v_mfma_f32_16x16x32_f16 v[122:125], v[238:241], v[222:225], v[122:125]
	v_mfma_f32_16x16x32_f16 v[54:57], v[230:233], v[198:201], v[54:57]
	v_mfma_f32_16x16x32_f16 v[146:149], v[230:233], v[214:217], v[146:149]
	s_setprio 0
	s_barrier
	ds_read_b128 v[154:157], v2
	ds_read_b128 v[158:161], v3
	ds_read_b128 v[162:165], v4
	ds_read_b128 v[166:169], v5
	s_mov_b32 m0, s7
	v_lshl_add_u64 v[194:195], v[18:19], 0, s[0:1]
	global_load_lds_dwordx4 v[194:195], off
	v_lshl_add_u64 v[194:195], v[20:21], 0, s[0:1]
	s_mov_b32 m0, s2
	s_nop 0
	global_load_lds_dwordx4 v[194:195], off
	ds_read_b128 v[194:197], v1
	ds_read_b128 v[198:201], v1 offset:1024
	ds_read_b128 v[202:205], v1 offset:2048
	ds_read_b128 v[206:209], v1 offset:3072
	ds_read_b128 v[210:213], v1 offset:4096
	ds_read_b128 v[214:217], v1 offset:5120
	ds_read_b128 v[218:221], v1 offset:6144
	ds_read_b128 v[222:225], v1 offset:7168
	s_waitcnt lgkmcnt(8)
	s_barrier
	s_waitcnt lgkmcnt(0)
	s_setprio 1
	s_waitcnt lgkmcnt(0)
	v_mfma_f32_16x16x32_f16 v[86:89], v[154:157], v[194:197], v[86:89]
	v_mfma_f32_16x16x32_f16 v[90:93], v[162:165], v[194:197], v[90:93]
	v_mfma_f32_16x16x32_f16 v[94:97], v[154:157], v[202:205], v[94:97]
	v_mfma_f32_16x16x32_f16 v[98:101], v[162:165], v[202:205], v[98:101]
	v_mfma_f32_16x16x32_f16 v[102:105], v[154:157], v[210:213], v[102:105]
	v_mfma_f32_16x16x32_f16 v[106:109], v[162:165], v[210:213], v[106:109]
	v_mfma_f32_16x16x32_f16 v[110:113], v[154:157], v[218:221], v[110:113]
	v_mfma_f32_16x16x32_f16 v[114:117], v[162:165], v[218:221], v[114:117]
	v_mfma_f32_16x16x32_f16 v[86:89], v[158:161], v[198:201], v[86:89]
	v_mfma_f32_16x16x32_f16 v[90:93], v[166:169], v[198:201], v[90:93]
	v_mfma_f32_16x16x32_f16 v[94:97], v[158:161], v[206:209], v[94:97]
	v_mfma_f32_16x16x32_f16 v[98:101], v[166:169], v[206:209], v[98:101]
	v_mfma_f32_16x16x32_f16 v[102:105], v[158:161], v[214:217], v[102:105]
	v_mfma_f32_16x16x32_f16 v[106:109], v[166:169], v[214:217], v[106:109]
	v_mfma_f32_16x16x32_f16 v[110:113], v[158:161], v[222:225], v[110:113]
	v_mfma_f32_16x16x32_f16 v[114:117], v[166:169], v[222:225], v[114:117]
	s_setprio 0
	s_barrier
	s_mov_b64 s[0:1], 0x200
	s_mov_b32 m0, s15
	v_lshl_add_u64 v[242:243], v[30:31], 0, s[0:1]
	ds_read_b128 v[226:229], v6
	ds_read_b128 v[230:233], v7
	ds_read_b128 v[234:237], v8
	ds_read_b128 v[238:241], v9
	global_load_lds_dwordx4 v[242:243], off
	v_lshl_add_u64 v[242:243], v[32:33], 0, s[0:1]
	s_mov_b32 m0, s5
	s_nop 0
	global_load_lds_dwordx4 v[242:243], off
	s_barrier
	s_waitcnt lgkmcnt(0)
	s_setprio 1
	s_waitcnt lgkmcnt(0)
	v_mfma_f32_16x16x32_f16 v[134:137], v[226:229], v[194:197], v[134:137]
	v_mfma_f32_16x16x32_f16 v[138:141], v[226:229], v[202:205], v[138:141]
	v_mfma_f32_16x16x32_f16 v[66:69], v[226:229], v[210:213], v[66:69]
	v_mfma_f32_16x16x32_f16 v[70:73], v[234:237], v[210:213], v[70:73]
	v_mfma_f32_16x16x32_f16 v[74:77], v[226:229], v[218:221], v[74:77]
	v_mfma_f32_16x16x32_f16 v[78:81], v[234:237], v[218:221], v[78:81]
	v_mfma_f32_16x16x32_f16 v[134:137], v[230:233], v[198:201], v[134:137]
	v_mfma_f32_16x16x32_f16 v[58:61], v[234:237], v[194:197], v[58:61]
	v_mfma_f32_16x16x32_f16 v[138:141], v[230:233], v[206:209], v[138:141]
	v_mfma_f32_16x16x32_f16 v[62:65], v[234:237], v[202:205], v[62:65]
	v_mfma_f32_16x16x32_f16 v[66:69], v[230:233], v[214:217], v[66:69]
	v_mfma_f32_16x16x32_f16 v[70:73], v[238:241], v[214:217], v[70:73]
	v_mfma_f32_16x16x32_f16 v[74:77], v[230:233], v[222:225], v[74:77]
	v_mfma_f32_16x16x32_f16 v[78:81], v[238:241], v[222:225], v[78:81]
	v_mfma_f32_16x16x32_f16 v[58:61], v[238:241], v[198:201], v[58:61]
	v_mfma_f32_16x16x32_f16 v[62:65], v[238:241], v[206:209], v[62:65]
	s_setprio 0
	s_mov_b32 m0, s16
	v_lshl_add_u64 v[242:243], v[26:27], 0, s[0:1]
	s_barrier
	ds_read_b128 v[194:197], v1 offset:16384
	ds_read_b128 v[198:201], v1 offset:17408
	ds_read_b128 v[202:205], v1 offset:18432
	ds_read_b128 v[206:209], v1 offset:19456
	ds_read_b128 v[210:213], v1 offset:20480
	ds_read_b128 v[214:217], v1 offset:21504
	ds_read_b128 v[218:221], v1 offset:22528
	ds_read_b128 v[222:225], v1 offset:23552
	global_load_lds_dwordx4 v[242:243], off
	v_lshl_add_u64 v[242:243], v[28:29], 0, s[0:1]
	s_mov_b32 m0, s10
	s_nop 0
	global_load_lds_dwordx4 v[242:243], off
	s_barrier
	s_waitcnt lgkmcnt(0)
	s_setprio 1
	s_waitcnt lgkmcnt(0)
	v_mfma_f32_16x16x32_f16 v[126:129], v[154:157], v[218:221], v[126:129]
	v_mfma_f32_16x16x32_f16 v[170:173], v[154:157], v[194:197], v[170:173]
	v_mfma_f32_16x16x32_f16 v[174:177], v[162:165], v[194:197], v[174:177]
	v_mfma_f32_16x16x32_f16 v[178:181], v[154:157], v[202:205], v[178:181]
	v_mfma_f32_16x16x32_f16 v[182:185], v[162:165], v[202:205], v[182:185]
	v_mfma_f32_16x16x32_f16 v[186:189], v[154:157], v[210:213], v[186:189]
	v_mfma_f32_16x16x32_f16 v[190:193], v[162:165], v[210:213], v[190:193]
	v_mfma_f32_16x16x32_f16 v[126:129], v[158:161], v[222:225], v[126:129]
	v_mfma_f32_16x16x32_f16 v[50:53], v[162:165], v[218:221], v[50:53]
	v_mfma_f32_16x16x32_f16 v[170:173], v[158:161], v[198:201], v[170:173]
	v_mfma_f32_16x16x32_f16 v[174:177], v[166:169], v[198:201], v[174:177]
	v_mfma_f32_16x16x32_f16 v[178:181], v[158:161], v[206:209], v[178:181]
	v_mfma_f32_16x16x32_f16 v[182:185], v[166:169], v[206:209], v[182:185]
	v_mfma_f32_16x16x32_f16 v[186:189], v[158:161], v[214:217], v[186:189]
	v_mfma_f32_16x16x32_f16 v[190:193], v[166:169], v[214:217], v[190:193]
	v_mfma_f32_16x16x32_f16 v[50:53], v[166:169], v[222:225], v[50:53]
	s_setprio 0
	s_barrier
	s_mov_b32 m0, s14
	v_lshl_add_u64 v[154:155], v[22:23], 0, s[0:1]
	global_load_lds_dwordx4 v[154:155], off
	v_lshl_add_u64 v[154:155], v[24:25], 0, s[0:1]
	s_mov_b32 m0, s11
	s_nop 0
	global_load_lds_dwordx4 v[154:155], off
	s_waitcnt vmcnt(6)
	s_barrier
	s_setprio 1
	v_mfma_f32_16x16x32_f16 v[82:85], v[234:237], v[194:197], v[82:85]
	v_mfma_f32_16x16x32_f16 v[130:133], v[226:229], v[202:205], v[130:133]
	v_mfma_f32_16x16x32_f16 v[142:145], v[234:237], v[202:205], v[142:145]
	v_mfma_f32_16x16x32_f16 v[150:153], v[234:237], v[210:213], v[150:153]
	v_mfma_f32_16x16x32_f16 v[118:121], v[226:229], v[218:221], v[118:121]
	v_mfma_f32_16x16x32_f16 v[122:125], v[234:237], v[218:221], v[122:125]
	v_mfma_f32_16x16x32_f16 v[54:57], v[226:229], v[194:197], v[54:57]
	v_mfma_f32_16x16x32_f16 v[82:85], v[238:241], v[198:201], v[82:85]
	v_mfma_f32_16x16x32_f16 v[130:133], v[230:233], v[206:209], v[130:133]
	v_mfma_f32_16x16x32_f16 v[142:145], v[238:241], v[206:209], v[142:145]
	v_mfma_f32_16x16x32_f16 v[146:149], v[226:229], v[210:213], v[146:149]
	v_mfma_f32_16x16x32_f16 v[150:153], v[238:241], v[214:217], v[150:153]
	v_mfma_f32_16x16x32_f16 v[118:121], v[230:233], v[222:225], v[118:121]
	v_mfma_f32_16x16x32_f16 v[122:125], v[238:241], v[222:225], v[122:125]
	v_mfma_f32_16x16x32_f16 v[54:57], v[230:233], v[198:201], v[54:57]
	v_mfma_f32_16x16x32_f16 v[146:149], v[230:233], v[214:217], v[146:149]
	s_setprio 0
	s_barrier
	ds_read_b128 v[154:157], v10
	ds_read_b128 v[158:161], v11
	ds_read_b128 v[162:165], v12
	ds_read_b128 v[166:169], v13
	s_mov_b32 m0, s20
	v_lshl_add_u64 v[226:227], v[18:19], 0, s[0:1]
	ds_read_b128 v[194:197], v1 offset:32768
	ds_read_b128 v[198:201], v1 offset:33792
	ds_read_b128 v[202:205], v1 offset:34816
	ds_read_b128 v[206:209], v1 offset:35840
	ds_read_b128 v[210:213], v1 offset:36864
	ds_read_b128 v[214:217], v1 offset:37888
	ds_read_b128 v[218:221], v1 offset:38912
	ds_read_b128 v[222:225], v1 offset:39936
	global_load_lds_dwordx4 v[226:227], off
	v_lshl_add_u64 v[226:227], v[20:21], 0, s[0:1]
	s_mov_b32 m0, s18
	s_nop 0
	global_load_lds_dwordx4 v[226:227], off
	s_waitcnt lgkmcnt(8)
	s_barrier
	s_waitcnt lgkmcnt(0)
	s_setprio 1
	s_waitcnt lgkmcnt(0)
	v_mfma_f32_16x16x32_f16 v[86:89], v[154:157], v[194:197], v[86:89]
	v_mfma_f32_16x16x32_f16 v[90:93], v[162:165], v[194:197], v[90:93]
	v_mfma_f32_16x16x32_f16 v[94:97], v[154:157], v[202:205], v[94:97]
	v_mfma_f32_16x16x32_f16 v[98:101], v[162:165], v[202:205], v[98:101]
	v_mfma_f32_16x16x32_f16 v[102:105], v[154:157], v[210:213], v[102:105]
	v_mfma_f32_16x16x32_f16 v[106:109], v[162:165], v[210:213], v[106:109]
	v_mfma_f32_16x16x32_f16 v[110:113], v[154:157], v[218:221], v[110:113]
	v_mfma_f32_16x16x32_f16 v[114:117], v[162:165], v[218:221], v[114:117]
	v_mfma_f32_16x16x32_f16 v[86:89], v[158:161], v[198:201], v[86:89]
	v_mfma_f32_16x16x32_f16 v[90:93], v[166:169], v[198:201], v[90:93]
	v_mfma_f32_16x16x32_f16 v[94:97], v[158:161], v[206:209], v[94:97]
	v_mfma_f32_16x16x32_f16 v[98:101], v[166:169], v[206:209], v[98:101]
	v_mfma_f32_16x16x32_f16 v[102:105], v[158:161], v[214:217], v[102:105]
	v_mfma_f32_16x16x32_f16 v[106:109], v[166:169], v[214:217], v[106:109]
	v_mfma_f32_16x16x32_f16 v[110:113], v[158:161], v[222:225], v[110:113]
	v_mfma_f32_16x16x32_f16 v[114:117], v[166:169], v[222:225], v[114:117]
	s_setprio 0
	s_barrier
	s_mov_b64 s[0:1], 0x280
	v_readfirstlane_b32 s10, v48
	v_lshl_add_u64 v[242:243], v[30:31], 0, s[0:1]
	s_mov_b32 m0, s10
	v_readfirstlane_b32 s2, v49
	ds_read_b128 v[226:229], v14
	ds_read_b128 v[230:233], v15
	ds_read_b128 v[234:237], v16
	ds_read_b128 v[238:241], v17
	global_load_lds_dwordx4 v[242:243], off
	v_lshl_add_u64 v[242:243], v[32:33], 0, s[0:1]
	s_mov_b32 m0, s2
	s_nop 0
	global_load_lds_dwordx4 v[242:243], off
	s_barrier
	s_waitcnt lgkmcnt(0)
	s_setprio 1
	s_waitcnt lgkmcnt(0)
	v_mfma_f32_16x16x32_f16 v[134:137], v[226:229], v[194:197], v[134:137]
	v_mfma_f32_16x16x32_f16 v[138:141], v[226:229], v[202:205], v[138:141]
	v_mfma_f32_16x16x32_f16 v[66:69], v[226:229], v[210:213], v[66:69]
	v_mfma_f32_16x16x32_f16 v[70:73], v[234:237], v[210:213], v[70:73]
	v_mfma_f32_16x16x32_f16 v[74:77], v[226:229], v[218:221], v[74:77]
	v_mfma_f32_16x16x32_f16 v[78:81], v[234:237], v[218:221], v[78:81]
	v_mfma_f32_16x16x32_f16 v[134:137], v[230:233], v[198:201], v[134:137]
	v_mfma_f32_16x16x32_f16 v[58:61], v[234:237], v[194:197], v[58:61]
	v_mfma_f32_16x16x32_f16 v[138:141], v[230:233], v[206:209], v[138:141]
	v_mfma_f32_16x16x32_f16 v[62:65], v[234:237], v[202:205], v[62:65]
	v_mfma_f32_16x16x32_f16 v[66:69], v[230:233], v[214:217], v[66:69]
	v_mfma_f32_16x16x32_f16 v[70:73], v[238:241], v[214:217], v[70:73]
	v_mfma_f32_16x16x32_f16 v[74:77], v[230:233], v[222:225], v[74:77]
	v_mfma_f32_16x16x32_f16 v[78:81], v[238:241], v[222:225], v[78:81]
	v_mfma_f32_16x16x32_f16 v[58:61], v[238:241], v[198:201], v[58:61]
	v_mfma_f32_16x16x32_f16 v[62:65], v[238:241], v[206:209], v[62:65]
	s_setprio 0
	v_readfirstlane_b32 s11, v46
	v_lshl_add_u64 v[48:49], v[26:27], 0, s[0:1]
	s_mov_b32 m0, s11
	v_readfirstlane_b32 s3, v47
	s_barrier
	ds_read_b128 v[194:197], v1 offset:49152
	ds_read_b128 v[198:201], v1 offset:50176
	ds_read_b128 v[202:205], v1 offset:51200
	ds_read_b128 v[206:209], v1 offset:52224
	ds_read_b128 v[210:213], v1 offset:53248
	ds_read_b128 v[214:217], v1 offset:54272
	ds_read_b128 v[218:221], v1 offset:55296
	ds_read_b128 v[222:225], v1 offset:56320
	global_load_lds_dwordx4 v[48:49], off
	v_lshl_add_u64 v[48:49], v[28:29], 0, s[0:1]
	s_mov_b32 m0, s3
	s_nop 0
	global_load_lds_dwordx4 v[48:49], off
	s_barrier
	s_waitcnt lgkmcnt(0)
	s_setprio 1
	s_waitcnt lgkmcnt(0)
	v_mfma_f32_16x16x32_f16 v[126:129], v[154:157], v[218:221], v[126:129]
	v_mfma_f32_16x16x32_f16 v[46:49], v[154:157], v[194:197], v[170:173]
	v_mfma_f32_16x16x32_f16 v[170:173], v[162:165], v[194:197], v[174:177]
	v_mfma_f32_16x16x32_f16 v[174:177], v[154:157], v[202:205], v[178:181]
	v_mfma_f32_16x16x32_f16 v[178:181], v[162:165], v[202:205], v[182:185]
	v_mfma_f32_16x16x32_f16 v[182:185], v[154:157], v[210:213], v[186:189]
	v_mfma_f32_16x16x32_f16 v[186:189], v[162:165], v[210:213], v[190:193]
	v_mfma_f32_16x16x32_f16 v[126:129], v[158:161], v[222:225], v[126:129]
	v_mfma_f32_16x16x32_f16 v[50:53], v[162:165], v[218:221], v[50:53]
	v_mfma_f32_16x16x32_f16 v[46:49], v[158:161], v[198:201], v[46:49]
	v_mfma_f32_16x16x32_f16 v[170:173], v[166:169], v[198:201], v[170:173]
	v_mfma_f32_16x16x32_f16 v[174:177], v[158:161], v[206:209], v[174:177]
	v_mfma_f32_16x16x32_f16 v[178:181], v[166:169], v[206:209], v[178:181]
	v_mfma_f32_16x16x32_f16 v[182:185], v[158:161], v[214:217], v[182:185]
	v_mfma_f32_16x16x32_f16 v[186:189], v[166:169], v[214:217], v[186:189]
	v_mfma_f32_16x16x32_f16 v[50:53], v[166:169], v[222:225], v[50:53]
	s_setprio 0
	s_barrier
	v_readfirstlane_b32 s5, v38
	v_lshl_add_u64 v[154:155], v[22:23], 0, s[0:1]
	s_mov_b32 m0, s5
	v_readfirstlane_b32 s4, v40
	global_load_lds_dwordx4 v[154:155], off
	v_lshl_add_u64 v[154:155], v[24:25], 0, s[0:1]
	s_mov_b32 m0, s4
	s_nop 0
	global_load_lds_dwordx4 v[154:155], off
	s_waitcnt vmcnt(6)
	s_barrier
	s_setprio 1
	v_mfma_f32_16x16x32_f16 v[82:85], v[234:237], v[194:197], v[82:85]
	v_mfma_f32_16x16x32_f16 v[130:133], v[226:229], v[202:205], v[130:133]
	v_mfma_f32_16x16x32_f16 v[142:145], v[234:237], v[202:205], v[142:145]
	v_mfma_f32_16x16x32_f16 v[150:153], v[234:237], v[210:213], v[150:153]
	v_mfma_f32_16x16x32_f16 v[118:121], v[226:229], v[218:221], v[118:121]
	v_mfma_f32_16x16x32_f16 v[122:125], v[234:237], v[218:221], v[122:125]
	v_mfma_f32_16x16x32_f16 v[54:57], v[226:229], v[194:197], v[54:57]
	v_mfma_f32_16x16x32_f16 v[82:85], v[238:241], v[198:201], v[82:85]
	v_mfma_f32_16x16x32_f16 v[130:133], v[230:233], v[206:209], v[130:133]
	v_mfma_f32_16x16x32_f16 v[142:145], v[238:241], v[206:209], v[142:145]
	v_mfma_f32_16x16x32_f16 v[146:149], v[226:229], v[210:213], v[146:149]
	v_mfma_f32_16x16x32_f16 v[150:153], v[238:241], v[214:217], v[150:153]
	v_mfma_f32_16x16x32_f16 v[118:121], v[230:233], v[222:225], v[118:121]
	v_mfma_f32_16x16x32_f16 v[122:125], v[238:241], v[222:225], v[122:125]
	v_mfma_f32_16x16x32_f16 v[54:57], v[230:233], v[198:201], v[54:57]
	v_mfma_f32_16x16x32_f16 v[146:149], v[230:233], v[214:217], v[146:149]
	s_setprio 0
	s_barrier
	ds_read_b128 v[154:157], v2
	ds_read_b128 v[158:161], v3
	ds_read_b128 v[162:165], v4
	ds_read_b128 v[166:169], v5
	v_readfirstlane_b32 s14, v37
	v_lshl_add_u64 v[190:191], v[18:19], 0, s[0:1]
	s_mov_b32 m0, s14
	v_readfirstlane_b32 s7, v39
	global_load_lds_dwordx4 v[190:191], off
	v_lshl_add_u64 v[190:191], v[20:21], 0, s[0:1]
	s_mov_b32 m0, s7
	s_nop 0
	global_load_lds_dwordx4 v[190:191], off
	ds_read_b128 v[190:193], v1
	ds_read_b128 v[194:197], v1 offset:1024
	ds_read_b128 v[198:201], v1 offset:2048
	ds_read_b128 v[202:205], v1 offset:3072
	ds_read_b128 v[206:209], v1 offset:4096
	ds_read_b128 v[210:213], v1 offset:5120
	ds_read_b128 v[214:217], v1 offset:6144
	ds_read_b128 v[218:221], v1 offset:7168
	s_waitcnt lgkmcnt(8)
	s_barrier
	s_waitcnt lgkmcnt(0)
	s_setprio 1
	s_waitcnt lgkmcnt(0)
	v_mfma_f32_16x16x32_f16 v[86:89], v[154:157], v[190:193], v[86:89]
	v_mfma_f32_16x16x32_f16 v[90:93], v[162:165], v[190:193], v[90:93]
	v_mfma_f32_16x16x32_f16 v[94:97], v[154:157], v[198:201], v[94:97]
	v_mfma_f32_16x16x32_f16 v[98:101], v[162:165], v[198:201], v[98:101]
	v_mfma_f32_16x16x32_f16 v[102:105], v[154:157], v[206:209], v[102:105]
	v_mfma_f32_16x16x32_f16 v[106:109], v[162:165], v[206:209], v[106:109]
	v_mfma_f32_16x16x32_f16 v[110:113], v[154:157], v[214:217], v[110:113]
	v_mfma_f32_16x16x32_f16 v[114:117], v[162:165], v[214:217], v[114:117]
	v_mfma_f32_16x16x32_f16 v[86:89], v[158:161], v[194:197], v[86:89]
	v_mfma_f32_16x16x32_f16 v[90:93], v[166:169], v[194:197], v[90:93]
	v_mfma_f32_16x16x32_f16 v[94:97], v[158:161], v[202:205], v[94:97]
	v_mfma_f32_16x16x32_f16 v[98:101], v[166:169], v[202:205], v[98:101]
	v_mfma_f32_16x16x32_f16 v[102:105], v[158:161], v[210:213], v[102:105]
	v_mfma_f32_16x16x32_f16 v[106:109], v[166:169], v[210:213], v[106:109]
	v_mfma_f32_16x16x32_f16 v[110:113], v[158:161], v[218:221], v[110:113]
	v_mfma_f32_16x16x32_f16 v[114:117], v[166:169], v[218:221], v[114:117]
	s_setprio 0
	s_barrier
	s_mov_b64 s[0:1], 0x300
	v_readfirstlane_b32 s15, v36
	v_lshl_add_u64 v[38:39], v[30:31], 0, s[0:1]
	s_mov_b32 m0, s15
	v_readfirstlane_b32 s15, v41
	ds_read_b128 v[222:225], v6
	ds_read_b128 v[226:229], v7
	ds_read_b128 v[230:233], v8
	ds_read_b128 v[234:237], v9
	global_load_lds_dwordx4 v[38:39], off
	v_lshl_add_u64 v[36:37], v[32:33], 0, s[0:1]
	s_mov_b32 m0, s15
	s_nop 0
	global_load_lds_dwordx4 v[36:37], off
	s_barrier
	s_waitcnt lgkmcnt(0)
	s_setprio 1
	s_waitcnt lgkmcnt(0)
	v_mfma_f32_16x16x32_f16 v[36:39], v[222:225], v[190:193], v[134:137]
	v_mfma_f32_16x16x32_f16 v[134:137], v[222:225], v[198:201], v[138:141]
	v_mfma_f32_16x16x32_f16 v[66:69], v[222:225], v[206:209], v[66:69]
	v_mfma_f32_16x16x32_f16 v[70:73], v[230:233], v[206:209], v[70:73]
	v_mfma_f32_16x16x32_f16 v[74:77], v[222:225], v[214:217], v[74:77]
	v_mfma_f32_16x16x32_f16 v[78:81], v[230:233], v[214:217], v[78:81]
	v_mfma_f32_16x16x32_f16 v[58:61], v[230:233], v[190:193], v[58:61]
	v_mfma_f32_16x16x32_f16 v[134:137], v[226:229], v[202:205], v[134:137]
	v_mfma_f32_16x16x32_f16 v[62:65], v[230:233], v[198:201], v[62:65]
	v_mfma_f32_16x16x32_f16 v[66:69], v[226:229], v[210:213], v[66:69]
	v_mfma_f32_16x16x32_f16 v[70:73], v[234:237], v[210:213], v[70:73]
	v_mfma_f32_16x16x32_f16 v[74:77], v[226:229], v[218:221], v[74:77]
	v_mfma_f32_16x16x32_f16 v[78:81], v[234:237], v[218:221], v[78:81]
	v_mfma_f32_16x16x32_f16 v[36:39], v[226:229], v[194:197], v[36:39]
	v_mfma_f32_16x16x32_f16 v[58:61], v[234:237], v[194:197], v[58:61]
	v_mfma_f32_16x16x32_f16 v[62:65], v[234:237], v[202:205], v[62:65]
	s_setprio 0
	v_readfirstlane_b32 s15, v35
	v_lshl_add_u64 v[40:41], v[26:27], 0, s[0:1]
	s_mov_b32 m0, s15
	v_readfirstlane_b32 s15, v42
	s_barrier
	ds_read_b128 v[138:141], v1 offset:16384
	ds_read_b128 v[190:193], v1 offset:17408
	ds_read_b128 v[194:197], v1 offset:18432
	ds_read_b128 v[198:201], v1 offset:19456
	ds_read_b128 v[202:205], v1 offset:20480
	ds_read_b128 v[206:209], v1 offset:21504
	ds_read_b128 v[210:213], v1 offset:22528
	ds_read_b128 v[214:217], v1 offset:23552
	global_load_lds_dwordx4 v[40:41], off
	v_lshl_add_u64 v[40:41], v[28:29], 0, s[0:1]
	s_mov_b32 m0, s15
	s_nop 0
	global_load_lds_dwordx4 v[40:41], off
	s_barrier
	s_waitcnt lgkmcnt(0)
	s_setprio 1
	s_waitcnt lgkmcnt(0)
	v_mfma_f32_16x16x32_f16 v[126:129], v[154:157], v[210:213], v[126:129]
	v_mfma_f32_16x16x32_f16 v[46:49], v[154:157], v[138:141], v[46:49]
	v_mfma_f32_16x16x32_f16 v[170:173], v[162:165], v[138:141], v[170:173]
	v_mfma_f32_16x16x32_f16 v[174:177], v[154:157], v[194:197], v[174:177]
	v_mfma_f32_16x16x32_f16 v[178:181], v[162:165], v[194:197], v[178:181]
	v_mfma_f32_16x16x32_f16 v[182:185], v[154:157], v[202:205], v[182:185]
	v_mfma_f32_16x16x32_f16 v[186:189], v[162:165], v[202:205], v[186:189]
	v_mfma_f32_16x16x32_f16 v[126:129], v[158:161], v[214:217], v[126:129]
	v_mfma_f32_16x16x32_f16 v[50:53], v[162:165], v[210:213], v[50:53]
	v_mfma_f32_16x16x32_f16 v[46:49], v[158:161], v[190:193], v[46:49]
	v_mfma_f32_16x16x32_f16 v[170:173], v[166:169], v[190:193], v[170:173]
	v_mfma_f32_16x16x32_f16 v[174:177], v[158:161], v[198:201], v[174:177]
	v_mfma_f32_16x16x32_f16 v[178:181], v[166:169], v[198:201], v[178:181]
	v_mfma_f32_16x16x32_f16 v[182:185], v[158:161], v[206:209], v[182:185]
	v_mfma_f32_16x16x32_f16 v[186:189], v[166:169], v[206:209], v[186:189]
	v_mfma_f32_16x16x32_f16 v[50:53], v[166:169], v[214:217], v[50:53]
	s_setprio 0
	s_barrier
	v_readfirstlane_b32 s15, v34
	v_lshl_add_u64 v[40:41], v[22:23], 0, s[0:1]
	s_mov_b32 m0, s15
	v_readfirstlane_b32 s15, v43
	global_load_lds_dwordx4 v[40:41], off
	v_lshl_add_u64 v[34:35], v[24:25], 0, s[0:1]
	s_mov_b32 m0, s15
	s_nop 0
	global_load_lds_dwordx4 v[34:35], off
	s_waitcnt vmcnt(6)
	s_barrier
	s_setprio 1
	v_mfma_f32_16x16x32_f16 v[40:43], v[222:225], v[138:141], v[54:57]
	v_mfma_f32_16x16x32_f16 v[54:57], v[230:233], v[138:141], v[82:85]
	v_mfma_f32_16x16x32_f16 v[82:85], v[222:225], v[194:197], v[130:133]
	v_mfma_f32_16x16x32_f16 v[130:133], v[230:233], v[194:197], v[142:145]
	v_mfma_f32_16x16x32_f16 v[138:141], v[222:225], v[202:205], v[146:149]
	v_mfma_f32_16x16x32_f16 v[142:145], v[230:233], v[202:205], v[150:153]
	v_mfma_f32_16x16x32_f16 v[118:121], v[222:225], v[210:213], v[118:121]
	v_mfma_f32_16x16x32_f16 v[122:125], v[230:233], v[210:213], v[122:125]
	v_mfma_f32_16x16x32_f16 v[82:85], v[226:229], v[198:201], v[82:85]
	v_mfma_f32_16x16x32_f16 v[130:133], v[234:237], v[198:201], v[130:133]
	v_mfma_f32_16x16x32_f16 v[138:141], v[226:229], v[206:209], v[138:141]
	v_mfma_f32_16x16x32_f16 v[142:145], v[234:237], v[206:209], v[142:145]
	v_mfma_f32_16x16x32_f16 v[118:121], v[226:229], v[214:217], v[118:121]
	v_mfma_f32_16x16x32_f16 v[122:125], v[234:237], v[214:217], v[122:125]
	v_mfma_f32_16x16x32_f16 v[40:43], v[226:229], v[190:193], v[40:43]
	v_mfma_f32_16x16x32_f16 v[54:57], v[234:237], v[190:193], v[54:57]
	s_setprio 0
	s_barrier
	ds_read_b128 v[146:149], v10
	ds_read_b128 v[150:153], v11
	ds_read_b128 v[154:157], v12
	ds_read_b128 v[158:161], v13
	v_readfirstlane_b32 s15, v44
	v_lshl_add_u64 v[34:35], v[18:19], 0, s[0:1]
	s_mov_b32 m0, s15
	ds_read_b128 v[162:165], v1 offset:32768
	ds_read_b128 v[166:169], v1 offset:33792
	ds_read_b128 v[190:193], v1 offset:34816
	ds_read_b128 v[194:197], v1 offset:35840
	ds_read_b128 v[198:201], v1 offset:36864
	ds_read_b128 v[202:205], v1 offset:37888
	ds_read_b128 v[206:209], v1 offset:38912
	ds_read_b128 v[210:213], v1 offset:39936
	global_load_lds_dwordx4 v[34:35], off
	v_lshl_add_u64 v[34:35], v[20:21], 0, s[0:1]
	v_readfirstlane_b32 s0, v45
	s_mov_b32 m0, s0
	s_nop 0
	global_load_lds_dwordx4 v[34:35], off
	s_waitcnt lgkmcnt(8)
	s_barrier
	s_waitcnt lgkmcnt(0)
	s_setprio 1
	s_waitcnt lgkmcnt(0)
	v_mfma_f32_16x16x32_f16 v[86:89], v[146:149], v[162:165], v[86:89]
	v_mfma_f32_16x16x32_f16 v[90:93], v[154:157], v[162:165], v[90:93]
	v_mfma_f32_16x16x32_f16 v[94:97], v[146:149], v[190:193], v[94:97]
	v_mfma_f32_16x16x32_f16 v[98:101], v[154:157], v[190:193], v[98:101]
	v_mfma_f32_16x16x32_f16 v[102:105], v[146:149], v[198:201], v[102:105]
	v_mfma_f32_16x16x32_f16 v[106:109], v[154:157], v[198:201], v[106:109]
	v_mfma_f32_16x16x32_f16 v[110:113], v[146:149], v[206:209], v[110:113]
	v_mfma_f32_16x16x32_f16 v[114:117], v[154:157], v[206:209], v[114:117]
	v_mfma_f32_16x16x32_f16 v[86:89], v[150:153], v[166:169], v[86:89]
	v_mfma_f32_16x16x32_f16 v[90:93], v[158:161], v[166:169], v[90:93]
	v_mfma_f32_16x16x32_f16 v[94:97], v[150:153], v[194:197], v[94:97]
	v_mfma_f32_16x16x32_f16 v[98:101], v[158:161], v[194:197], v[98:101]
	v_mfma_f32_16x16x32_f16 v[102:105], v[150:153], v[202:205], v[102:105]
	v_mfma_f32_16x16x32_f16 v[106:109], v[158:161], v[202:205], v[106:109]
	v_mfma_f32_16x16x32_f16 v[110:113], v[150:153], v[210:213], v[110:113]
	v_mfma_f32_16x16x32_f16 v[114:117], v[158:161], v[210:213], v[114:117]
	s_setprio 0
	s_barrier
	s_mov_b64 s[0:1], 0x380
	s_mov_b32 m0, s10
	v_lshl_add_u64 v[30:31], v[30:31], 0, s[0:1]
	ds_read_b128 v[214:217], v14
	ds_read_b128 v[218:221], v15
	ds_read_b128 v[222:225], v16
	ds_read_b128 v[226:229], v17
	global_load_lds_dwordx4 v[30:31], off
	v_lshl_add_u64 v[30:31], v[32:33], 0, s[0:1]
	s_mov_b32 m0, s2
	s_nop 0
	global_load_lds_dwordx4 v[30:31], off
	s_barrier
	s_waitcnt lgkmcnt(0)
	s_setprio 1
	s_waitcnt lgkmcnt(0)
	v_mfma_f32_16x16x32_f16 v[30:33], v[214:217], v[162:165], v[36:39]
	v_mfma_f32_16x16x32_f16 v[66:69], v[214:217], v[198:201], v[66:69]
	v_mfma_f32_16x16x32_f16 v[70:73], v[222:225], v[198:201], v[70:73]
	v_mfma_f32_16x16x32_f16 v[74:77], v[214:217], v[206:209], v[74:77]
	v_mfma_f32_16x16x32_f16 v[78:81], v[222:225], v[206:209], v[78:81]
	v_mfma_f32_16x16x32_f16 v[30:33], v[218:221], v[166:169], v[30:33]
	v_mfma_f32_16x16x32_f16 v[34:37], v[222:225], v[162:165], v[58:61]
	v_mfma_f32_16x16x32_f16 v[58:61], v[214:217], v[190:193], v[134:137]
	v_mfma_f32_16x16x32_f16 v[62:65], v[222:225], v[190:193], v[62:65]
	v_mfma_f32_16x16x32_f16 v[66:69], v[218:221], v[202:205], v[66:69]
	v_mfma_f32_16x16x32_f16 v[70:73], v[226:229], v[202:205], v[70:73]
	v_mfma_f32_16x16x32_f16 v[74:77], v[218:221], v[210:213], v[74:77]
	v_mfma_f32_16x16x32_f16 v[78:81], v[226:229], v[210:213], v[78:81]
	v_mfma_f32_16x16x32_f16 v[34:37], v[226:229], v[166:169], v[34:37]
	v_mfma_f32_16x16x32_f16 v[58:61], v[218:221], v[194:197], v[58:61]
	v_mfma_f32_16x16x32_f16 v[62:65], v[226:229], v[194:197], v[62:65]
	s_setprio 0
	s_mov_b32 m0, s11
	v_lshl_add_u64 v[26:27], v[26:27], 0, s[0:1]
	s_barrier
	ds_read_b128 v[134:137], v1 offset:49152
	ds_read_b128 v[162:165], v1 offset:50176
	ds_read_b128 v[166:169], v1 offset:51200
	ds_read_b128 v[190:193], v1 offset:52224
	ds_read_b128 v[194:197], v1 offset:53248
	ds_read_b128 v[198:201], v1 offset:54272
	ds_read_b128 v[202:205], v1 offset:55296
	ds_read_b128 v[206:209], v1 offset:56320
	global_load_lds_dwordx4 v[26:27], off
	v_lshl_add_u64 v[26:27], v[28:29], 0, s[0:1]
	s_mov_b32 m0, s3
	s_nop 0
	global_load_lds_dwordx4 v[26:27], off
	s_barrier
	s_waitcnt lgkmcnt(0)
	s_setprio 1
	s_waitcnt lgkmcnt(0)
	v_mfma_f32_16x16x32_f16 v[26:29], v[146:149], v[134:137], v[46:49]
	v_mfma_f32_16x16x32_f16 v[126:129], v[146:149], v[202:205], v[126:129]
	v_mfma_f32_16x16x32_f16 v[26:29], v[150:153], v[162:165], v[26:29]
	v_mfma_f32_16x16x32_f16 v[44:47], v[154:157], v[134:137], v[170:173]
	v_mfma_f32_16x16x32_f16 v[170:173], v[146:149], v[166:169], v[174:177]
	v_mfma_f32_16x16x32_f16 v[174:177], v[154:157], v[166:169], v[178:181]
	v_mfma_f32_16x16x32_f16 v[178:181], v[146:149], v[194:197], v[182:185]
	v_mfma_f32_16x16x32_f16 v[182:185], v[154:157], v[194:197], v[186:189]
	v_mfma_f32_16x16x32_f16 v[126:129], v[150:153], v[206:209], v[126:129]
	v_mfma_f32_16x16x32_f16 v[48:51], v[154:157], v[202:205], v[50:53]
	v_mfma_f32_16x16x32_f16 v[44:47], v[158:161], v[162:165], v[44:47]
	v_mfma_f32_16x16x32_f16 v[170:173], v[150:153], v[190:193], v[170:173]
	v_mfma_f32_16x16x32_f16 v[174:177], v[158:161], v[190:193], v[174:177]
	v_mfma_f32_16x16x32_f16 v[178:181], v[150:153], v[198:201], v[178:181]
	v_mfma_f32_16x16x32_f16 v[182:185], v[158:161], v[198:201], v[182:185]
	v_mfma_f32_16x16x32_f16 v[48:51], v[158:161], v[206:209], v[48:51]
	s_setprio 0
	s_barrier
	s_mov_b32 m0, s5
	v_lshl_add_u64 v[22:23], v[22:23], 0, s[0:1]
	global_load_lds_dwordx4 v[22:23], off
	v_lshl_add_u64 v[22:23], v[24:25], 0, s[0:1]
	s_mov_b32 m0, s4
	s_nop 0
	global_load_lds_dwordx4 v[22:23], off
	s_waitcnt vmcnt(6)
	s_barrier
	s_setprio 1
	v_mfma_f32_16x16x32_f16 v[22:25], v[214:217], v[134:137], v[40:43]
	v_mfma_f32_16x16x32_f16 v[38:41], v[222:225], v[134:137], v[54:57]
	v_mfma_f32_16x16x32_f16 v[52:55], v[214:217], v[166:169], v[82:85]
	v_mfma_f32_16x16x32_f16 v[82:85], v[222:225], v[166:169], v[130:133]
	v_mfma_f32_16x16x32_f16 v[130:133], v[214:217], v[194:197], v[138:141]
	v_mfma_f32_16x16x32_f16 v[134:137], v[222:225], v[194:197], v[142:145]
	v_mfma_f32_16x16x32_f16 v[118:121], v[214:217], v[202:205], v[118:121]
	v_mfma_f32_16x16x32_f16 v[122:125], v[222:225], v[202:205], v[122:125]
	v_mfma_f32_16x16x32_f16 v[22:25], v[218:221], v[162:165], v[22:25]
	v_mfma_f32_16x16x32_f16 v[82:85], v[226:229], v[190:193], v[82:85]
	v_mfma_f32_16x16x32_f16 v[130:133], v[218:221], v[198:201], v[130:133]
	v_mfma_f32_16x16x32_f16 v[134:137], v[226:229], v[198:201], v[134:137]
	v_mfma_f32_16x16x32_f16 v[118:121], v[218:221], v[206:209], v[118:121]
	v_mfma_f32_16x16x32_f16 v[122:125], v[226:229], v[206:209], v[122:125]
	v_mfma_f32_16x16x32_f16 v[38:41], v[226:229], v[162:165], v[38:41]
	v_mfma_f32_16x16x32_f16 v[52:55], v[218:221], v[190:193], v[52:55]
	s_setprio 0
	s_mov_b32 m0, s14
	v_lshl_add_u64 v[18:19], v[18:19], 0, s[0:1]
	s_barrier
	ds_read_b128 v[138:141], v2
	ds_read_b128 v[142:145], v3
	ds_read_b128 v[146:149], v4
	ds_read_b128 v[2:5], v5
	global_load_lds_dwordx4 v[18:19], off
	v_lshl_add_u64 v[18:19], v[20:21], 0, s[0:1]
	s_mov_b32 m0, s7
	s_nop 0
	global_load_lds_dwordx4 v[18:19], off
	ds_read_b128 v[18:21], v1
	ds_read_b128 v[150:153], v1 offset:1024
	ds_read_b128 v[154:157], v1 offset:2048
	ds_read_b128 v[158:161], v1 offset:3072
	ds_read_b128 v[162:165], v1 offset:4096
	ds_read_b128 v[166:169], v1 offset:5120
	ds_read_b128 v[186:189], v1 offset:6144
	ds_read_b128 v[190:193], v1 offset:7168
	s_barrier
	s_waitcnt lgkmcnt(0)
	s_setprio 1
	s_waitcnt lgkmcnt(0)
	v_mfma_f32_16x16x32_f16 v[86:89], v[138:141], v[18:21], v[86:89]
	v_mfma_f32_16x16x32_f16 v[90:93], v[146:149], v[18:21], v[90:93]
	v_mfma_f32_16x16x32_f16 v[94:97], v[138:141], v[154:157], v[94:97]
	v_mfma_f32_16x16x32_f16 v[98:101], v[146:149], v[154:157], v[98:101]
	v_mfma_f32_16x16x32_f16 v[102:105], v[138:141], v[162:165], v[102:105]
	v_mfma_f32_16x16x32_f16 v[106:109], v[146:149], v[162:165], v[106:109]
	v_mfma_f32_16x16x32_f16 v[110:113], v[138:141], v[186:189], v[110:113]
	v_mfma_f32_16x16x32_f16 v[86:89], v[142:145], v[150:153], v[86:89]
	v_mfma_f32_16x16x32_f16 v[90:93], v[2:5], v[150:153], v[90:93]
	v_mfma_f32_16x16x32_f16 v[94:97], v[142:145], v[158:161], v[94:97]
	v_mfma_f32_16x16x32_f16 v[98:101], v[2:5], v[158:161], v[98:101]
	v_mfma_f32_16x16x32_f16 v[102:105], v[142:145], v[166:169], v[102:105]
	v_mfma_f32_16x16x32_f16 v[106:109], v[2:5], v[166:169], v[106:109]
	v_mfma_f32_16x16x32_f16 v[110:113], v[142:145], v[190:193], v[110:113]
	v_mfma_f32_16x16x32_f16 v[114:117], v[146:149], v[186:189], v[114:117]
	v_mfma_f32_16x16x32_f16 v[194:197], v[2:5], v[190:193], v[114:117]
	s_setprio 0
	s_barrier
	s_nop 4
	ds_read_b128 v[114:117], v6
	ds_read_b128 v[198:201], v7
	ds_read_b128 v[202:205], v8
	ds_read_b128 v[6:9], v9
	s_barrier
	s_waitcnt lgkmcnt(0)
	s_setprio 1
	s_waitcnt lgkmcnt(0)
	v_mfma_f32_16x16x32_f16 v[30:33], v[114:117], v[18:21], v[30:33]
	v_mfma_f32_16x16x32_f16 v[18:21], v[202:205], v[18:21], v[34:37]
	v_mfma_f32_16x16x32_f16 v[34:37], v[114:117], v[154:157], v[58:61]
	v_mfma_f32_16x16x32_f16 v[56:59], v[202:205], v[154:157], v[62:65]
	v_mfma_f32_16x16x32_f16 v[60:63], v[114:117], v[162:165], v[66:69]
	v_mfma_f32_16x16x32_f16 v[64:67], v[202:205], v[162:165], v[70:73]
	v_mfma_f32_16x16x32_f16 v[68:71], v[114:117], v[186:189], v[74:77]
	v_mfma_f32_16x16x32_f16 v[72:75], v[202:205], v[186:189], v[78:81]
	v_mfma_f32_16x16x32_f16 v[30:33], v[198:201], v[150:153], v[30:33]
	v_mfma_f32_16x16x32_f16 v[18:21], v[6:9], v[150:153], v[18:21]
	v_mfma_f32_16x16x32_f16 v[64:67], v[6:9], v[166:169], v[64:67]
	v_mfma_f32_16x16x32_f16 v[68:71], v[198:201], v[190:193], v[68:71]
	v_mfma_f32_16x16x32_f16 v[72:75], v[6:9], v[190:193], v[72:75]
	v_mfma_f32_16x16x32_f16 v[34:37], v[198:201], v[158:161], v[34:37]
	v_mfma_f32_16x16x32_f16 v[56:59], v[6:9], v[158:161], v[56:59]
	v_mfma_f32_16x16x32_f16 v[60:63], v[198:201], v[166:169], v[60:63]
	s_setprio 0
	s_barrier
	ds_read_b128 v[76:79], v1 offset:16384
	ds_read_b128 v[150:153], v1 offset:17408
	ds_read_b128 v[154:157], v1 offset:18432
	ds_read_b128 v[158:161], v1 offset:19456
	ds_read_b128 v[162:165], v1 offset:20480
	ds_read_b128 v[166:169], v1 offset:21504
	ds_read_b128 v[186:189], v1 offset:22528
	ds_read_b128 v[190:193], v1 offset:23552
	s_waitcnt vmcnt(4)
	s_barrier
	s_waitcnt lgkmcnt(0)
	s_setprio 1
	s_waitcnt lgkmcnt(0)
	v_mfma_f32_16x16x32_f16 v[26:29], v[138:141], v[76:79], v[26:29]
	v_mfma_f32_16x16x32_f16 v[42:45], v[146:149], v[76:79], v[44:47]
	v_mfma_f32_16x16x32_f16 v[174:177], v[146:149], v[154:157], v[174:177]
	v_mfma_f32_16x16x32_f16 v[182:185], v[146:149], v[162:165], v[182:185]
	v_mfma_f32_16x16x32_f16 v[46:49], v[146:149], v[186:189], v[48:51]
	v_mfma_f32_16x16x32_f16 v[26:29], v[142:145], v[150:153], v[26:29]
	v_mfma_f32_16x16x32_f16 v[42:45], v[2:5], v[150:153], v[42:45]
	v_mfma_f32_16x16x32_f16 v[170:173], v[138:141], v[154:157], v[170:173]
	v_mfma_f32_16x16x32_f16 v[174:177], v[2:5], v[158:161], v[174:177]
	v_mfma_f32_16x16x32_f16 v[178:181], v[138:141], v[162:165], v[178:181]
	v_mfma_f32_16x16x32_f16 v[182:185], v[2:5], v[166:169], v[182:185]
	v_mfma_f32_16x16x32_f16 v[126:129], v[138:141], v[186:189], v[126:129]
	v_mfma_f32_16x16x32_f16 v[2:5], v[2:5], v[190:193], v[46:49]
	v_mfma_f32_16x16x32_f16 v[170:173], v[142:145], v[158:161], v[170:173]
	v_mfma_f32_16x16x32_f16 v[178:181], v[142:145], v[166:169], v[178:181]
	v_mfma_f32_16x16x32_f16 v[206:209], v[142:145], v[190:193], v[126:129]
	s_setprio 0
	s_setprio 1
	v_mfma_f32_16x16x32_f16 v[22:25], v[114:117], v[76:79], v[22:25]
	v_mfma_f32_16x16x32_f16 v[46:49], v[198:201], v[150:153], v[22:25]
	v_mfma_f32_16x16x32_f16 v[22:25], v[202:205], v[76:79], v[38:41]
	v_mfma_f32_16x16x32_f16 v[38:41], v[6:9], v[150:153], v[22:25]
	v_mfma_f32_16x16x32_f16 v[22:25], v[114:117], v[154:157], v[52:55]
	v_mfma_f32_16x16x32_f16 v[50:53], v[198:201], v[158:161], v[22:25]
	v_mfma_f32_16x16x32_f16 v[22:25], v[202:205], v[154:157], v[82:85]
	v_mfma_f32_16x16x32_f16 v[146:149], v[6:9], v[158:161], v[22:25]
	v_mfma_f32_16x16x32_f16 v[22:25], v[114:117], v[162:165], v[130:133]
	v_mfma_f32_16x16x32_f16 v[210:213], v[198:201], v[166:169], v[22:25]
	v_mfma_f32_16x16x32_f16 v[22:25], v[202:205], v[162:165], v[134:137]
	v_mfma_f32_16x16x32_f16 v[166:169], v[6:9], v[166:169], v[22:25]
	v_mfma_f32_16x16x32_f16 v[22:25], v[114:117], v[186:189], v[118:121]
	v_mfma_f32_16x16x32_f16 v[198:201], v[198:201], v[190:193], v[22:25]
	v_mfma_f32_16x16x32_f16 v[22:25], v[202:205], v[186:189], v[122:125]
	v_mfma_f32_16x16x32_f16 v[186:189], v[6:9], v[190:193], v[22:25]
	s_setprio 0
	s_barrier
	ds_read_b128 v[6:9], v10
	ds_read_b128 v[76:79], v11
	ds_read_b128 v[190:193], v12
	ds_read_b128 v[10:13], v13
	s_nop 0
	ds_read_b128 v[22:25], v1 offset:32768
	ds_read_b128 v[122:125], v1 offset:33792
	ds_read_b128 v[126:129], v1 offset:34816
	ds_read_b128 v[138:141], v1 offset:35840
	ds_read_b128 v[202:205], v1 offset:36864
	ds_read_b128 v[214:217], v1 offset:37888
	ds_read_b128 v[218:221], v1 offset:38912
	ds_read_b128 v[222:225], v1 offset:39936
	s_waitcnt vmcnt(2)
	s_barrier
	s_waitcnt lgkmcnt(0)
	s_setprio 1
	s_waitcnt lgkmcnt(0)
	v_mfma_f32_16x16x32_f16 v[80:83], v[6:9], v[22:25], v[86:89]
	v_mfma_f32_16x16x32_f16 v[162:165], v[76:79], v[122:125], v[80:83]
	v_mfma_f32_16x16x32_f16 v[80:83], v[190:193], v[22:25], v[90:93]
	v_mfma_f32_16x16x32_f16 v[154:157], v[10:13], v[122:125], v[80:83]
	v_mfma_f32_16x16x32_f16 v[80:83], v[6:9], v[126:129], v[94:97]
	v_mfma_f32_16x16x32_f16 v[134:137], v[76:79], v[138:141], v[80:83]
	v_mfma_f32_16x16x32_f16 v[80:83], v[190:193], v[126:129], v[98:101]
	v_mfma_f32_16x16x32_f16 v[130:133], v[10:13], v[138:141], v[80:83]
	v_mfma_f32_16x16x32_f16 v[80:83], v[6:9], v[202:205], v[102:105]
	v_mfma_f32_16x16x32_f16 v[118:121], v[76:79], v[214:217], v[80:83]
	v_mfma_f32_16x16x32_f16 v[80:83], v[190:193], v[202:205], v[106:109]
	v_mfma_f32_16x16x32_f16 v[114:117], v[10:13], v[214:217], v[80:83]
	v_mfma_f32_16x16x32_f16 v[80:83], v[6:9], v[218:221], v[110:113]
	v_mfma_f32_16x16x32_f16 v[86:89], v[76:79], v[222:225], v[80:83]
	v_mfma_f32_16x16x32_f16 v[80:83], v[190:193], v[218:221], v[194:197]
	v_mfma_f32_16x16x32_f16 v[82:85], v[10:13], v[222:225], v[80:83]
	s_setprio 0
	s_barrier
	ds_read_b128 v[194:197], v14
	ds_read_b128 v[226:229], v15
	ds_read_b128 v[230:233], v16
	ds_read_b128 v[234:237], v17
	s_waitcnt vmcnt(0)
	s_barrier
	s_waitcnt lgkmcnt(0)
	s_setprio 1
	s_waitcnt lgkmcnt(0)
	v_mfma_f32_16x16x32_f16 v[14:17], v[194:197], v[22:25], v[30:33]
	v_mfma_f32_16x16x32_f16 v[158:161], v[226:229], v[122:125], v[14:17]
	v_mfma_f32_16x16x32_f16 v[14:17], v[230:233], v[22:25], v[18:21]
	v_mfma_f32_16x16x32_f16 v[150:153], v[234:237], v[122:125], v[14:17]
	v_mfma_f32_16x16x32_f16 v[14:17], v[194:197], v[126:129], v[34:37]
	v_mfma_f32_16x16x32_f16 v[142:145], v[226:229], v[138:141], v[14:17]
	v_mfma_f32_16x16x32_f16 v[14:17], v[230:233], v[126:129], v[56:59]
	v_mfma_f32_16x16x32_f16 v[138:141], v[234:237], v[138:141], v[14:17]
	v_mfma_f32_16x16x32_f16 v[14:17], v[194:197], v[202:205], v[60:63]
	v_mfma_f32_16x16x32_f16 v[126:129], v[226:229], v[214:217], v[14:17]
	v_mfma_f32_16x16x32_f16 v[14:17], v[230:233], v[202:205], v[64:67]
	v_mfma_f32_16x16x32_f16 v[122:125], v[234:237], v[214:217], v[14:17]
	v_mfma_f32_16x16x32_f16 v[14:17], v[194:197], v[218:221], v[68:71]
	v_mfma_f32_16x16x32_f16 v[98:101], v[226:229], v[222:225], v[14:17]
	v_mfma_f32_16x16x32_f16 v[14:17], v[230:233], v[218:221], v[72:75]
	v_mfma_f32_16x16x32_f16 v[90:93], v[234:237], v[222:225], v[14:17]
	s_setprio 0
	s_barrier
	ds_read_b128 v[30:33], v1 offset:49152
	ds_read_b128 v[34:37], v1 offset:50176
	ds_read_b128 v[54:57], v1 offset:51200
	ds_read_b128 v[58:61], v1 offset:52224
	ds_read_b128 v[62:65], v1 offset:53248
	ds_read_b128 v[202:205], v1 offset:54272
	ds_read_b128 v[214:217], v1 offset:55296
	ds_read_b128 v[218:221], v1 offset:56320
	s_barrier
	s_waitcnt lgkmcnt(0)
	s_setprio 1
	s_waitcnt lgkmcnt(0)
	v_mfma_f32_16x16x32_f16 v[14:17], v[6:9], v[30:33], v[26:29]
	v_mfma_f32_16x16x32_f16 v[102:105], v[76:79], v[34:37], v[14:17]
	v_mfma_f32_16x16x32_f16 v[14:17], v[190:193], v[30:33], v[42:45]
	v_mfma_f32_16x16x32_f16 v[94:97], v[10:13], v[34:37], v[14:17]
	v_mfma_f32_16x16x32_f16 v[14:17], v[6:9], v[54:57], v[170:173]
	v_mfma_f32_16x16x32_f16 v[70:73], v[76:79], v[58:61], v[14:17]
	v_mfma_f32_16x16x32_f16 v[14:17], v[190:193], v[54:57], v[174:177]
	v_mfma_f32_16x16x32_f16 v[66:69], v[10:13], v[58:61], v[14:17]
	v_mfma_f32_16x16x32_f16 v[14:17], v[6:9], v[62:65], v[178:181]
	v_mfma_f32_16x16x32_f16 v[22:25], v[76:79], v[202:205], v[14:17]
	v_mfma_f32_16x16x32_f16 v[14:17], v[190:193], v[62:65], v[182:185]
	v_mfma_f32_16x16x32_f16 v[6:9], v[6:9], v[214:217], v[206:209]
	v_mfma_f32_16x16x32_f16 v[2:5], v[190:193], v[214:217], v[2:5]
	v_mfma_f32_16x16x32_f16 v[18:21], v[10:13], v[202:205], v[14:17]
	v_mfma_f32_16x16x32_f16 v[14:17], v[76:79], v[218:221], v[6:9]
	v_mfma_f32_16x16x32_f16 v[6:9], v[10:13], v[218:221], v[2:5]
	s_setprio 0
	s_setprio 1
	v_mfma_f32_16x16x32_f16 v[2:5], v[194:197], v[30:33], v[46:49]
	v_mfma_f32_16x16x32_f16 v[110:113], v[226:229], v[34:37], v[2:5]
	v_mfma_f32_16x16x32_f16 v[2:5], v[230:233], v[30:33], v[38:41]
	v_mfma_f32_16x16x32_f16 v[106:109], v[234:237], v[34:37], v[2:5]
	v_mfma_f32_16x16x32_f16 v[2:5], v[194:197], v[54:57], v[50:53]
	v_mfma_f32_16x16x32_f16 v[78:81], v[226:229], v[58:61], v[2:5]
	v_mfma_f32_16x16x32_f16 v[2:5], v[230:233], v[54:57], v[146:149]
	v_mfma_f32_16x16x32_f16 v[74:77], v[234:237], v[58:61], v[2:5]
	v_mfma_f32_16x16x32_f16 v[2:5], v[194:197], v[62:65], v[210:213]
	v_mfma_f32_16x16x32_f16 v[30:33], v[226:229], v[202:205], v[2:5]
	v_mfma_f32_16x16x32_f16 v[2:5], v[230:233], v[62:65], v[166:169]
	v_mfma_f32_16x16x32_f16 v[26:29], v[234:237], v[202:205], v[2:5]
	v_mfma_f32_16x16x32_f16 v[2:5], v[194:197], v[214:217], v[198:201]
	v_mfma_f32_16x16x32_f16 v[10:13], v[226:229], v[218:221], v[2:5]
	v_mfma_f32_16x16x32_f16 v[2:5], v[230:233], v[214:217], v[186:189]
	v_mfma_f32_16x16x32_f16 v[2:5], v[234:237], v[218:221], v[2:5]
	s_setprio 0
	s_barrier
	s_add_i32 s0, 0, 0x20800
	v_bfe_u32 v166, v0, 4, 2
	v_bfe_u32 v1, v0, 6, 2
	v_lshlrev_b32_e32 v34, 5, v166
	v_lshl_or_b32 v34, v1, 7, v34
	v_add_u32_e32 v35, s0, v34
	s_add_i32 s1, 0, 0x20c00
	v_add_u32_e32 v36, s1, v34
	ds_read_b128 v[58:61], v35
	ds_read_b128 v[62:65], v36
	v_or_b32_e32 v35, 16, v34
	v_add_u32_e32 v36, s0, v35
	v_add_u32_e32 v35, s1, v35
	ds_read_b128 v[50:53], v36
	ds_read_b128 v[54:57], v35
	v_or_b32_e32 v35, 0x200, v34
	v_add_u32_e32 v36, s0, v35
	v_add_u32_e32 v35, s1, v35
	v_or_b32_e32 v34, 0x210, v34
	ds_read_b128 v[42:45], v36
	ds_read_b128 v[46:49], v35
	v_add_u32_e32 v35, s0, v34
	v_and_b32_e32 v146, 15, v0
	v_ashrrev_i32_e32 v0, 2, v0
	s_movk_i32 s0, 0xffc0
	v_and_or_b32 v168, v0, s0, v146
	s_add_i32 s0, 0, 0x20000
	v_add_u32_e32 v38, s1, v34
	v_lshl_add_u32 v169, v168, 3, s0
	ds_read_b128 v[34:37], v35
	ds_read_b128 v[38:41], v38
	s_waitcnt vmcnt(0)
	ds_read2st64_b64 v[146:149], v169 offset1:2
	v_lshlrev_b32_e32 v0, 5, v1
	v_lshlrev_b32_e32 v1, 3, v166
	v_or3_b32 v166, v0, v1, s13
	v_add_u32_e32 v167, s12, v168
	s_waitcnt lgkmcnt(0)
	v_pk_fma_f32 v[0:1], v[146:147], v[58:59], v[162:163] op_sel_hi:[0,1,1] neg_lo:[1,0,0] neg_hi:[1,0,0]
	v_pk_fma_f32 v[0:1], v[146:147], v[0:1], v[62:63] op_sel:[1,0,0]
	v_mul_lo_u32 v170, v167, s6
	v_cvt_pk_f16_f32 v162, v0, v1
	v_pk_fma_f32 v[0:1], v[146:147], v[60:61], v[164:165] op_sel_hi:[0,1,1] neg_lo:[1,0,0] neg_hi:[1,0,0]
	v_pk_fma_f32 v[0:1], v[146:147], v[0:1], v[64:65] op_sel:[1,0,0]
	s_and_b32 s9, s9, 0xffff
	v_cvt_pk_f16_f32 v163, v0, v1
	v_pk_fma_f32 v[0:1], v[146:147], v[50:51], v[154:155] op_sel_hi:[0,1,1] neg_lo:[1,0,0] neg_hi:[1,0,0]
	v_pk_fma_f32 v[0:1], v[146:147], v[0:1], v[54:55] op_sel:[1,0,0]
	s_mov_b32 s11, 0x20000
	v_cvt_pk_f16_f32 v164, v0, v1
	v_pk_fma_f32 v[0:1], v[146:147], v[52:53], v[156:157] op_sel_hi:[0,1,1] neg_lo:[1,0,0] neg_hi:[1,0,0]
	v_pk_fma_f32 v[0:1], v[146:147], v[0:1], v[56:57] op_sel:[1,0,0]
	s_mov_b32 s10, 0x7ffffff0
	v_cvt_pk_f16_f32 v165, v0, v1
	v_pk_fma_f32 v[0:1], v[146:147], v[42:43], v[158:159] op_sel_hi:[0,1,1] neg_lo:[1,0,0] neg_hi:[1,0,0]
	v_pk_fma_f32 v[0:1], v[146:147], v[0:1], v[46:47] op_sel:[1,0,0]
	v_add_lshl_u32 v170, v166, v170, 1
	v_cvt_pk_f16_f32 v154, v0, v1
	v_pk_fma_f32 v[0:1], v[146:147], v[44:45], v[160:161] op_sel_hi:[0,1,1] neg_lo:[1,0,0] neg_hi:[1,0,0]
	v_pk_fma_f32 v[0:1], v[146:147], v[0:1], v[48:49] op_sel:[1,0,0]
	buffer_store_dwordx4 v[162:165], v170, s[8:11], 0 offen sc1
	s_and_saveexec_b64 s[44:45], vcc
	s_cbranch_execz .LBB6_34
	s_barrier
.LBB6_34:
	s_or_b64 exec, exec, s[44:45]
	v_cvt_pk_f16_f32 v155, v0, v1
	v_pk_fma_f32 v[0:1], v[146:147], v[34:35], v[150:151] op_sel_hi:[0,1,1] neg_lo:[1,0,0] neg_hi:[1,0,0]
	v_pk_fma_f32 v[0:1], v[146:147], v[0:1], v[38:39] op_sel:[1,0,0]
	s_nop 0
	v_cvt_pk_f16_f32 v156, v0, v1
	v_pk_fma_f32 v[0:1], v[146:147], v[36:37], v[152:153] op_sel_hi:[0,1,1] neg_lo:[1,0,0] neg_hi:[1,0,0]
	v_pk_fma_f32 v[0:1], v[146:147], v[0:1], v[40:41] op_sel:[1,0,0]
	s_nop 0
	v_cvt_pk_f16_f32 v157, v0, v1
	v_or_b32_e32 v0, 16, v168
	v_add_u32_e32 v146, s12, v0
	v_lshl_add_u32 v0, v0, 3, s0
	ds_read_b64 v[0:1], v0
	buffer_store_dwordx4 v[154:157], v170, s[8:11], 0 offen offset:256 sc1
	s_waitcnt lgkmcnt(0)
	v_pk_fma_f32 v[134:135], v[0:1], v[58:59], v[134:135] op_sel_hi:[0,1,1] neg_lo:[1,0,0] neg_hi:[1,0,0]
	v_pk_fma_f32 v[136:137], v[0:1], v[60:61], v[136:137] op_sel_hi:[0,1,1] neg_lo:[1,0,0] neg_hi:[1,0,0]
	v_pk_fma_f32 v[130:131], v[0:1], v[50:51], v[130:131] op_sel_hi:[0,1,1] neg_lo:[1,0,0] neg_hi:[1,0,0]
	v_pk_fma_f32 v[134:135], v[0:1], v[134:135], v[62:63] op_sel:[1,0,0]
	v_pk_fma_f32 v[136:137], v[0:1], v[136:137], v[64:65] op_sel:[1,0,0]
	v_pk_fma_f32 v[130:131], v[0:1], v[130:131], v[54:55] op_sel:[1,0,0]
	v_cvt_pk_f16_f32 v134, v134, v135
	v_cvt_pk_f16_f32 v135, v136, v137
	v_cvt_pk_f16_f32 v136, v130, v131
	v_pk_fma_f32 v[130:131], v[0:1], v[52:53], v[132:133] op_sel_hi:[0,1,1] neg_lo:[1,0,0] neg_hi:[1,0,0]
	v_pk_fma_f32 v[130:131], v[0:1], v[130:131], v[56:57] op_sel:[1,0,0]
	v_mul_lo_u32 v154, v146, s6
	v_or_b32_e32 v155, 32, v168
	v_or_b32_e32 v156, 48, v168
	v_cvt_pk_f16_f32 v137, v130, v131
	v_pk_fma_f32 v[130:131], v[0:1], v[42:43], v[142:143] op_sel_hi:[0,1,1] neg_lo:[1,0,0] neg_hi:[1,0,0]
	v_pk_fma_f32 v[132:133], v[0:1], v[44:45], v[144:145] op_sel_hi:[0,1,1] neg_lo:[1,0,0] neg_hi:[1,0,0]
	v_lshl_add_u32 v146, v155, 3, s0
	v_lshl_add_u32 v147, v156, 3, s0
	v_add_lshl_u32 v154, v166, v154, 1
	v_pk_fma_f32 v[130:131], v[0:1], v[130:131], v[46:47] op_sel:[1,0,0]
	v_pk_fma_f32 v[132:133], v[0:1], v[132:133], v[48:49] op_sel:[1,0,0]
	ds_read_b64 v[150:151], v146
	ds_read_b64 v[146:147], v147
	ds_read_b64 v[152:153], v169 offset:1408
	buffer_store_dwordx4 v[134:137], v154, s[8:11], 0 offen sc1
	v_cvt_pk_f16_f32 v130, v130, v131
	v_cvt_pk_f16_f32 v131, v132, v133
	v_pk_fma_f32 v[132:133], v[0:1], v[34:35], v[138:139] op_sel_hi:[0,1,1] neg_lo:[1,0,0] neg_hi:[1,0,0]
	v_pk_fma_f32 v[134:135], v[0:1], v[36:37], v[140:141] op_sel_hi:[0,1,1] neg_lo:[1,0,0] neg_hi:[1,0,0]
	v_pk_fma_f32 v[132:133], v[0:1], v[132:133], v[38:39] op_sel:[1,0,0]
	v_pk_fma_f32 v[0:1], v[0:1], v[134:135], v[40:41] op_sel:[1,0,0]
	v_cvt_pk_f16_f32 v132, v132, v133
	v_cvt_pk_f16_f32 v133, v0, v1
	v_add_u32_e32 v0, s12, v155
	buffer_store_dwordx4 v[130:133], v154, s[8:11], 0 offen offset:256 sc1
	s_waitcnt lgkmcnt(0)
	v_pk_fma_f32 v[2:3], v[152:153], v[34:35], v[2:3] op_sel_hi:[0,1,1] neg_lo:[1,0,0] neg_hi:[1,0,0]
	v_pk_fma_f32 v[4:5], v[152:153], v[36:37], v[4:5] op_sel_hi:[0,1,1] neg_lo:[1,0,0] neg_hi:[1,0,0]
	v_mul_lo_u32 v130, v0, s6
	v_pk_fma_f32 v[0:1], v[150:151], v[58:59], v[118:119] op_sel_hi:[0,1,1] neg_lo:[1,0,0] neg_hi:[1,0,0]
	v_pk_fma_f32 v[0:1], v[150:151], v[0:1], v[62:63] op_sel:[1,0,0]
	v_add_lshl_u32 v130, v166, v130, 1
	v_cvt_pk_f16_f32 v118, v0, v1
	v_pk_fma_f32 v[0:1], v[150:151], v[60:61], v[120:121] op_sel_hi:[0,1,1] neg_lo:[1,0,0] neg_hi:[1,0,0]
	v_pk_fma_f32 v[0:1], v[150:151], v[0:1], v[64:65] op_sel:[1,0,0]
	v_pk_fma_f32 v[2:3], v[152:153], v[2:3], v[38:39] op_sel:[1,0,0]
	v_cvt_pk_f16_f32 v119, v0, v1
	v_pk_fma_f32 v[0:1], v[150:151], v[50:51], v[114:115] op_sel_hi:[0,1,1] neg_lo:[1,0,0] neg_hi:[1,0,0]
	v_pk_fma_f32 v[0:1], v[150:151], v[0:1], v[54:55] op_sel:[1,0,0]
	v_pk_fma_f32 v[4:5], v[152:153], v[4:5], v[40:41] op_sel:[1,0,0]
	v_cvt_pk_f16_f32 v120, v0, v1
	v_pk_fma_f32 v[0:1], v[150:151], v[52:53], v[116:117] op_sel_hi:[0,1,1] neg_lo:[1,0,0] neg_hi:[1,0,0]
	v_pk_fma_f32 v[0:1], v[150:151], v[0:1], v[56:57] op_sel:[1,0,0]
	v_cvt_pk_f16_f32 v2, v2, v3
	v_cvt_pk_f16_f32 v121, v0, v1
	v_pk_fma_f32 v[0:1], v[150:151], v[42:43], v[126:127] op_sel_hi:[0,1,1] neg_lo:[1,0,0] neg_hi:[1,0,0]
	v_pk_fma_f32 v[0:1], v[150:151], v[0:1], v[46:47] op_sel:[1,0,0]
	buffer_store_dwordx4 v[118:121], v130, s[8:11], 0 offen sc1
	v_cvt_pk_f16_f32 v114, v0, v1
	v_pk_fma_f32 v[0:1], v[150:151], v[44:45], v[128:129] op_sel_hi:[0,1,1] neg_lo:[1,0,0] neg_hi:[1,0,0]
	v_pk_fma_f32 v[0:1], v[150:151], v[0:1], v[48:49] op_sel:[1,0,0]
	v_cvt_pk_f16_f32 v3, v4, v5
	v_cvt_pk_f16_f32 v115, v0, v1
	v_pk_fma_f32 v[0:1], v[150:151], v[34:35], v[122:123] op_sel_hi:[0,1,1] neg_lo:[1,0,0] neg_hi:[1,0,0]
	v_pk_fma_f32 v[0:1], v[150:151], v[0:1], v[38:39] op_sel:[1,0,0]
	s_nop 0
	v_cvt_pk_f16_f32 v116, v0, v1
	v_pk_fma_f32 v[0:1], v[150:151], v[36:37], v[124:125] op_sel_hi:[0,1,1] neg_lo:[1,0,0] neg_hi:[1,0,0]
	v_pk_fma_f32 v[0:1], v[150:151], v[0:1], v[40:41] op_sel:[1,0,0]
	s_nop 0
	v_cvt_pk_f16_f32 v117, v0, v1
	v_add_u32_e32 v0, s12, v156
	buffer_store_dwordx4 v[114:117], v130, s[8:11], 0 offen offset:256 sc1
	s_nop 1
	v_mul_lo_u32 v114, v0, s6
	v_pk_fma_f32 v[0:1], v[146:147], v[58:59], v[86:87] op_sel_hi:[0,1,1] neg_lo:[1,0,0] neg_hi:[1,0,0]
	v_pk_fma_f32 v[0:1], v[146:147], v[0:1], v[62:63] op_sel:[1,0,0]
	v_add_lshl_u32 v114, v166, v114, 1
	v_cvt_pk_f16_f32 v86, v0, v1
	v_pk_fma_f32 v[0:1], v[146:147], v[60:61], v[88:89] op_sel_hi:[0,1,1] neg_lo:[1,0,0] neg_hi:[1,0,0]
	v_pk_fma_f32 v[0:1], v[146:147], v[0:1], v[64:65] op_sel:[1,0,0]
	s_nop 0
	v_cvt_pk_f16_f32 v87, v0, v1
	v_pk_fma_f32 v[0:1], v[146:147], v[50:51], v[82:83] op_sel_hi:[0,1,1] neg_lo:[1,0,0] neg_hi:[1,0,0]
	v_pk_fma_f32 v[0:1], v[146:147], v[0:1], v[54:55] op_sel:[1,0,0]
	s_nop 0
	v_cvt_pk_f16_f32 v88, v0, v1
	v_pk_fma_f32 v[0:1], v[146:147], v[52:53], v[84:85] op_sel_hi:[0,1,1] neg_lo:[1,0,0] neg_hi:[1,0,0]
	v_pk_fma_f32 v[0:1], v[146:147], v[0:1], v[56:57] op_sel:[1,0,0]
	s_nop 0
	v_cvt_pk_f16_f32 v89, v0, v1
	v_pk_fma_f32 v[0:1], v[146:147], v[42:43], v[98:99] op_sel_hi:[0,1,1] neg_lo:[1,0,0] neg_hi:[1,0,0]
	v_pk_fma_f32 v[0:1], v[146:147], v[0:1], v[46:47] op_sel:[1,0,0]
	buffer_store_dwordx4 v[86:89], v114, s[8:11], 0 offen sc1
	v_cvt_pk_f16_f32 v82, v0, v1
	v_pk_fma_f32 v[0:1], v[146:147], v[44:45], v[100:101] op_sel_hi:[0,1,1] neg_lo:[1,0,0] neg_hi:[1,0,0]
	v_pk_fma_f32 v[0:1], v[146:147], v[0:1], v[48:49] op_sel:[1,0,0]
	s_nop 0
	v_cvt_pk_f16_f32 v83, v0, v1
	v_pk_fma_f32 v[0:1], v[146:147], v[34:35], v[90:91] op_sel_hi:[0,1,1] neg_lo:[1,0,0] neg_hi:[1,0,0]
	v_pk_fma_f32 v[0:1], v[146:147], v[0:1], v[38:39] op_sel:[1,0,0]
	s_nop 0
	v_cvt_pk_f16_f32 v84, v0, v1
	v_pk_fma_f32 v[0:1], v[146:147], v[36:37], v[92:93] op_sel_hi:[0,1,1] neg_lo:[1,0,0] neg_hi:[1,0,0]
	v_pk_fma_f32 v[0:1], v[146:147], v[0:1], v[40:41] op_sel:[1,0,0]
	s_nop 0
	v_cvt_pk_f16_f32 v85, v0, v1
	v_add_u32_e32 v0, 0x80, v167
	v_mul_lo_u32 v86, v0, s6
	v_pk_fma_f32 v[0:1], v[148:149], v[58:59], v[102:103] op_sel_hi:[0,1,1] neg_lo:[1,0,0] neg_hi:[1,0,0]
	v_pk_fma_f32 v[0:1], v[148:149], v[0:1], v[62:63] op_sel:[1,0,0]
	buffer_store_dwordx4 v[82:85], v114, s[8:11], 0 offen offset:256 sc1
	v_add_lshl_u32 v90, v166, v86, 1
	ds_read2_b64 v[86:89], v169 offset0:144 offset1:160
	v_cvt_pk_f16_f32 v82, v0, v1
	v_pk_fma_f32 v[0:1], v[148:149], v[60:61], v[104:105] op_sel_hi:[0,1,1] neg_lo:[1,0,0] neg_hi:[1,0,0]
	v_pk_fma_f32 v[0:1], v[148:149], v[0:1], v[64:65] op_sel:[1,0,0]
	s_nop 0
	v_cvt_pk_f16_f32 v83, v0, v1
	v_pk_fma_f32 v[0:1], v[148:149], v[50:51], v[94:95] op_sel_hi:[0,1,1] neg_lo:[1,0,0] neg_hi:[1,0,0]
	v_pk_fma_f32 v[0:1], v[148:149], v[0:1], v[54:55] op_sel:[1,0,0]
	s_nop 0
	v_cvt_pk_f16_f32 v84, v0, v1
	v_pk_fma_f32 v[0:1], v[148:149], v[52:53], v[96:97] op_sel_hi:[0,1,1] neg_lo:[1,0,0] neg_hi:[1,0,0]
	v_pk_fma_f32 v[0:1], v[148:149], v[0:1], v[56:57] op_sel:[1,0,0]
	s_nop 0
	v_cvt_pk_f16_f32 v85, v0, v1
	v_pk_fma_f32 v[0:1], v[148:149], v[42:43], v[110:111] op_sel_hi:[0,1,1] neg_lo:[1,0,0] neg_hi:[1,0,0]
	v_pk_fma_f32 v[0:1], v[148:149], v[0:1], v[46:47] op_sel:[1,0,0]
	buffer_store_dwordx4 v[82:85], v90, s[8:11], 0 offen sc1
	s_nop 1
	v_cvt_pk_f16_f32 v82, v0, v1
	v_pk_fma_f32 v[0:1], v[148:149], v[44:45], v[112:113] op_sel_hi:[0,1,1] neg_lo:[1,0,0] neg_hi:[1,0,0]
	v_pk_fma_f32 v[0:1], v[148:149], v[0:1], v[48:49] op_sel:[1,0,0]
	s_nop 0
	v_cvt_pk_f16_f32 v83, v0, v1
	v_pk_fma_f32 v[0:1], v[148:149], v[34:35], v[106:107] op_sel_hi:[0,1,1] neg_lo:[1,0,0] neg_hi:[1,0,0]
	v_pk_fma_f32 v[0:1], v[148:149], v[0:1], v[38:39] op_sel:[1,0,0]
	s_nop 0
	v_cvt_pk_f16_f32 v84, v0, v1
	v_pk_fma_f32 v[0:1], v[148:149], v[36:37], v[108:109] op_sel_hi:[0,1,1] neg_lo:[1,0,0] neg_hi:[1,0,0]
	v_pk_fma_f32 v[0:1], v[148:149], v[0:1], v[40:41] op_sel:[1,0,0]
	s_nop 0
	v_cvt_pk_f16_f32 v85, v0, v1
	v_add_u32_e32 v0, 0x90, v167
	buffer_store_dwordx4 v[82:85], v90, s[8:11], 0 offen offset:256 sc1
	s_nop 1
	v_mul_lo_u32 v82, v0, s6
	s_waitcnt lgkmcnt(0)
	v_pk_fma_f32 v[0:1], v[86:87], v[58:59], v[70:71] op_sel_hi:[0,1,1] neg_lo:[1,0,0] neg_hi:[1,0,0]
	v_pk_fma_f32 v[0:1], v[86:87], v[0:1], v[62:63] op_sel:[1,0,0]
	v_add_lshl_u32 v82, v166, v82, 1
	v_cvt_pk_f16_f32 v70, v0, v1
	v_pk_fma_f32 v[0:1], v[86:87], v[60:61], v[72:73] op_sel_hi:[0,1,1] neg_lo:[1,0,0] neg_hi:[1,0,0]
	v_pk_fma_f32 v[0:1], v[86:87], v[0:1], v[64:65] op_sel:[1,0,0]
	s_nop 0
	v_cvt_pk_f16_f32 v71, v0, v1
	v_pk_fma_f32 v[0:1], v[86:87], v[50:51], v[66:67] op_sel_hi:[0,1,1] neg_lo:[1,0,0] neg_hi:[1,0,0]
	v_pk_fma_f32 v[0:1], v[86:87], v[0:1], v[54:55] op_sel:[1,0,0]
	s_nop 0
	v_cvt_pk_f16_f32 v72, v0, v1
	v_pk_fma_f32 v[0:1], v[86:87], v[52:53], v[68:69] op_sel_hi:[0,1,1] neg_lo:[1,0,0] neg_hi:[1,0,0]
	v_pk_fma_f32 v[0:1], v[86:87], v[0:1], v[56:57] op_sel:[1,0,0]
	s_nop 0
	v_cvt_pk_f16_f32 v73, v0, v1
	v_pk_fma_f32 v[0:1], v[86:87], v[42:43], v[78:79] op_sel_hi:[0,1,1] neg_lo:[1,0,0] neg_hi:[1,0,0]
	v_pk_fma_f32 v[0:1], v[86:87], v[0:1], v[46:47] op_sel:[1,0,0]
	buffer_store_dwordx4 v[70:73], v82, s[8:11], 0 offen sc1
	v_cvt_pk_f16_f32 v66, v0, v1
	v_pk_fma_f32 v[0:1], v[86:87], v[44:45], v[80:81] op_sel_hi:[0,1,1] neg_lo:[1,0,0] neg_hi:[1,0,0]
	v_pk_fma_f32 v[0:1], v[86:87], v[0:1], v[48:49] op_sel:[1,0,0]
	s_nop 0
	v_cvt_pk_f16_f32 v67, v0, v1
	v_pk_fma_f32 v[0:1], v[86:87], v[34:35], v[74:75] op_sel_hi:[0,1,1] neg_lo:[1,0,0] neg_hi:[1,0,0]
	v_pk_fma_f32 v[0:1], v[86:87], v[0:1], v[38:39] op_sel:[1,0,0]
	s_nop 0
	v_cvt_pk_f16_f32 v68, v0, v1
	v_pk_fma_f32 v[0:1], v[86:87], v[36:37], v[76:77] op_sel_hi:[0,1,1] neg_lo:[1,0,0] neg_hi:[1,0,0]
	v_pk_fma_f32 v[0:1], v[86:87], v[0:1], v[40:41] op_sel:[1,0,0]
	s_nop 0
	v_cvt_pk_f16_f32 v69, v0, v1
	v_add_u32_e32 v0, 0xa0, v167
	buffer_store_dwordx4 v[66:69], v82, s[8:11], 0 offen offset:256 sc1
	s_nop 1
	v_mul_lo_u32 v66, v0, s6
	v_pk_fma_f32 v[0:1], v[88:89], v[58:59], v[22:23] op_sel_hi:[0,1,1] neg_lo:[1,0,0] neg_hi:[1,0,0]
	v_pk_fma_f32 v[0:1], v[88:89], v[0:1], v[62:63] op_sel:[1,0,0]
	v_add_lshl_u32 v66, v166, v66, 1
	v_cvt_pk_f16_f32 v22, v0, v1
	v_pk_fma_f32 v[0:1], v[88:89], v[60:61], v[24:25] op_sel_hi:[0,1,1] neg_lo:[1,0,0] neg_hi:[1,0,0]
	v_pk_fma_f32 v[0:1], v[88:89], v[0:1], v[64:65] op_sel:[1,0,0]
	s_nop 0
	v_cvt_pk_f16_f32 v23, v0, v1
	v_pk_fma_f32 v[0:1], v[88:89], v[50:51], v[18:19] op_sel_hi:[0,1,1] neg_lo:[1,0,0] neg_hi:[1,0,0]
	v_pk_fma_f32 v[0:1], v[88:89], v[0:1], v[54:55] op_sel:[1,0,0]
	s_nop 0
	v_cvt_pk_f16_f32 v24, v0, v1
	v_pk_fma_f32 v[0:1], v[88:89], v[52:53], v[20:21] op_sel_hi:[0,1,1] neg_lo:[1,0,0] neg_hi:[1,0,0]
	v_pk_fma_f32 v[0:1], v[88:89], v[0:1], v[56:57] op_sel:[1,0,0]
	s_nop 0
	v_cvt_pk_f16_f32 v25, v0, v1
	v_pk_fma_f32 v[0:1], v[88:89], v[42:43], v[30:31] op_sel_hi:[0,1,1] neg_lo:[1,0,0] neg_hi:[1,0,0]
	v_pk_fma_f32 v[0:1], v[88:89], v[0:1], v[46:47] op_sel:[1,0,0]
	buffer_store_dwordx4 v[22:25], v66, s[8:11], 0 offen sc1
	v_cvt_pk_f16_f32 v18, v0, v1
	v_pk_fma_f32 v[0:1], v[88:89], v[44:45], v[32:33] op_sel_hi:[0,1,1] neg_lo:[1,0,0] neg_hi:[1,0,0]
	v_pk_fma_f32 v[0:1], v[88:89], v[0:1], v[48:49] op_sel:[1,0,0]
	s_nop 0
	v_cvt_pk_f16_f32 v19, v0, v1
	v_pk_fma_f32 v[0:1], v[88:89], v[34:35], v[26:27] op_sel_hi:[0,1,1] neg_lo:[1,0,0] neg_hi:[1,0,0]
	v_pk_fma_f32 v[0:1], v[88:89], v[0:1], v[38:39] op_sel:[1,0,0]
	s_nop 0
	v_cvt_pk_f16_f32 v20, v0, v1
	v_pk_fma_f32 v[0:1], v[88:89], v[36:37], v[28:29] op_sel_hi:[0,1,1] neg_lo:[1,0,0] neg_hi:[1,0,0]
	v_pk_fma_f32 v[0:1], v[88:89], v[0:1], v[40:41] op_sel:[1,0,0]
	s_nop 0
	v_cvt_pk_f16_f32 v21, v0, v1
	v_add_u32_e32 v0, 0xb0, v167
	buffer_store_dwordx4 v[18:21], v66, s[8:11], 0 offen offset:256 sc1
	s_nop 1
	v_mul_lo_u32 v18, v0, s6
	v_pk_fma_f32 v[0:1], v[152:153], v[58:59], v[14:15] op_sel_hi:[0,1,1] neg_lo:[1,0,0] neg_hi:[1,0,0]
	v_pk_fma_f32 v[0:1], v[152:153], v[0:1], v[62:63] op_sel:[1,0,0]
	s_nop 0
	v_cvt_pk_f16_f32 v14, v0, v1
	v_pk_fma_f32 v[0:1], v[152:153], v[60:61], v[16:17] op_sel_hi:[0,1,1] neg_lo:[1,0,0] neg_hi:[1,0,0]
	v_pk_fma_f32 v[0:1], v[152:153], v[0:1], v[64:65] op_sel:[1,0,0]
	s_nop 0
	v_cvt_pk_f16_f32 v15, v0, v1
	v_pk_fma_f32 v[0:1], v[152:153], v[50:51], v[6:7] op_sel_hi:[0,1,1] neg_lo:[1,0,0] neg_hi:[1,0,0]
	v_pk_fma_f32 v[0:1], v[152:153], v[0:1], v[54:55] op_sel:[1,0,0]
	v_pk_fma_f32 v[6:7], v[152:153], v[44:45], v[12:13] op_sel_hi:[0,1,1] neg_lo:[1,0,0] neg_hi:[1,0,0]
	v_cvt_pk_f16_f32 v16, v0, v1
	v_pk_fma_f32 v[0:1], v[152:153], v[52:53], v[8:9] op_sel_hi:[0,1,1] neg_lo:[1,0,0] neg_hi:[1,0,0]
	v_pk_fma_f32 v[0:1], v[152:153], v[0:1], v[56:57] op_sel:[1,0,0]
	v_pk_fma_f32 v[6:7], v[152:153], v[6:7], v[48:49] op_sel:[1,0,0]
	v_cvt_pk_f16_f32 v17, v0, v1
	v_pk_fma_f32 v[0:1], v[152:153], v[42:43], v[10:11] op_sel_hi:[0,1,1] neg_lo:[1,0,0] neg_hi:[1,0,0]
	v_pk_fma_f32 v[0:1], v[152:153], v[0:1], v[46:47] op_sel:[1,0,0]
	v_add_lshl_u32 v8, v166, v18, 1
	v_cvt_pk_f16_f32 v0, v0, v1
	v_cvt_pk_f16_f32 v1, v6, v7
	buffer_store_dwordx4 v[14:17], v8, s[8:11], 0 offen sc1
	buffer_store_dwordx4 v[0:3], v8, s[8:11], 0 offen offset:256 sc1
	s_endpgm

	.amdhsa_kernel _Z6gemm_qILi0ELi1EEvPKDF16_S1_iiiiiiPKfS3_S3_S3_PDF16_8ConvArgs
		.amdhsa_group_segment_fixed_size 0
		.amdhsa_private_segment_fixed_size 0
		.amdhsa_kernarg_size 224
		.amdhsa_user_sgpr_count 2
		.amdhsa_user_sgpr_dispatch_ptr 0
		.amdhsa_user_sgpr_queue_ptr 0
		.amdhsa_user_sgpr_kernarg_segment_ptr 1
		.amdhsa_user_sgpr_dispatch_id 0
		.amdhsa_user_sgpr_kernarg_preload_length 0
		.amdhsa_user_sgpr_kernarg_preload_offset 0
		.amdhsa_user_sgpr_private_segment_size 0
		.amdhsa_uses_dynamic_stack 0
		.amdhsa_enable_private_segment 0
		.amdhsa_system_sgpr_workgroup_id_x 1
		.amdhsa_system_sgpr_workgroup_id_y 0
		.amdhsa_system_sgpr_workgroup_id_z 0
		.amdhsa_system_sgpr_workgroup_info 0
		.amdhsa_system_vgpr_workitem_id 0
		.amdhsa_next_free_vgpr 244
		.amdhsa_next_free_sgpr 46
		.amdhsa_accum_offset 244
		.amdhsa_reserve_vcc 1
		.amdhsa_float_round_mode_32 0
		.amdhsa_float_round_mode_16_64 0
		.amdhsa_float_denorm_mode_32 3
		.amdhsa_float_denorm_mode_16_64 3
		.amdhsa_dx10_clamp 1
		.amdhsa_ieee_mode 1
		.amdhsa_fp16_overflow 0
		.amdhsa_tg_split 0
		.amdhsa_exception_fp_ieee_invalid_op 0
		.amdhsa_exception_fp_denorm_src 0
		.amdhsa_exception_fp_ieee_div_zero 0
		.amdhsa_exception_fp_ieee_overflow 0
		.amdhsa_exception_fp_ieee_underflow 0
		.amdhsa_exception_fp_ieee_inexact 0
		.amdhsa_exception_int_div_zero 0
	.end_amdhsa_kernel

.LBB8_6:
	s_or_b64 exec, exec, s[2:3]
	s_add_i32 s0, 0, 0x18000
	v_add_u32_e32 v48, s0, v38
	s_mov_b64 s[0:1], 0x80
	v_readfirstlane_b32 s22, v48
	v_add_u32_e32 v49, 0x2000, v48
	v_lshl_add_u64 v[2:3], v[30:31], 0, s[0:1]
	s_mov_b32 m0, s22
	v_readfirstlane_b32 s21, v49
	v_add_u32_e32 v46, 0x8000, v35
	s_waitcnt vmcnt(4)
	s_barrier
	global_load_lds_dwordx4 v[2:3], off
	v_lshl_add_u64 v[2:3], v[32:33], 0, s[0:1]
	s_mov_b32 m0, s21
	v_readfirstlane_b32 s19, v46
	v_add_u32_e32 v47, 0xa000, v35
	s_add_i32 s2, 0, 0x1c000
	global_load_lds_dwordx4 v[2:3], off
	v_lshl_add_u64 v[2:3], v[26:27], 0, s[0:1]
	s_mov_b32 m0, s19
	v_readfirstlane_b32 s16, v47
	v_add_u32_e32 v37, s2, v38
	global_load_lds_dwordx4 v[2:3], off
	v_lshl_add_u64 v[2:3], v[28:29], 0, s[0:1]
	s_mov_b32 m0, s16
	v_readfirstlane_b32 s3, v37
	v_add_u32_e32 v39, 0x2000, v37
	global_load_lds_dwordx4 v[2:3], off
	v_lshl_add_u64 v[2:3], v[22:23], 0, s[0:1]
	s_mov_b32 m0, s3
	v_readfirstlane_b32 s2, v39
	global_load_lds_dwordx4 v[2:3], off
	v_lshl_add_u64 v[2:3], v[24:25], 0, s[0:1]
	s_mov_b32 m0, s2
	v_lshlrev_b32_e32 v1, 6, v0
	global_load_lds_dwordx4 v[2:3], off
	v_lshlrev_b32_e32 v4, 2, v0
	v_and_b32_e32 v2, 0x3c0, v1
	v_and_b32_e32 v3, 48, v0
	v_and_b32_e32 v4, 32, v4
	v_bitop3_b32 v6, v2, v4, v3 bitop3:0x36
	v_and_b32_e32 v1, 0x3000, v1
	v_add3_u32 v234, 0, v1, v6
	v_add_u32_e32 v2, 0x10000, v234
	v_add_u32_e32 v4, 0x10800, v234
	s_waitcnt vmcnt(6)
	s_barrier
	v_add_u32_e32 v3, 0x10400, v234
	ds_read_b128 v[10:13], v2
	ds_read_b128 v[14:17], v3
	v_add_u32_e32 v5, 0x10c00, v234
	ds_read_b128 v[50:53], v4
	ds_read_b128 v[54:57], v5
	v_lshlrev_b32_e32 v1, 5, v0
	v_and_b32_e32 v1, 0x2000, v1
	v_add3_u32 v1, 0, v1, v6
	v_add_u32_e32 v38, 0xc000, v35
	v_add_u32_e32 v40, 0xe000, v35
	v_readfirstlane_b32 s7, v38
	v_lshl_add_u64 v[6:7], v[18:19], 0, s[0:1]
	s_mov_b32 m0, s7
	v_readfirstlane_b32 s4, v40
	global_load_lds_dwordx4 v[6:7], off
	v_lshl_add_u64 v[6:7], v[20:21], 0, s[0:1]
	s_mov_b32 m0, s4
	s_nop 0
	global_load_lds_dwordx4 v[6:7], off
	ds_read_b128 v[42:45], v1
	ds_read_b128 v[58:61], v1 offset:1024
	ds_read_b128 v[62:65], v1 offset:2048
	ds_read_b128 v[66:69], v1 offset:3072
	ds_read_b128 v[70:73], v1 offset:4096
	ds_read_b128 v[74:77], v1 offset:5120
	ds_read_b128 v[78:81], v1 offset:6144
	ds_read_b128 v[82:85], v1 offset:7168
	s_waitcnt lgkmcnt(8)
	s_barrier
	s_waitcnt lgkmcnt(0)
	s_setprio 1
	s_waitcnt lgkmcnt(0)
	v_mfma_f32_16x16x32_f16 v[6:9], v[10:13], v[42:45], 0
	v_mfma_f32_16x16x32_f16 v[86:89], v[14:17], v[58:61], v[6:9]
	v_mfma_f32_16x16x32_f16 v[6:9], v[50:53], v[42:45], 0
	v_mfma_f32_16x16x32_f16 v[90:93], v[54:57], v[58:61], v[6:9]
	v_mfma_f32_16x16x32_f16 v[6:9], v[10:13], v[62:65], 0
	v_mfma_f32_16x16x32_f16 v[94:97], v[14:17], v[66:69], v[6:9]
	v_mfma_f32_16x16x32_f16 v[6:9], v[50:53], v[62:65], 0
	v_mfma_f32_16x16x32_f16 v[98:101], v[54:57], v[66:69], v[6:9]
	v_mfma_f32_16x16x32_f16 v[6:9], v[10:13], v[70:73], 0
	v_mfma_f32_16x16x32_f16 v[102:105], v[14:17], v[74:77], v[6:9]
	v_mfma_f32_16x16x32_f16 v[6:9], v[50:53], v[70:73], 0
	v_mfma_f32_16x16x32_f16 v[106:109], v[54:57], v[74:77], v[6:9]
	v_mfma_f32_16x16x32_f16 v[6:9], v[10:13], v[78:81], 0
	v_mfma_f32_16x16x32_f16 v[110:113], v[14:17], v[82:85], v[6:9]
	v_mfma_f32_16x16x32_f16 v[6:9], v[50:53], v[78:81], 0
	v_mfma_f32_16x16x32_f16 v[114:117], v[54:57], v[82:85], v[6:9]
	s_setprio 0
	s_barrier
	s_mov_b64 s[0:1], 0x100
	v_readfirstlane_b32 s15, v36
	v_add_u32_e32 v41, 0x2000, v36
	s_nop 1
	v_add_u32_e32 v6, 0x14000, v234
	v_add_u32_e32 v8, 0x14800, v234
	v_lshl_add_u64 v[134:135], v[30:31], 0, s[0:1]
	s_mov_b32 m0, s15
	v_readfirstlane_b32 s5, v41
	v_add_u32_e32 v7, 0x14400, v234
	ds_read_b128 v[118:121], v6
	ds_read_b128 v[122:125], v7
	v_add_u32_e32 v9, 0x14c00, v234
	ds_read_b128 v[126:129], v8
	ds_read_b128 v[130:133], v9
	global_load_lds_dwordx4 v[134:135], off
	v_lshl_add_u64 v[134:135], v[32:33], 0, s[0:1]
	s_mov_b32 m0, s5
	s_nop 0
	global_load_lds_dwordx4 v[134:135], off
	s_barrier
	s_waitcnt lgkmcnt(0)
	s_setprio 1
	s_waitcnt lgkmcnt(0)
	v_mfma_f32_16x16x32_f16 v[134:137], v[118:121], v[42:45], 0
	v_mfma_f32_16x16x32_f16 v[42:45], v[126:129], v[42:45], 0
	v_mfma_f32_16x16x32_f16 v[134:137], v[122:125], v[58:61], v[134:137]
	v_mfma_f32_16x16x32_f16 v[58:61], v[130:133], v[58:61], v[42:45]
	v_mfma_f32_16x16x32_f16 v[42:45], v[118:121], v[62:65], 0
	v_mfma_f32_16x16x32_f16 v[138:141], v[122:125], v[66:69], v[42:45]
	v_mfma_f32_16x16x32_f16 v[42:45], v[126:129], v[62:65], 0
	v_mfma_f32_16x16x32_f16 v[62:65], v[130:133], v[66:69], v[42:45]
	v_mfma_f32_16x16x32_f16 v[42:45], v[118:121], v[70:73], 0
	v_mfma_f32_16x16x32_f16 v[66:69], v[122:125], v[74:77], v[42:45]
	v_mfma_f32_16x16x32_f16 v[42:45], v[126:129], v[70:73], 0
	v_mfma_f32_16x16x32_f16 v[70:73], v[130:133], v[74:77], v[42:45]
	v_mfma_f32_16x16x32_f16 v[42:45], v[118:121], v[78:81], 0
	v_mfma_f32_16x16x32_f16 v[74:77], v[122:125], v[82:85], v[42:45]
	v_mfma_f32_16x16x32_f16 v[42:45], v[126:129], v[78:81], 0
	v_mfma_f32_16x16x32_f16 v[78:81], v[130:133], v[82:85], v[42:45]
	s_setprio 0
	v_readfirstlane_b32 s17, v35
	s_nop 4
	v_lshl_add_u64 v[42:43], v[26:27], 0, s[0:1]
	s_mov_b32 m0, s17
	s_barrier
	ds_read_b128 v[82:85], v1 offset:16384
	ds_read_b128 v[142:145], v1 offset:17408
	ds_read_b128 v[146:149], v1 offset:18432
	ds_read_b128 v[150:153], v1 offset:19456
	ds_read_b128 v[154:157], v1 offset:20480
	ds_read_b128 v[158:161], v1 offset:21504
	ds_read_b128 v[162:165], v1 offset:22528
	ds_read_b128 v[166:169], v1 offset:23552
	global_load_lds_dwordx4 v[42:43], off
	v_add_u32_e32 v42, 0x2000, v35
	v_lshl_add_u64 v[44:45], v[28:29], 0, s[0:1]
	v_readfirstlane_b32 s10, v42
	s_mov_b32 m0, s10
	s_nop 0
	global_load_lds_dwordx4 v[44:45], off
	s_barrier
	s_waitcnt lgkmcnt(0)
	s_setprio 1
	s_waitcnt lgkmcnt(0)
	v_mfma_f32_16x16x32_f16 v[170:173], v[10:13], v[82:85], 0
	v_mfma_f32_16x16x32_f16 v[178:181], v[10:13], v[146:149], 0
	v_mfma_f32_16x16x32_f16 v[186:189], v[10:13], v[154:157], 0
	v_mfma_f32_16x16x32_f16 v[10:13], v[10:13], v[162:165], 0
	v_mfma_f32_16x16x32_f16 v[194:197], v[14:17], v[166:169], v[10:13]
	v_mfma_f32_16x16x32_f16 v[10:13], v[50:53], v[162:165], 0
	v_mfma_f32_16x16x32_f16 v[174:177], v[50:53], v[82:85], 0
	v_mfma_f32_16x16x32_f16 v[182:185], v[50:53], v[146:149], 0
	v_mfma_f32_16x16x32_f16 v[190:193], v[50:53], v[154:157], 0
	v_mfma_f32_16x16x32_f16 v[50:53], v[54:57], v[166:169], v[10:13]
	v_mfma_f32_16x16x32_f16 v[170:173], v[14:17], v[142:145], v[170:173]
	v_mfma_f32_16x16x32_f16 v[174:177], v[54:57], v[142:145], v[174:177]
	v_mfma_f32_16x16x32_f16 v[178:181], v[14:17], v[150:153], v[178:181]
	v_mfma_f32_16x16x32_f16 v[182:185], v[54:57], v[150:153], v[182:185]
	v_mfma_f32_16x16x32_f16 v[186:189], v[14:17], v[158:161], v[186:189]
	v_mfma_f32_16x16x32_f16 v[190:193], v[54:57], v[158:161], v[190:193]
	s_setprio 0
	s_barrier
	v_readfirstlane_b32 s14, v34
	v_add_u32_e32 v43, 0x2000, v34
	v_lshl_add_u64 v[10:11], v[22:23], 0, s[0:1]
	s_mov_b32 m0, s14
	v_readfirstlane_b32 s11, v43
	global_load_lds_dwordx4 v[10:11], off
	v_lshl_add_u64 v[10:11], v[24:25], 0, s[0:1]
	s_mov_b32 m0, s11
	s_nop 0
	global_load_lds_dwordx4 v[10:11], off
	s_waitcnt vmcnt(6)
	s_barrier
	s_setprio 1
	v_mfma_f32_16x16x32_f16 v[10:13], v[118:121], v[82:85], 0
	v_mfma_f32_16x16x32_f16 v[54:57], v[122:125], v[142:145], v[10:13]
	v_mfma_f32_16x16x32_f16 v[10:13], v[126:129], v[82:85], 0
	v_mfma_f32_16x16x32_f16 v[82:85], v[130:133], v[142:145], v[10:13]
	v_mfma_f32_16x16x32_f16 v[10:13], v[118:121], v[146:149], 0
	v_mfma_f32_16x16x32_f16 v[142:145], v[122:125], v[150:153], v[10:13]
	v_mfma_f32_16x16x32_f16 v[10:13], v[126:129], v[146:149], 0
	v_mfma_f32_16x16x32_f16 v[146:149], v[130:133], v[150:153], v[10:13]
	v_mfma_f32_16x16x32_f16 v[10:13], v[118:121], v[154:157], 0
	v_mfma_f32_16x16x32_f16 v[150:153], v[122:125], v[158:161], v[10:13]
	v_mfma_f32_16x16x32_f16 v[10:13], v[126:129], v[154:157], 0
	v_mfma_f32_16x16x32_f16 v[154:157], v[130:133], v[158:161], v[10:13]
	v_mfma_f32_16x16x32_f16 v[10:13], v[118:121], v[162:165], 0
	v_mfma_f32_16x16x32_f16 v[118:121], v[122:125], v[166:169], v[10:13]
	v_mfma_f32_16x16x32_f16 v[10:13], v[126:129], v[162:165], 0
	v_mfma_f32_16x16x32_f16 v[122:125], v[130:133], v[166:169], v[10:13]
	s_setprio 0
	s_nop 5
	v_add_u32_e32 v10, 0x18000, v234
	v_add_u32_e32 v12, 0x18800, v234
	s_barrier
	v_add_u32_e32 v11, 0x18400, v234
	ds_read_b128 v[126:129], v10
	ds_read_b128 v[130:133], v11
	v_add_u32_e32 v13, 0x18c00, v234
	ds_read_b128 v[158:161], v12
	ds_read_b128 v[162:165], v13
	v_add_u32_e32 v44, 0x4000, v35
	v_add_u32_e32 v45, 0x6000, v35
	v_readfirstlane_b32 s20, v44
	v_lshl_add_u64 v[14:15], v[18:19], 0, s[0:1]
	s_mov_b32 m0, s20
	v_readfirstlane_b32 s18, v45
	ds_read_b128 v[166:169], v1 offset:32768
	ds_read_b128 v[198:201], v1 offset:33792
	ds_read_b128 v[202:205], v1 offset:34816
	ds_read_b128 v[206:209], v1 offset:35840
	ds_read_b128 v[210:213], v1 offset:36864
	ds_read_b128 v[214:217], v1 offset:37888
	ds_read_b128 v[218:221], v1 offset:38912
	ds_read_b128 v[222:225], v1 offset:39936
	global_load_lds_dwordx4 v[14:15], off
	v_lshl_add_u64 v[14:15], v[20:21], 0, s[0:1]
	s_mov_b32 m0, s18
	s_nop 0
	global_load_lds_dwordx4 v[14:15], off
	s_waitcnt lgkmcnt(8)
	s_barrier
	s_waitcnt lgkmcnt(0)
	s_setprio 1
	s_waitcnt lgkmcnt(0)
	v_mfma_f32_16x16x32_f16 v[14:17], v[126:129], v[166:169], v[86:89]
	v_mfma_f32_16x16x32_f16 v[86:89], v[130:133], v[198:201], v[14:17]
	v_mfma_f32_16x16x32_f16 v[14:17], v[158:161], v[166:169], v[90:93]
	v_mfma_f32_16x16x32_f16 v[90:93], v[162:165], v[198:201], v[14:17]
	v_mfma_f32_16x16x32_f16 v[14:17], v[126:129], v[202:205], v[94:97]
	v_mfma_f32_16x16x32_f16 v[94:97], v[130:133], v[206:209], v[14:17]
	v_mfma_f32_16x16x32_f16 v[14:17], v[158:161], v[202:205], v[98:101]
	v_mfma_f32_16x16x32_f16 v[98:101], v[162:165], v[206:209], v[14:17]
	v_mfma_f32_16x16x32_f16 v[14:17], v[126:129], v[210:213], v[102:105]
	v_mfma_f32_16x16x32_f16 v[102:105], v[130:133], v[214:217], v[14:17]
	v_mfma_f32_16x16x32_f16 v[14:17], v[158:161], v[210:213], v[106:109]
	v_mfma_f32_16x16x32_f16 v[106:109], v[162:165], v[214:217], v[14:17]
	v_mfma_f32_16x16x32_f16 v[14:17], v[126:129], v[218:221], v[110:113]
	v_mfma_f32_16x16x32_f16 v[110:113], v[130:133], v[222:225], v[14:17]
	v_mfma_f32_16x16x32_f16 v[14:17], v[158:161], v[218:221], v[114:117]
	v_mfma_f32_16x16x32_f16 v[114:117], v[162:165], v[222:225], v[14:17]
	s_setprio 0
	s_barrier
	s_mov_b64 s[0:1], 0x180
	s_mov_b32 m0, s22
	s_nop 2
	v_add_u32_e32 v14, 0x1c000, v234
	v_add_u32_e32 v16, 0x1c800, v234
	v_lshl_add_u64 v[242:243], v[30:31], 0, s[0:1]
	v_add_u32_e32 v15, 0x1c400, v234
	ds_read_b128 v[226:229], v14
	ds_read_b128 v[230:233], v15
	v_add_u32_e32 v17, 0x1cc00, v234
	ds_read_b128 v[234:237], v16
	ds_read_b128 v[238:241], v17
	global_load_lds_dwordx4 v[242:243], off
	v_lshl_add_u64 v[242:243], v[32:33], 0, s[0:1]
	s_mov_b32 m0, s21
	s_nop 0
	global_load_lds_dwordx4 v[242:243], off
	s_barrier
	s_waitcnt lgkmcnt(0)
	s_setprio 1
	s_waitcnt lgkmcnt(0)
	v_mfma_f32_16x16x32_f16 v[134:137], v[226:229], v[166:169], v[134:137]
	v_mfma_f32_16x16x32_f16 v[58:61], v[234:237], v[166:169], v[58:61]
	v_mfma_f32_16x16x32_f16 v[138:141], v[226:229], v[202:205], v[138:141]
	v_mfma_f32_16x16x32_f16 v[62:65], v[234:237], v[202:205], v[62:65]
	v_mfma_f32_16x16x32_f16 v[66:69], v[226:229], v[210:213], v[66:69]
	v_mfma_f32_16x16x32_f16 v[70:73], v[234:237], v[210:213], v[70:73]
	v_mfma_f32_16x16x32_f16 v[74:77], v[226:229], v[218:221], v[74:77]
	v_mfma_f32_16x16x32_f16 v[78:81], v[234:237], v[218:221], v[78:81]
	v_mfma_f32_16x16x32_f16 v[134:137], v[230:233], v[198:201], v[134:137]
	v_mfma_f32_16x16x32_f16 v[58:61], v[238:241], v[198:201], v[58:61]
	v_mfma_f32_16x16x32_f16 v[138:141], v[230:233], v[206:209], v[138:141]
	v_mfma_f32_16x16x32_f16 v[62:65], v[238:241], v[206:209], v[62:65]
	v_mfma_f32_16x16x32_f16 v[66:69], v[230:233], v[214:217], v[66:69]
	v_mfma_f32_16x16x32_f16 v[70:73], v[238:241], v[214:217], v[70:73]
	v_mfma_f32_16x16x32_f16 v[74:77], v[230:233], v[222:225], v[74:77]
	v_mfma_f32_16x16x32_f16 v[78:81], v[238:241], v[222:225], v[78:81]
	s_setprio 0
	s_mov_b32 m0, s19
	v_lshl_add_u64 v[242:243], v[26:27], 0, s[0:1]
	s_barrier
	ds_read_b128 v[166:169], v1 offset:49152
	ds_read_b128 v[198:201], v1 offset:50176
	ds_read_b128 v[202:205], v1 offset:51200
	ds_read_b128 v[206:209], v1 offset:52224
	ds_read_b128 v[210:213], v1 offset:53248
	ds_read_b128 v[214:217], v1 offset:54272
	ds_read_b128 v[218:221], v1 offset:55296
	ds_read_b128 v[222:225], v1 offset:56320
	global_load_lds_dwordx4 v[242:243], off
	v_lshl_add_u64 v[242:243], v[28:29], 0, s[0:1]
	s_mov_b32 m0, s16
	s_nop 0
	global_load_lds_dwordx4 v[242:243], off
	s_barrier
	s_waitcnt lgkmcnt(0)
	s_setprio 1
	s_waitcnt lgkmcnt(0)
	v_mfma_f32_16x16x32_f16 v[170:173], v[126:129], v[166:169], v[170:173]
	v_mfma_f32_16x16x32_f16 v[178:181], v[126:129], v[202:205], v[178:181]
	v_mfma_f32_16x16x32_f16 v[186:189], v[126:129], v[210:213], v[186:189]
	v_mfma_f32_16x16x32_f16 v[126:129], v[126:129], v[218:221], v[194:197]
	v_mfma_f32_16x16x32_f16 v[50:53], v[158:161], v[218:221], v[50:53]
	v_mfma_f32_16x16x32_f16 v[174:177], v[158:161], v[166:169], v[174:177]
	v_mfma_f32_16x16x32_f16 v[182:185], v[158:161], v[202:205], v[182:185]
	v_mfma_f32_16x16x32_f16 v[190:193], v[158:161], v[210:213], v[190:193]
	v_mfma_f32_16x16x32_f16 v[126:129], v[130:133], v[222:225], v[126:129]
	v_mfma_f32_16x16x32_f16 v[50:53], v[162:165], v[222:225], v[50:53]
	v_mfma_f32_16x16x32_f16 v[170:173], v[130:133], v[198:201], v[170:173]
	v_mfma_f32_16x16x32_f16 v[174:177], v[162:165], v[198:201], v[174:177]
	v_mfma_f32_16x16x32_f16 v[178:181], v[130:133], v[206:209], v[178:181]
	v_mfma_f32_16x16x32_f16 v[182:185], v[162:165], v[206:209], v[182:185]
	v_mfma_f32_16x16x32_f16 v[186:189], v[130:133], v[214:217], v[186:189]
	v_mfma_f32_16x16x32_f16 v[190:193], v[162:165], v[214:217], v[190:193]
	s_setprio 0
	s_barrier
	s_mov_b32 m0, s3
	v_lshl_add_u64 v[130:131], v[22:23], 0, s[0:1]
	global_load_lds_dwordx4 v[130:131], off
	v_lshl_add_u64 v[130:131], v[24:25], 0, s[0:1]
	s_mov_b32 m0, s2
	s_nop 0
	global_load_lds_dwordx4 v[130:131], off
	s_waitcnt vmcnt(6)
	s_barrier
	s_setprio 1
	v_mfma_f32_16x16x32_f16 v[82:85], v[234:237], v[166:169], v[82:85]
	v_mfma_f32_16x16x32_f16 v[130:133], v[226:229], v[202:205], v[142:145]
	v_mfma_f32_16x16x32_f16 v[142:145], v[234:237], v[202:205], v[146:149]
	v_mfma_f32_16x16x32_f16 v[146:149], v[226:229], v[210:213], v[150:153]
	v_mfma_f32_16x16x32_f16 v[150:153], v[234:237], v[210:213], v[154:157]
	v_mfma_f32_16x16x32_f16 v[118:121], v[226:229], v[218:221], v[118:121]
	v_mfma_f32_16x16x32_f16 v[122:125], v[234:237], v[218:221], v[122:125]
	v_mfma_f32_16x16x32_f16 v[54:57], v[226:229], v[166:169], v[54:57]
	v_mfma_f32_16x16x32_f16 v[82:85], v[238:241], v[198:201], v[82:85]
	v_mfma_f32_16x16x32_f16 v[130:133], v[230:233], v[206:209], v[130:133]
	v_mfma_f32_16x16x32_f16 v[142:145], v[238:241], v[206:209], v[142:145]
	v_mfma_f32_16x16x32_f16 v[146:149], v[230:233], v[214:217], v[146:149]
	v_mfma_f32_16x16x32_f16 v[150:153], v[238:241], v[214:217], v[150:153]
	v_mfma_f32_16x16x32_f16 v[118:121], v[230:233], v[222:225], v[118:121]
	v_mfma_f32_16x16x32_f16 v[122:125], v[238:241], v[222:225], v[122:125]
	v_mfma_f32_16x16x32_f16 v[54:57], v[230:233], v[198:201], v[54:57]
	s_setprio 0
	s_barrier
	ds_read_b128 v[154:157], v2
	ds_read_b128 v[158:161], v3
	ds_read_b128 v[162:165], v4
	ds_read_b128 v[166:169], v5
	s_mov_b32 m0, s7
	v_lshl_add_u64 v[194:195], v[18:19], 0, s[0:1]
	global_load_lds_dwordx4 v[194:195], off
	v_lshl_add_u64 v[194:195], v[20:21], 0, s[0:1]
	s_mov_b32 m0, s4
	s_nop 0
	global_load_lds_dwordx4 v[194:195], off
	ds_read_b128 v[194:197], v1
	ds_read_b128 v[198:201], v1 offset:1024
	ds_read_b128 v[202:205], v1 offset:2048
	ds_read_b128 v[206:209], v1 offset:3072
	ds_read_b128 v[210:213], v1 offset:4096
	ds_read_b128 v[214:217], v1 offset:5120
	ds_read_b128 v[218:221], v1 offset:6144
	ds_read_b128 v[222:225], v1 offset:7168
	s_waitcnt lgkmcnt(8)
	s_barrier
	s_waitcnt lgkmcnt(0)
	s_setprio 1
	s_waitcnt lgkmcnt(0)
	v_mfma_f32_16x16x32_f16 v[86:89], v[154:157], v[194:197], v[86:89]
	v_mfma_f32_16x16x32_f16 v[90:93], v[162:165], v[194:197], v[90:93]
	v_mfma_f32_16x16x32_f16 v[94:97], v[154:157], v[202:205], v[94:97]
	v_mfma_f32_16x16x32_f16 v[98:101], v[162:165], v[202:205], v[98:101]
	v_mfma_f32_16x16x32_f16 v[102:105], v[154:157], v[210:213], v[102:105]
	v_mfma_f32_16x16x32_f16 v[106:109], v[162:165], v[210:213], v[106:109]
	v_mfma_f32_16x16x32_f16 v[110:113], v[154:157], v[218:221], v[110:113]
	v_mfma_f32_16x16x32_f16 v[86:89], v[158:161], v[198:201], v[86:89]
	v_mfma_f32_16x16x32_f16 v[90:93], v[166:169], v[198:201], v[90:93]
	v_mfma_f32_16x16x32_f16 v[94:97], v[158:161], v[206:209], v[94:97]
	v_mfma_f32_16x16x32_f16 v[98:101], v[166:169], v[206:209], v[98:101]
	v_mfma_f32_16x16x32_f16 v[102:105], v[158:161], v[214:217], v[102:105]
	v_mfma_f32_16x16x32_f16 v[106:109], v[166:169], v[214:217], v[106:109]
	v_mfma_f32_16x16x32_f16 v[110:113], v[158:161], v[222:225], v[110:113]
	v_mfma_f32_16x16x32_f16 v[114:117], v[162:165], v[218:221], v[114:117]
	v_mfma_f32_16x16x32_f16 v[114:117], v[166:169], v[222:225], v[114:117]
	s_setprio 0
	s_barrier
	s_mov_b64 s[0:1], 0x200
	s_mov_b32 m0, s15
	v_lshl_add_u64 v[242:243], v[30:31], 0, s[0:1]
	ds_read_b128 v[226:229], v6
	ds_read_b128 v[230:233], v7
	ds_read_b128 v[234:237], v8
	ds_read_b128 v[238:241], v9
	global_load_lds_dwordx4 v[242:243], off
	v_lshl_add_u64 v[242:243], v[32:33], 0, s[0:1]
	s_mov_b32 m0, s5
	s_nop 0
	global_load_lds_dwordx4 v[242:243], off
	s_barrier
	s_waitcnt lgkmcnt(0)
	s_setprio 1
	s_waitcnt lgkmcnt(0)
	v_mfma_f32_16x16x32_f16 v[134:137], v[226:229], v[194:197], v[134:137]
	v_mfma_f32_16x16x32_f16 v[58:61], v[234:237], v[194:197], v[58:61]
	v_mfma_f32_16x16x32_f16 v[138:141], v[226:229], v[202:205], v[138:141]
	v_mfma_f32_16x16x32_f16 v[62:65], v[234:237], v[202:205], v[62:65]
	v_mfma_f32_16x16x32_f16 v[66:69], v[226:229], v[210:213], v[66:69]
	v_mfma_f32_16x16x32_f16 v[70:73], v[234:237], v[210:213], v[70:73]
	v_mfma_f32_16x16x32_f16 v[74:77], v[226:229], v[218:221], v[74:77]
	v_mfma_f32_16x16x32_f16 v[78:81], v[234:237], v[218:221], v[78:81]
	v_mfma_f32_16x16x32_f16 v[134:137], v[230:233], v[198:201], v[134:137]
	v_mfma_f32_16x16x32_f16 v[58:61], v[238:241], v[198:201], v[58:61]
	v_mfma_f32_16x16x32_f16 v[138:141], v[230:233], v[206:209], v[138:141]
	v_mfma_f32_16x16x32_f16 v[62:65], v[238:241], v[206:209], v[62:65]
	v_mfma_f32_16x16x32_f16 v[66:69], v[230:233], v[214:217], v[66:69]
	v_mfma_f32_16x16x32_f16 v[70:73], v[238:241], v[214:217], v[70:73]
	v_mfma_f32_16x16x32_f16 v[74:77], v[230:233], v[222:225], v[74:77]
	v_mfma_f32_16x16x32_f16 v[78:81], v[238:241], v[222:225], v[78:81]
	s_setprio 0
	s_mov_b32 m0, s17
	v_lshl_add_u64 v[242:243], v[26:27], 0, s[0:1]
	s_barrier
	ds_read_b128 v[194:197], v1 offset:16384
	ds_read_b128 v[198:201], v1 offset:17408
	ds_read_b128 v[202:205], v1 offset:18432
	ds_read_b128 v[206:209], v1 offset:19456
	ds_read_b128 v[210:213], v1 offset:20480
	ds_read_b128 v[214:217], v1 offset:21504
	ds_read_b128 v[218:221], v1 offset:22528
	ds_read_b128 v[222:225], v1 offset:23552
	global_load_lds_dwordx4 v[242:243], off
	v_lshl_add_u64 v[242:243], v[28:29], 0, s[0:1]
	s_mov_b32 m0, s10
	s_nop 0
	global_load_lds_dwordx4 v[242:243], off
	s_barrier
	s_waitcnt lgkmcnt(0)
	s_setprio 1
	s_waitcnt lgkmcnt(0)
	v_mfma_f32_16x16x32_f16 v[126:129], v[154:157], v[218:221], v[126:129]
	v_mfma_f32_16x16x32_f16 v[50:53], v[162:165], v[218:221], v[50:53]
	v_mfma_f32_16x16x32_f16 v[170:173], v[154:157], v[194:197], v[170:173]
	v_mfma_f32_16x16x32_f16 v[174:177], v[162:165], v[194:197], v[174:177]
	v_mfma_f32_16x16x32_f16 v[178:181], v[154:157], v[202:205], v[178:181]
	v_mfma_f32_16x16x32_f16 v[182:185], v[162:165], v[202:205], v[182:185]
	v_mfma_f32_16x16x32_f16 v[186:189], v[154:157], v[210:213], v[186:189]
	v_mfma_f32_16x16x32_f16 v[190:193], v[162:165], v[210:213], v[190:193]
	v_mfma_f32_16x16x32_f16 v[126:129], v[158:161], v[222:225], v[126:129]
	v_mfma_f32_16x16x32_f16 v[50:53], v[166:169], v[222:225], v[50:53]
	v_mfma_f32_16x16x32_f16 v[170:173], v[158:161], v[198:201], v[170:173]
	v_mfma_f32_16x16x32_f16 v[174:177], v[166:169], v[198:201], v[174:177]
	v_mfma_f32_16x16x32_f16 v[178:181], v[158:161], v[206:209], v[178:181]
	v_mfma_f32_16x16x32_f16 v[182:185], v[166:169], v[206:209], v[182:185]
	v_mfma_f32_16x16x32_f16 v[186:189], v[158:161], v[214:217], v[186:189]
	v_mfma_f32_16x16x32_f16 v[190:193], v[166:169], v[214:217], v[190:193]
	s_setprio 0
	s_barrier
	s_mov_b32 m0, s14
	v_lshl_add_u64 v[154:155], v[22:23], 0, s[0:1]
	global_load_lds_dwordx4 v[154:155], off
	v_lshl_add_u64 v[154:155], v[24:25], 0, s[0:1]
	s_mov_b32 m0, s11
	s_nop 0
	global_load_lds_dwordx4 v[154:155], off
	s_waitcnt vmcnt(6)
	s_barrier
	s_setprio 1
	v_mfma_f32_16x16x32_f16 v[82:85], v[234:237], v[194:197], v[82:85]
	v_mfma_f32_16x16x32_f16 v[130:133], v[226:229], v[202:205], v[130:133]
	v_mfma_f32_16x16x32_f16 v[142:145], v[234:237], v[202:205], v[142:145]
	v_mfma_f32_16x16x32_f16 v[146:149], v[226:229], v[210:213], v[146:149]
	v_mfma_f32_16x16x32_f16 v[150:153], v[234:237], v[210:213], v[150:153]
	v_mfma_f32_16x16x32_f16 v[118:121], v[226:229], v[218:221], v[118:121]
	v_mfma_f32_16x16x32_f16 v[122:125], v[234:237], v[218:221], v[122:125]
	v_mfma_f32_16x16x32_f16 v[54:57], v[226:229], v[194:197], v[54:57]
	v_mfma_f32_16x16x32_f16 v[82:85], v[238:241], v[198:201], v[82:85]
	v_mfma_f32_16x16x32_f16 v[130:133], v[230:233], v[206:209], v[130:133]
	v_mfma_f32_16x16x32_f16 v[142:145], v[238:241], v[206:209], v[142:145]
	v_mfma_f32_16x16x32_f16 v[146:149], v[230:233], v[214:217], v[146:149]
	v_mfma_f32_16x16x32_f16 v[150:153], v[238:241], v[214:217], v[150:153]
	v_mfma_f32_16x16x32_f16 v[118:121], v[230:233], v[222:225], v[118:121]
	v_mfma_f32_16x16x32_f16 v[122:125], v[238:241], v[222:225], v[122:125]
	v_mfma_f32_16x16x32_f16 v[54:57], v[230:233], v[198:201], v[54:57]
	s_setprio 0
	s_barrier
	ds_read_b128 v[154:157], v10
	ds_read_b128 v[158:161], v11
	ds_read_b128 v[162:165], v12
	ds_read_b128 v[166:169], v13
	s_mov_b32 m0, s20
	v_lshl_add_u64 v[226:227], v[18:19], 0, s[0:1]
	ds_read_b128 v[194:197], v1 offset:32768
	ds_read_b128 v[198:201], v1 offset:33792
	ds_read_b128 v[202:205], v1 offset:34816
	ds_read_b128 v[206:209], v1 offset:35840
	ds_read_b128 v[210:213], v1 offset:36864
	ds_read_b128 v[214:217], v1 offset:37888
	ds_read_b128 v[218:221], v1 offset:38912
	ds_read_b128 v[222:225], v1 offset:39936
	global_load_lds_dwordx4 v[226:227], off
	v_lshl_add_u64 v[226:227], v[20:21], 0, s[0:1]
	s_mov_b32 m0, s18
	s_nop 0
	global_load_lds_dwordx4 v[226:227], off
	s_waitcnt lgkmcnt(8)
	s_barrier
	s_waitcnt lgkmcnt(0)
	s_setprio 1
	s_waitcnt lgkmcnt(0)
	v_mfma_f32_16x16x32_f16 v[86:89], v[154:157], v[194:197], v[86:89]
	v_mfma_f32_16x16x32_f16 v[90:93], v[162:165], v[194:197], v[90:93]
	v_mfma_f32_16x16x32_f16 v[94:97], v[154:157], v[202:205], v[94:97]
	v_mfma_f32_16x16x32_f16 v[98:101], v[162:165], v[202:205], v[98:101]
	v_mfma_f32_16x16x32_f16 v[102:105], v[154:157], v[210:213], v[102:105]
	v_mfma_f32_16x16x32_f16 v[106:109], v[162:165], v[210:213], v[106:109]
	v_mfma_f32_16x16x32_f16 v[110:113], v[154:157], v[218:221], v[110:113]
	v_mfma_f32_16x16x32_f16 v[86:89], v[158:161], v[198:201], v[86:89]
	v_mfma_f32_16x16x32_f16 v[90:93], v[166:169], v[198:201], v[90:93]
	v_mfma_f32_16x16x32_f16 v[94:97], v[158:161], v[206:209], v[94:97]
	v_mfma_f32_16x16x32_f16 v[98:101], v[166:169], v[206:209], v[98:101]
	v_mfma_f32_16x16x32_f16 v[102:105], v[158:161], v[214:217], v[102:105]
	v_mfma_f32_16x16x32_f16 v[106:109], v[166:169], v[214:217], v[106:109]
	v_mfma_f32_16x16x32_f16 v[110:113], v[158:161], v[222:225], v[110:113]
	v_mfma_f32_16x16x32_f16 v[114:117], v[162:165], v[218:221], v[114:117]
	v_mfma_f32_16x16x32_f16 v[114:117], v[166:169], v[222:225], v[114:117]
	s_setprio 0
	s_barrier
	s_mov_b64 s[0:1], 0x280
	v_readfirstlane_b32 s10, v48
	v_lshl_add_u64 v[242:243], v[30:31], 0, s[0:1]
	s_mov_b32 m0, s10
	v_readfirstlane_b32 s2, v49
	ds_read_b128 v[226:229], v14
	ds_read_b128 v[230:233], v15
	ds_read_b128 v[234:237], v16
	ds_read_b128 v[238:241], v17
	global_load_lds_dwordx4 v[242:243], off
	v_lshl_add_u64 v[242:243], v[32:33], 0, s[0:1]
	s_mov_b32 m0, s2
	s_nop 0
	global_load_lds_dwordx4 v[242:243], off
	s_barrier
	s_waitcnt lgkmcnt(0)
	s_setprio 1
	s_waitcnt lgkmcnt(0)
	v_mfma_f32_16x16x32_f16 v[134:137], v[226:229], v[194:197], v[134:137]
	v_mfma_f32_16x16x32_f16 v[58:61], v[234:237], v[194:197], v[58:61]
	v_mfma_f32_16x16x32_f16 v[138:141], v[226:229], v[202:205], v[138:141]
	v_mfma_f32_16x16x32_f16 v[62:65], v[234:237], v[202:205], v[62:65]
	v_mfma_f32_16x16x32_f16 v[66:69], v[226:229], v[210:213], v[66:69]
	v_mfma_f32_16x16x32_f16 v[70:73], v[234:237], v[210:213], v[70:73]
	v_mfma_f32_16x16x32_f16 v[74:77], v[226:229], v[218:221], v[74:77]
	v_mfma_f32_16x16x32_f16 v[78:81], v[234:237], v[218:221], v[78:81]
	v_mfma_f32_16x16x32_f16 v[134:137], v[230:233], v[198:201], v[134:137]
	v_mfma_f32_16x16x32_f16 v[58:61], v[238:241], v[198:201], v[58:61]
	v_mfma_f32_16x16x32_f16 v[138:141], v[230:233], v[206:209], v[138:141]
	v_mfma_f32_16x16x32_f16 v[62:65], v[238:241], v[206:209], v[62:65]
	v_mfma_f32_16x16x32_f16 v[66:69], v[230:233], v[214:217], v[66:69]
	v_mfma_f32_16x16x32_f16 v[70:73], v[238:241], v[214:217], v[70:73]
	v_mfma_f32_16x16x32_f16 v[74:77], v[230:233], v[222:225], v[74:77]
	v_mfma_f32_16x16x32_f16 v[78:81], v[238:241], v[222:225], v[78:81]
	s_setprio 0
	v_readfirstlane_b32 s11, v46
	v_lshl_add_u64 v[48:49], v[26:27], 0, s[0:1]
	s_mov_b32 m0, s11
	v_readfirstlane_b32 s3, v47
	s_barrier
	ds_read_b128 v[194:197], v1 offset:49152
	ds_read_b128 v[198:201], v1 offset:50176
	ds_read_b128 v[202:205], v1 offset:51200
	ds_read_b128 v[206:209], v1 offset:52224
	ds_read_b128 v[210:213], v1 offset:53248
	ds_read_b128 v[214:217], v1 offset:54272
	ds_read_b128 v[218:221], v1 offset:55296
	ds_read_b128 v[222:225], v1 offset:56320
	global_load_lds_dwordx4 v[48:49], off
	v_lshl_add_u64 v[48:49], v[28:29], 0, s[0:1]
	s_mov_b32 m0, s3
	s_nop 0
	global_load_lds_dwordx4 v[48:49], off
	s_barrier
	s_waitcnt lgkmcnt(0)
	s_setprio 1
	s_waitcnt lgkmcnt(0)
	v_mfma_f32_16x16x32_f16 v[126:129], v[154:157], v[218:221], v[126:129]
	v_mfma_f32_16x16x32_f16 v[50:53], v[162:165], v[218:221], v[50:53]
	v_mfma_f32_16x16x32_f16 v[46:49], v[154:157], v[194:197], v[170:173]
	v_mfma_f32_16x16x32_f16 v[170:173], v[162:165], v[194:197], v[174:177]
	v_mfma_f32_16x16x32_f16 v[174:177], v[154:157], v[202:205], v[178:181]
	v_mfma_f32_16x16x32_f16 v[178:181], v[162:165], v[202:205], v[182:185]
	v_mfma_f32_16x16x32_f16 v[182:185], v[154:157], v[210:213], v[186:189]
	v_mfma_f32_16x16x32_f16 v[186:189], v[162:165], v[210:213], v[190:193]
	v_mfma_f32_16x16x32_f16 v[126:129], v[158:161], v[222:225], v[126:129]
	v_mfma_f32_16x16x32_f16 v[50:53], v[166:169], v[222:225], v[50:53]
	v_mfma_f32_16x16x32_f16 v[46:49], v[158:161], v[198:201], v[46:49]
	v_mfma_f32_16x16x32_f16 v[170:173], v[166:169], v[198:201], v[170:173]
	v_mfma_f32_16x16x32_f16 v[174:177], v[158:161], v[206:209], v[174:177]
	v_mfma_f32_16x16x32_f16 v[178:181], v[166:169], v[206:209], v[178:181]
	v_mfma_f32_16x16x32_f16 v[182:185], v[158:161], v[214:217], v[182:185]
	v_mfma_f32_16x16x32_f16 v[186:189], v[166:169], v[214:217], v[186:189]
	s_setprio 0
	s_barrier
	v_readfirstlane_b32 s5, v37
	v_lshl_add_u64 v[154:155], v[22:23], 0, s[0:1]
	s_mov_b32 m0, s5
	v_readfirstlane_b32 s4, v39
	global_load_lds_dwordx4 v[154:155], off
	v_lshl_add_u64 v[154:155], v[24:25], 0, s[0:1]
	s_mov_b32 m0, s4
	s_nop 0
	global_load_lds_dwordx4 v[154:155], off
	s_waitcnt vmcnt(6)
	s_barrier
	s_setprio 1
	v_mfma_f32_16x16x32_f16 v[82:85], v[234:237], v[194:197], v[82:85]
	v_mfma_f32_16x16x32_f16 v[130:133], v[226:229], v[202:205], v[130:133]
	v_mfma_f32_16x16x32_f16 v[142:145], v[234:237], v[202:205], v[142:145]
	v_mfma_f32_16x16x32_f16 v[146:149], v[226:229], v[210:213], v[146:149]
	v_mfma_f32_16x16x32_f16 v[150:153], v[234:237], v[210:213], v[150:153]
	v_mfma_f32_16x16x32_f16 v[118:121], v[226:229], v[218:221], v[118:121]
	v_mfma_f32_16x16x32_f16 v[122:125], v[234:237], v[218:221], v[122:125]
	v_mfma_f32_16x16x32_f16 v[54:57], v[226:229], v[194:197], v[54:57]
	v_mfma_f32_16x16x32_f16 v[82:85], v[238:241], v[198:201], v[82:85]
	v_mfma_f32_16x16x32_f16 v[130:133], v[230:233], v[206:209], v[130:133]
	v_mfma_f32_16x16x32_f16 v[142:145], v[238:241], v[206:209], v[142:145]
	v_mfma_f32_16x16x32_f16 v[146:149], v[230:233], v[214:217], v[146:149]
	v_mfma_f32_16x16x32_f16 v[150:153], v[238:241], v[214:217], v[150:153]
	v_mfma_f32_16x16x32_f16 v[118:121], v[230:233], v[222:225], v[118:121]
	v_mfma_f32_16x16x32_f16 v[122:125], v[238:241], v[222:225], v[122:125]
	v_mfma_f32_16x16x32_f16 v[54:57], v[230:233], v[198:201], v[54:57]
	s_setprio 0
	s_barrier
	ds_read_b128 v[154:157], v2
	ds_read_b128 v[158:161], v3
	ds_read_b128 v[162:165], v4
	ds_read_b128 v[166:169], v5
	v_readfirstlane_b32 s14, v38
	v_lshl_add_u64 v[190:191], v[18:19], 0, s[0:1]
	s_mov_b32 m0, s14
	v_readfirstlane_b32 s7, v40
	global_load_lds_dwordx4 v[190:191], off
	v_lshl_add_u64 v[38:39], v[20:21], 0, s[0:1]
	s_mov_b32 m0, s7
	s_nop 0
	global_load_lds_dwordx4 v[38:39], off
	ds_read_b128 v[190:193], v1
	ds_read_b128 v[194:197], v1 offset:1024
	ds_read_b128 v[198:201], v1 offset:2048
	ds_read_b128 v[202:205], v1 offset:3072
	ds_read_b128 v[206:209], v1 offset:4096
	ds_read_b128 v[210:213], v1 offset:5120
	ds_read_b128 v[214:217], v1 offset:6144
	ds_read_b128 v[218:221], v1 offset:7168
	s_waitcnt lgkmcnt(8)
	s_barrier
	s_waitcnt lgkmcnt(0)
	s_setprio 1
	s_waitcnt lgkmcnt(0)
	v_mfma_f32_16x16x32_f16 v[86:89], v[154:157], v[190:193], v[86:89]
	v_mfma_f32_16x16x32_f16 v[90:93], v[162:165], v[190:193], v[90:93]
	v_mfma_f32_16x16x32_f16 v[94:97], v[154:157], v[198:201], v[94:97]
	v_mfma_f32_16x16x32_f16 v[98:101], v[162:165], v[198:201], v[98:101]
	v_mfma_f32_16x16x32_f16 v[102:105], v[154:157], v[206:209], v[102:105]
	v_mfma_f32_16x16x32_f16 v[106:109], v[162:165], v[206:209], v[106:109]
	v_mfma_f32_16x16x32_f16 v[110:113], v[154:157], v[214:217], v[110:113]
	v_mfma_f32_16x16x32_f16 v[86:89], v[158:161], v[194:197], v[86:89]
	v_mfma_f32_16x16x32_f16 v[90:93], v[166:169], v[194:197], v[90:93]
	v_mfma_f32_16x16x32_f16 v[94:97], v[158:161], v[202:205], v[94:97]
	v_mfma_f32_16x16x32_f16 v[98:101], v[166:169], v[202:205], v[98:101]
	v_mfma_f32_16x16x32_f16 v[102:105], v[158:161], v[210:213], v[102:105]
	v_mfma_f32_16x16x32_f16 v[106:109], v[166:169], v[210:213], v[106:109]
	v_mfma_f32_16x16x32_f16 v[110:113], v[158:161], v[218:221], v[110:113]
	v_mfma_f32_16x16x32_f16 v[114:117], v[162:165], v[214:217], v[114:117]
	v_mfma_f32_16x16x32_f16 v[114:117], v[166:169], v[218:221], v[114:117]
	s_setprio 0
	s_barrier
	s_mov_b64 s[0:1], 0x300
	v_readfirstlane_b32 s15, v36
	v_lshl_add_u64 v[38:39], v[30:31], 0, s[0:1]
	s_mov_b32 m0, s15
	v_readfirstlane_b32 s15, v41
	ds_read_b128 v[222:225], v6
	ds_read_b128 v[226:229], v7
	ds_read_b128 v[230:233], v8
	ds_read_b128 v[234:237], v9
	global_load_lds_dwordx4 v[38:39], off
	v_lshl_add_u64 v[36:37], v[32:33], 0, s[0:1]
	s_mov_b32 m0, s15
	s_nop 0
	global_load_lds_dwordx4 v[36:37], off
	s_barrier
	s_waitcnt lgkmcnt(0)
	s_setprio 1
	s_waitcnt lgkmcnt(0)
	v_mfma_f32_16x16x32_f16 v[36:39], v[222:225], v[190:193], v[134:137]
	v_mfma_f32_16x16x32_f16 v[58:61], v[230:233], v[190:193], v[58:61]
	v_mfma_f32_16x16x32_f16 v[134:137], v[222:225], v[198:201], v[138:141]
	v_mfma_f32_16x16x32_f16 v[62:65], v[230:233], v[198:201], v[62:65]
	v_mfma_f32_16x16x32_f16 v[66:69], v[222:225], v[206:209], v[66:69]
	v_mfma_f32_16x16x32_f16 v[70:73], v[230:233], v[206:209], v[70:73]
	v_mfma_f32_16x16x32_f16 v[74:77], v[222:225], v[214:217], v[74:77]
	v_mfma_f32_16x16x32_f16 v[78:81], v[230:233], v[214:217], v[78:81]
	v_mfma_f32_16x16x32_f16 v[36:39], v[226:229], v[194:197], v[36:39]
	v_mfma_f32_16x16x32_f16 v[58:61], v[234:237], v[194:197], v[58:61]
	v_mfma_f32_16x16x32_f16 v[134:137], v[226:229], v[202:205], v[134:137]
	v_mfma_f32_16x16x32_f16 v[62:65], v[234:237], v[202:205], v[62:65]
	v_mfma_f32_16x16x32_f16 v[66:69], v[226:229], v[210:213], v[66:69]
	v_mfma_f32_16x16x32_f16 v[70:73], v[234:237], v[210:213], v[70:73]
	v_mfma_f32_16x16x32_f16 v[74:77], v[226:229], v[218:221], v[74:77]
	v_mfma_f32_16x16x32_f16 v[78:81], v[234:237], v[218:221], v[78:81]
	s_setprio 0
	v_readfirstlane_b32 s15, v35
	v_lshl_add_u64 v[40:41], v[26:27], 0, s[0:1]
	s_mov_b32 m0, s15
	v_readfirstlane_b32 s15, v42
	s_barrier
	ds_read_b128 v[138:141], v1 offset:16384
	ds_read_b128 v[190:193], v1 offset:17408
	ds_read_b128 v[194:197], v1 offset:18432
	ds_read_b128 v[198:201], v1 offset:19456
	ds_read_b128 v[202:205], v1 offset:20480
	ds_read_b128 v[206:209], v1 offset:21504
	ds_read_b128 v[210:213], v1 offset:22528
	ds_read_b128 v[214:217], v1 offset:23552
	global_load_lds_dwordx4 v[40:41], off
	v_lshl_add_u64 v[40:41], v[28:29], 0, s[0:1]
	s_mov_b32 m0, s15
	s_nop 0
	global_load_lds_dwordx4 v[40:41], off
	s_barrier
	s_waitcnt lgkmcnt(0)
	s_setprio 1
	s_waitcnt lgkmcnt(0)
	v_mfma_f32_16x16x32_f16 v[126:129], v[154:157], v[210:213], v[126:129]
	v_mfma_f32_16x16x32_f16 v[50:53], v[162:165], v[210:213], v[50:53]
	v_mfma_f32_16x16x32_f16 v[46:49], v[154:157], v[138:141], v[46:49]
	v_mfma_f32_16x16x32_f16 v[170:173], v[162:165], v[138:141], v[170:173]
	v_mfma_f32_16x16x32_f16 v[174:177], v[154:157], v[194:197], v[174:177]
	v_mfma_f32_16x16x32_f16 v[178:181], v[162:165], v[194:197], v[178:181]
	v_mfma_f32_16x16x32_f16 v[182:185], v[154:157], v[202:205], v[182:185]
	v_mfma_f32_16x16x32_f16 v[186:189], v[162:165], v[202:205], v[186:189]
	v_mfma_f32_16x16x32_f16 v[126:129], v[158:161], v[214:217], v[126:129]
	v_mfma_f32_16x16x32_f16 v[50:53], v[166:169], v[214:217], v[50:53]
	v_mfma_f32_16x16x32_f16 v[46:49], v[158:161], v[190:193], v[46:49]
	v_mfma_f32_16x16x32_f16 v[170:173], v[166:169], v[190:193], v[170:173]
	v_mfma_f32_16x16x32_f16 v[174:177], v[158:161], v[198:201], v[174:177]
	v_mfma_f32_16x16x32_f16 v[178:181], v[166:169], v[198:201], v[178:181]
	v_mfma_f32_16x16x32_f16 v[182:185], v[158:161], v[206:209], v[182:185]
	v_mfma_f32_16x16x32_f16 v[186:189], v[166:169], v[206:209], v[186:189]
	s_setprio 0
	s_barrier
	v_readfirstlane_b32 s15, v34
	v_lshl_add_u64 v[40:41], v[22:23], 0, s[0:1]
	s_mov_b32 m0, s15
	v_readfirstlane_b32 s15, v43
	global_load_lds_dwordx4 v[40:41], off
	v_lshl_add_u64 v[34:35], v[24:25], 0, s[0:1]
	s_mov_b32 m0, s15
	s_nop 0
	global_load_lds_dwordx4 v[34:35], off
	s_waitcnt vmcnt(6)
	s_barrier
	s_setprio 1
	v_mfma_f32_16x16x32_f16 v[40:43], v[222:225], v[138:141], v[54:57]
	v_mfma_f32_16x16x32_f16 v[54:57], v[230:233], v[138:141], v[82:85]
	v_mfma_f32_16x16x32_f16 v[82:85], v[222:225], v[194:197], v[130:133]
	v_mfma_f32_16x16x32_f16 v[130:133], v[230:233], v[194:197], v[142:145]
	v_mfma_f32_16x16x32_f16 v[138:141], v[222:225], v[202:205], v[146:149]
	v_mfma_f32_16x16x32_f16 v[142:145], v[230:233], v[202:205], v[150:153]
	v_mfma_f32_16x16x32_f16 v[118:121], v[222:225], v[210:213], v[118:121]
	v_mfma_f32_16x16x32_f16 v[122:125], v[230:233], v[210:213], v[122:125]
	v_mfma_f32_16x16x32_f16 v[82:85], v[226:229], v[198:201], v[82:85]
	v_mfma_f32_16x16x32_f16 v[130:133], v[234:237], v[198:201], v[130:133]
	v_mfma_f32_16x16x32_f16 v[138:141], v[226:229], v[206:209], v[138:141]
	v_mfma_f32_16x16x32_f16 v[142:145], v[234:237], v[206:209], v[142:145]
	v_mfma_f32_16x16x32_f16 v[118:121], v[226:229], v[214:217], v[118:121]
	v_mfma_f32_16x16x32_f16 v[122:125], v[234:237], v[214:217], v[122:125]
	v_mfma_f32_16x16x32_f16 v[40:43], v[226:229], v[190:193], v[40:43]
	v_mfma_f32_16x16x32_f16 v[54:57], v[234:237], v[190:193], v[54:57]
	s_setprio 0
	s_barrier
	ds_read_b128 v[146:149], v10
	ds_read_b128 v[150:153], v11
	ds_read_b128 v[154:157], v12
	ds_read_b128 v[158:161], v13
	v_readfirstlane_b32 s15, v44
	v_lshl_add_u64 v[34:35], v[18:19], 0, s[0:1]
	s_mov_b32 m0, s15
	ds_read_b128 v[162:165], v1 offset:32768
	ds_read_b128 v[166:169], v1 offset:33792
	ds_read_b128 v[190:193], v1 offset:34816
	ds_read_b128 v[194:197], v1 offset:35840
	ds_read_b128 v[198:201], v1 offset:36864
	ds_read_b128 v[202:205], v1 offset:37888
	ds_read_b128 v[206:209], v1 offset:38912
	ds_read_b128 v[210:213], v1 offset:39936
	global_load_lds_dwordx4 v[34:35], off
	v_lshl_add_u64 v[34:35], v[20:21], 0, s[0:1]
	v_readfirstlane_b32 s0, v45
	s_mov_b32 m0, s0
	s_nop 0
	global_load_lds_dwordx4 v[34:35], off
	s_waitcnt lgkmcnt(8)
	s_barrier
	s_waitcnt lgkmcnt(0)
	s_setprio 1
	s_waitcnt lgkmcnt(0)
	v_mfma_f32_16x16x32_f16 v[86:89], v[146:149], v[162:165], v[86:89]
	v_mfma_f32_16x16x32_f16 v[90:93], v[154:157], v[162:165], v[90:93]
	v_mfma_f32_16x16x32_f16 v[94:97], v[146:149], v[190:193], v[94:97]
	v_mfma_f32_16x16x32_f16 v[98:101], v[154:157], v[190:193], v[98:101]
	v_mfma_f32_16x16x32_f16 v[102:105], v[146:149], v[198:201], v[102:105]
	v_mfma_f32_16x16x32_f16 v[106:109], v[154:157], v[198:201], v[106:109]
	v_mfma_f32_16x16x32_f16 v[110:113], v[146:149], v[206:209], v[110:113]
	v_mfma_f32_16x16x32_f16 v[86:89], v[150:153], v[166:169], v[86:89]
	v_mfma_f32_16x16x32_f16 v[90:93], v[158:161], v[166:169], v[90:93]
	v_mfma_f32_16x16x32_f16 v[94:97], v[150:153], v[194:197], v[94:97]
	v_mfma_f32_16x16x32_f16 v[98:101], v[158:161], v[194:197], v[98:101]
	v_mfma_f32_16x16x32_f16 v[102:105], v[150:153], v[202:205], v[102:105]
	v_mfma_f32_16x16x32_f16 v[106:109], v[158:161], v[202:205], v[106:109]
	v_mfma_f32_16x16x32_f16 v[110:113], v[150:153], v[210:213], v[110:113]
	v_mfma_f32_16x16x32_f16 v[114:117], v[154:157], v[206:209], v[114:117]
	v_mfma_f32_16x16x32_f16 v[114:117], v[158:161], v[210:213], v[114:117]
	s_setprio 0
	s_barrier
	s_mov_b64 s[0:1], 0x380
	s_mov_b32 m0, s10
	v_lshl_add_u64 v[30:31], v[30:31], 0, s[0:1]
	ds_read_b128 v[214:217], v14
	ds_read_b128 v[218:221], v15
	ds_read_b128 v[222:225], v16
	ds_read_b128 v[226:229], v17
	global_load_lds_dwordx4 v[30:31], off
	v_lshl_add_u64 v[30:31], v[32:33], 0, s[0:1]
	s_mov_b32 m0, s2
	s_nop 0
	global_load_lds_dwordx4 v[30:31], off
	s_barrier
	s_waitcnt lgkmcnt(0)
	s_setprio 1
	s_waitcnt lgkmcnt(0)
	v_mfma_f32_16x16x32_f16 v[30:33], v[214:217], v[162:165], v[36:39]
	v_mfma_f32_16x16x32_f16 v[34:37], v[222:225], v[162:165], v[58:61]
	v_mfma_f32_16x16x32_f16 v[58:61], v[214:217], v[190:193], v[134:137]
	v_mfma_f32_16x16x32_f16 v[62:65], v[222:225], v[190:193], v[62:65]
	v_mfma_f32_16x16x32_f16 v[66:69], v[214:217], v[198:201], v[66:69]
	v_mfma_f32_16x16x32_f16 v[70:73], v[222:225], v[198:201], v[70:73]
	v_mfma_f32_16x16x32_f16 v[74:77], v[214:217], v[206:209], v[74:77]
	v_mfma_f32_16x16x32_f16 v[78:81], v[222:225], v[206:209], v[78:81]
	v_mfma_f32_16x16x32_f16 v[34:37], v[226:229], v[166:169], v[34:37]
	v_mfma_f32_16x16x32_f16 v[58:61], v[218:221], v[194:197], v[58:61]
	v_mfma_f32_16x16x32_f16 v[62:65], v[226:229], v[194:197], v[62:65]
	v_mfma_f32_16x16x32_f16 v[66:69], v[218:221], v[202:205], v[66:69]
	v_mfma_f32_16x16x32_f16 v[70:73], v[226:229], v[202:205], v[70:73]
	v_mfma_f32_16x16x32_f16 v[74:77], v[218:221], v[210:213], v[74:77]
	v_mfma_f32_16x16x32_f16 v[78:81], v[226:229], v[210:213], v[78:81]
	v_mfma_f32_16x16x32_f16 v[30:33], v[218:221], v[166:169], v[30:33]
	s_setprio 0
	s_mov_b32 m0, s11
	v_lshl_add_u64 v[26:27], v[26:27], 0, s[0:1]
	s_barrier
	ds_read_b128 v[134:137], v1 offset:49152
	ds_read_b128 v[162:165], v1 offset:50176
	ds_read_b128 v[166:169], v1 offset:51200
	ds_read_b128 v[190:193], v1 offset:52224
	ds_read_b128 v[194:197], v1 offset:53248
	ds_read_b128 v[198:201], v1 offset:54272
	ds_read_b128 v[202:205], v1 offset:55296
	ds_read_b128 v[206:209], v1 offset:56320
	global_load_lds_dwordx4 v[26:27], off
	v_lshl_add_u64 v[26:27], v[28:29], 0, s[0:1]
	s_mov_b32 m0, s3
	s_nop 0
	global_load_lds_dwordx4 v[26:27], off
	s_barrier
	s_waitcnt lgkmcnt(0)
	s_setprio 1
	s_waitcnt lgkmcnt(0)
	v_mfma_f32_16x16x32_f16 v[26:29], v[146:149], v[134:137], v[46:49]
	v_mfma_f32_16x16x32_f16 v[126:129], v[146:149], v[202:205], v[126:129]
	v_mfma_f32_16x16x32_f16 v[48:51], v[154:157], v[202:205], v[50:53]
	v_mfma_f32_16x16x32_f16 v[44:47], v[154:157], v[134:137], v[170:173]
	v_mfma_f32_16x16x32_f16 v[170:173], v[146:149], v[166:169], v[174:177]
	v_mfma_f32_16x16x32_f16 v[174:177], v[154:157], v[166:169], v[178:181]
	v_mfma_f32_16x16x32_f16 v[178:181], v[146:149], v[194:197], v[182:185]
	v_mfma_f32_16x16x32_f16 v[182:185], v[154:157], v[194:197], v[186:189]
	v_mfma_f32_16x16x32_f16 v[126:129], v[150:153], v[206:209], v[126:129]
	v_mfma_f32_16x16x32_f16 v[48:51], v[158:161], v[206:209], v[48:51]
	v_mfma_f32_16x16x32_f16 v[26:29], v[150:153], v[162:165], v[26:29]
	v_mfma_f32_16x16x32_f16 v[44:47], v[158:161], v[162:165], v[44:47]
	v_mfma_f32_16x16x32_f16 v[170:173], v[150:153], v[190:193], v[170:173]
	v_mfma_f32_16x16x32_f16 v[174:177], v[158:161], v[190:193], v[174:177]
	v_mfma_f32_16x16x32_f16 v[178:181], v[150:153], v[198:201], v[178:181]
	v_mfma_f32_16x16x32_f16 v[182:185], v[158:161], v[198:201], v[182:185]
	s_setprio 0
	s_barrier
	s_mov_b32 m0, s5
	v_lshl_add_u64 v[22:23], v[22:23], 0, s[0:1]
	global_load_lds_dwordx4 v[22:23], off
	v_lshl_add_u64 v[22:23], v[24:25], 0, s[0:1]
	s_mov_b32 m0, s4
	s_nop 0
	global_load_lds_dwordx4 v[22:23], off
	s_waitcnt vmcnt(6)
	s_barrier
	s_setprio 1
	v_mfma_f32_16x16x32_f16 v[22:25], v[214:217], v[134:137], v[40:43]
	v_mfma_f32_16x16x32_f16 v[38:41], v[222:225], v[134:137], v[54:57]
	v_mfma_f32_16x16x32_f16 v[52:55], v[214:217], v[166:169], v[82:85]
	v_mfma_f32_16x16x32_f16 v[82:85], v[222:225], v[166:169], v[130:133]
	v_mfma_f32_16x16x32_f16 v[130:133], v[214:217], v[194:197], v[138:141]
	v_mfma_f32_16x16x32_f16 v[134:137], v[222:225], v[194:197], v[142:145]
	v_mfma_f32_16x16x32_f16 v[118:121], v[214:217], v[202:205], v[118:121]
	v_mfma_f32_16x16x32_f16 v[122:125], v[222:225], v[202:205], v[122:125]
	v_mfma_f32_16x16x32_f16 v[52:55], v[218:221], v[190:193], v[52:55]
	v_mfma_f32_16x16x32_f16 v[82:85], v[226:229], v[190:193], v[82:85]
	v_mfma_f32_16x16x32_f16 v[130:133], v[218:221], v[198:201], v[130:133]
	v_mfma_f32_16x16x32_f16 v[134:137], v[226:229], v[198:201], v[134:137]
	v_mfma_f32_16x16x32_f16 v[118:121], v[218:221], v[206:209], v[118:121]
	v_mfma_f32_16x16x32_f16 v[122:125], v[226:229], v[206:209], v[122:125]
	v_mfma_f32_16x16x32_f16 v[22:25], v[218:221], v[162:165], v[22:25]
	v_mfma_f32_16x16x32_f16 v[38:41], v[226:229], v[162:165], v[38:41]
	s_setprio 0
	s_mov_b32 m0, s14
	v_lshl_add_u64 v[18:19], v[18:19], 0, s[0:1]
	s_barrier
	ds_read_b128 v[138:141], v2
	ds_read_b128 v[142:145], v3
	ds_read_b128 v[146:149], v4
	ds_read_b128 v[2:5], v5
	global_load_lds_dwordx4 v[18:19], off
	v_lshl_add_u64 v[18:19], v[20:21], 0, s[0:1]
	s_mov_b32 m0, s7
	s_nop 0
	global_load_lds_dwordx4 v[18:19], off
	ds_read_b128 v[18:21], v1
	ds_read_b128 v[150:153], v1 offset:1024
	ds_read_b128 v[154:157], v1 offset:2048
	ds_read_b128 v[158:161], v1 offset:3072
	ds_read_b128 v[162:165], v1 offset:4096
	ds_read_b128 v[166:169], v1 offset:5120
	ds_read_b128 v[186:189], v1 offset:6144
	ds_read_b128 v[190:193], v1 offset:7168
	s_barrier
	s_waitcnt lgkmcnt(0)
	s_setprio 1
	s_waitcnt lgkmcnt(0)
	v_mfma_f32_16x16x32_f16 v[86:89], v[138:141], v[18:21], v[86:89]
	v_mfma_f32_16x16x32_f16 v[90:93], v[146:149], v[18:21], v[90:93]
	v_mfma_f32_16x16x32_f16 v[94:97], v[138:141], v[154:157], v[94:97]
	v_mfma_f32_16x16x32_f16 v[98:101], v[146:149], v[154:157], v[98:101]
	v_mfma_f32_16x16x32_f16 v[102:105], v[138:141], v[162:165], v[102:105]
	v_mfma_f32_16x16x32_f16 v[106:109], v[146:149], v[162:165], v[106:109]
	v_mfma_f32_16x16x32_f16 v[110:113], v[138:141], v[186:189], v[110:113]
	v_mfma_f32_16x16x32_f16 v[86:89], v[142:145], v[150:153], v[86:89]
	v_mfma_f32_16x16x32_f16 v[90:93], v[2:5], v[150:153], v[90:93]
	v_mfma_f32_16x16x32_f16 v[94:97], v[142:145], v[158:161], v[94:97]
	v_mfma_f32_16x16x32_f16 v[98:101], v[2:5], v[158:161], v[98:101]
	v_mfma_f32_16x16x32_f16 v[102:105], v[142:145], v[166:169], v[102:105]
	v_mfma_f32_16x16x32_f16 v[106:109], v[2:5], v[166:169], v[106:109]
	v_mfma_f32_16x16x32_f16 v[110:113], v[142:145], v[190:193], v[110:113]
	v_mfma_f32_16x16x32_f16 v[114:117], v[146:149], v[186:189], v[114:117]
	v_mfma_f32_16x16x32_f16 v[114:117], v[2:5], v[190:193], v[114:117]
	s_setprio 0
	s_barrier
	ds_read_b128 v[194:197], v6
	ds_read_b128 v[198:201], v7
	ds_read_b128 v[202:205], v8
	ds_read_b128 v[6:9], v9
	s_barrier
	s_waitcnt lgkmcnt(0)
	s_setprio 1
	s_waitcnt lgkmcnt(0)
	v_mfma_f32_16x16x32_f16 v[30:33], v[194:197], v[18:21], v[30:33]
	v_mfma_f32_16x16x32_f16 v[18:21], v[202:205], v[18:21], v[34:37]
	v_mfma_f32_16x16x32_f16 v[34:37], v[194:197], v[154:157], v[58:61]
	v_mfma_f32_16x16x32_f16 v[56:59], v[202:205], v[154:157], v[62:65]
	v_mfma_f32_16x16x32_f16 v[60:63], v[194:197], v[162:165], v[66:69]
	v_mfma_f32_16x16x32_f16 v[64:67], v[202:205], v[162:165], v[70:73]
	v_mfma_f32_16x16x32_f16 v[68:71], v[194:197], v[186:189], v[74:77]
	v_mfma_f32_16x16x32_f16 v[72:75], v[202:205], v[186:189], v[78:81]
	v_mfma_f32_16x16x32_f16 v[34:37], v[198:201], v[158:161], v[34:37]
	v_mfma_f32_16x16x32_f16 v[56:59], v[6:9], v[158:161], v[56:59]
	v_mfma_f32_16x16x32_f16 v[60:63], v[198:201], v[166:169], v[60:63]
	v_mfma_f32_16x16x32_f16 v[64:67], v[6:9], v[166:169], v[64:67]
	v_mfma_f32_16x16x32_f16 v[68:71], v[198:201], v[190:193], v[68:71]
	v_mfma_f32_16x16x32_f16 v[72:75], v[6:9], v[190:193], v[72:75]
	v_mfma_f32_16x16x32_f16 v[30:33], v[198:201], v[150:153], v[30:33]
	v_mfma_f32_16x16x32_f16 v[18:21], v[6:9], v[150:153], v[18:21]
	s_setprio 0
	s_barrier
	ds_read_b128 v[76:79], v1 offset:16384
	ds_read_b128 v[150:153], v1 offset:17408
	ds_read_b128 v[154:157], v1 offset:18432
	ds_read_b128 v[158:161], v1 offset:19456
	ds_read_b128 v[162:165], v1 offset:20480
	ds_read_b128 v[166:169], v1 offset:21504
	ds_read_b128 v[186:189], v1 offset:22528
	ds_read_b128 v[190:193], v1 offset:23552
	s_waitcnt vmcnt(4)
	s_barrier
	s_waitcnt lgkmcnt(0)
	s_setprio 1
	s_waitcnt lgkmcnt(0)
	v_mfma_f32_16x16x32_f16 v[42:45], v[146:149], v[76:79], v[44:47]
	v_mfma_f32_16x16x32_f16 v[174:177], v[146:149], v[154:157], v[174:177]
	v_mfma_f32_16x16x32_f16 v[182:185], v[146:149], v[162:165], v[182:185]
	v_mfma_f32_16x16x32_f16 v[46:49], v[146:149], v[186:189], v[48:51]
	v_mfma_f32_16x16x32_f16 v[26:29], v[138:141], v[76:79], v[26:29]
	v_mfma_f32_16x16x32_f16 v[42:45], v[2:5], v[150:153], v[42:45]
	v_mfma_f32_16x16x32_f16 v[170:173], v[138:141], v[154:157], v[170:173]
	v_mfma_f32_16x16x32_f16 v[174:177], v[2:5], v[158:161], v[174:177]
	v_mfma_f32_16x16x32_f16 v[178:181], v[138:141], v[162:165], v[178:181]
	v_mfma_f32_16x16x32_f16 v[182:185], v[2:5], v[166:169], v[182:185]
	v_mfma_f32_16x16x32_f16 v[126:129], v[138:141], v[186:189], v[126:129]
	v_mfma_f32_16x16x32_f16 v[2:5], v[2:5], v[190:193], v[46:49]
	v_mfma_f32_16x16x32_f16 v[26:29], v[142:145], v[150:153], v[26:29]
	v_mfma_f32_16x16x32_f16 v[170:173], v[142:145], v[158:161], v[170:173]
	v_mfma_f32_16x16x32_f16 v[178:181], v[142:145], v[166:169], v[178:181]
	v_mfma_f32_16x16x32_f16 v[206:209], v[142:145], v[190:193], v[126:129]
	s_setprio 0
	s_setprio 1
	v_mfma_f32_16x16x32_f16 v[46:49], v[194:197], v[154:157], v[52:55]
	v_mfma_f32_16x16x32_f16 v[50:53], v[202:205], v[154:157], v[82:85]
	v_mfma_f32_16x16x32_f16 v[210:213], v[6:9], v[158:161], v[50:53]
	v_mfma_f32_16x16x32_f16 v[50:53], v[194:197], v[162:165], v[130:133]
	v_mfma_f32_16x16x32_f16 v[214:217], v[198:201], v[166:169], v[50:53]
	v_mfma_f32_16x16x32_f16 v[50:53], v[202:205], v[162:165], v[134:137]
	v_mfma_f32_16x16x32_f16 v[166:169], v[6:9], v[166:169], v[50:53]
	v_mfma_f32_16x16x32_f16 v[50:53], v[194:197], v[186:189], v[118:121]
	v_mfma_f32_16x16x32_f16 v[22:25], v[194:197], v[76:79], v[22:25]
	v_mfma_f32_16x16x32_f16 v[38:41], v[202:205], v[76:79], v[38:41]
	v_mfma_f32_16x16x32_f16 v[194:197], v[198:201], v[190:193], v[50:53]
	v_mfma_f32_16x16x32_f16 v[50:53], v[202:205], v[186:189], v[122:125]
	v_mfma_f32_16x16x32_f16 v[22:25], v[198:201], v[150:153], v[22:25]
	v_mfma_f32_16x16x32_f16 v[38:41], v[6:9], v[150:153], v[38:41]
	v_mfma_f32_16x16x32_f16 v[46:49], v[198:201], v[158:161], v[46:49]
	v_mfma_f32_16x16x32_f16 v[186:189], v[6:9], v[190:193], v[50:53]
	s_setprio 0
	s_barrier
	ds_read_b128 v[6:9], v10
	ds_read_b128 v[82:85], v11
	ds_read_b128 v[190:193], v12
	ds_read_b128 v[10:13], v13
	ds_read_b128 v[50:53], v1 offset:32768
	ds_read_b128 v[76:79], v1 offset:33792
	ds_read_b128 v[118:121], v1 offset:34816
	ds_read_b128 v[126:129], v1 offset:35840
	ds_read_b128 v[198:201], v1 offset:36864
	ds_read_b128 v[202:205], v1 offset:37888
	ds_read_b128 v[218:221], v1 offset:38912
	ds_read_b128 v[222:225], v1 offset:39936
	s_waitcnt vmcnt(2)
	s_barrier
	s_waitcnt lgkmcnt(0)
	s_setprio 1
	s_waitcnt lgkmcnt(0)
	v_mfma_f32_16x16x32_f16 v[86:89], v[6:9], v[50:53], v[86:89]
	v_mfma_f32_16x16x32_f16 v[162:165], v[82:85], v[76:79], v[86:89]
	v_mfma_f32_16x16x32_f16 v[86:89], v[190:193], v[50:53], v[90:93]
	v_mfma_f32_16x16x32_f16 v[154:157], v[10:13], v[76:79], v[86:89]
	v_mfma_f32_16x16x32_f16 v[86:89], v[6:9], v[118:121], v[94:97]
	v_mfma_f32_16x16x32_f16 v[146:149], v[82:85], v[126:129], v[86:89]
	v_mfma_f32_16x16x32_f16 v[86:89], v[190:193], v[118:121], v[98:101]
	v_mfma_f32_16x16x32_f16 v[138:141], v[10:13], v[126:129], v[86:89]
	v_mfma_f32_16x16x32_f16 v[86:89], v[6:9], v[198:201], v[102:105]
	v_mfma_f32_16x16x32_f16 v[130:133], v[82:85], v[202:205], v[86:89]
	v_mfma_f32_16x16x32_f16 v[86:89], v[190:193], v[198:201], v[106:109]
	v_mfma_f32_16x16x32_f16 v[122:125], v[10:13], v[202:205], v[86:89]
	v_mfma_f32_16x16x32_f16 v[86:89], v[6:9], v[218:221], v[110:113]
	v_mfma_f32_16x16x32_f16 v[110:113], v[82:85], v[222:225], v[86:89]
	v_mfma_f32_16x16x32_f16 v[86:89], v[190:193], v[218:221], v[114:117]
	v_mfma_f32_16x16x32_f16 v[102:105], v[10:13], v[222:225], v[86:89]
	s_setprio 0
	s_barrier
	ds_read_b128 v[114:117], v14
	ds_read_b128 v[226:229], v15
	ds_read_b128 v[230:233], v16
	ds_read_b128 v[234:237], v17
	s_waitcnt vmcnt(0)
	s_barrier
	s_waitcnt lgkmcnt(0)
	s_setprio 1
	s_waitcnt lgkmcnt(0)
	v_mfma_f32_16x16x32_f16 v[14:17], v[114:117], v[50:53], v[30:33]
	v_mfma_f32_16x16x32_f16 v[158:161], v[226:229], v[76:79], v[14:17]
	v_mfma_f32_16x16x32_f16 v[14:17], v[230:233], v[50:53], v[18:21]
	v_mfma_f32_16x16x32_f16 v[150:153], v[234:237], v[76:79], v[14:17]
	v_mfma_f32_16x16x32_f16 v[14:17], v[114:117], v[118:121], v[34:37]
	v_mfma_f32_16x16x32_f16 v[142:145], v[226:229], v[126:129], v[14:17]
	v_mfma_f32_16x16x32_f16 v[14:17], v[230:233], v[118:121], v[56:59]
	v_mfma_f32_16x16x32_f16 v[134:137], v[234:237], v[126:129], v[14:17]
	v_mfma_f32_16x16x32_f16 v[14:17], v[114:117], v[198:201], v[60:63]
	v_mfma_f32_16x16x32_f16 v[126:129], v[226:229], v[202:205], v[14:17]
	v_mfma_f32_16x16x32_f16 v[14:17], v[230:233], v[198:201], v[64:67]
	v_mfma_f32_16x16x32_f16 v[118:121], v[234:237], v[202:205], v[14:17]
	v_mfma_f32_16x16x32_f16 v[14:17], v[114:117], v[218:221], v[68:71]
	v_mfma_f32_16x16x32_f16 v[106:109], v[226:229], v[222:225], v[14:17]
	v_mfma_f32_16x16x32_f16 v[14:17], v[230:233], v[218:221], v[72:75]
	v_mfma_f32_16x16x32_f16 v[98:101], v[234:237], v[222:225], v[14:17]
	s_setprio 0
	s_barrier
	ds_read_b128 v[18:21], v1 offset:49152
	ds_read_b128 v[30:33], v1 offset:50176
	ds_read_b128 v[34:37], v1 offset:51200
	ds_read_b128 v[54:57], v1 offset:52224
	ds_read_b128 v[58:61], v1 offset:53248
	ds_read_b128 v[198:201], v1 offset:54272
	ds_read_b128 v[202:205], v1 offset:55296
	ds_read_b128 v[218:221], v1 offset:56320
	s_barrier
	s_waitcnt lgkmcnt(0)
	s_setprio 1
	s_waitcnt lgkmcnt(0)
	v_mfma_f32_16x16x32_f16 v[14:17], v[6:9], v[18:21], v[26:29]
	v_mfma_f32_16x16x32_f16 v[94:97], v[82:85], v[30:33], v[14:17]
	v_mfma_f32_16x16x32_f16 v[14:17], v[190:193], v[18:21], v[42:45]
	v_mfma_f32_16x16x32_f16 v[86:89], v[10:13], v[30:33], v[14:17]
	v_mfma_f32_16x16x32_f16 v[14:17], v[6:9], v[34:37], v[170:173]
	v_mfma_f32_16x16x32_f16 v[78:81], v[82:85], v[54:57], v[14:17]
	v_mfma_f32_16x16x32_f16 v[14:17], v[190:193], v[34:37], v[174:177]
	v_mfma_f32_16x16x32_f16 v[70:73], v[10:13], v[54:57], v[14:17]
	v_mfma_f32_16x16x32_f16 v[14:17], v[6:9], v[58:61], v[178:181]
	v_mfma_f32_16x16x32_f16 v[62:65], v[82:85], v[198:201], v[14:17]
	v_mfma_f32_16x16x32_f16 v[14:17], v[190:193], v[58:61], v[182:185]
	v_mfma_f32_16x16x32_f16 v[6:9], v[6:9], v[202:205], v[206:209]
	v_mfma_f32_16x16x32_f16 v[2:5], v[190:193], v[202:205], v[2:5]
	v_mfma_f32_16x16x32_f16 v[50:53], v[10:13], v[198:201], v[14:17]
	v_mfma_f32_16x16x32_f16 v[14:17], v[82:85], v[218:221], v[6:9]
	v_mfma_f32_16x16x32_f16 v[10:13], v[10:13], v[218:221], v[2:5]
	s_setprio 0
	s_setprio 1
	v_mfma_f32_16x16x32_f16 v[2:5], v[114:117], v[18:21], v[22:25]
	v_mfma_f32_16x16x32_f16 v[6:9], v[230:233], v[18:21], v[38:41]
	v_mfma_f32_16x16x32_f16 v[90:93], v[226:229], v[30:33], v[2:5]
	v_mfma_f32_16x16x32_f16 v[2:5], v[114:117], v[34:37], v[46:49]
	v_mfma_f32_16x16x32_f16 v[82:85], v[234:237], v[30:33], v[6:9]
	v_mfma_f32_16x16x32_f16 v[6:9], v[230:233], v[34:37], v[210:213]
	v_mfma_f32_16x16x32_f16 v[74:77], v[226:229], v[54:57], v[2:5]
	v_mfma_f32_16x16x32_f16 v[2:5], v[114:117], v[58:61], v[214:217]
	v_mfma_f32_16x16x32_f16 v[66:69], v[234:237], v[54:57], v[6:9]
	v_mfma_f32_16x16x32_f16 v[6:9], v[230:233], v[58:61], v[166:169]
	v_mfma_f32_16x16x32_f16 v[58:61], v[226:229], v[198:201], v[2:5]
	v_mfma_f32_16x16x32_f16 v[2:5], v[114:117], v[202:205], v[194:197]
	v_mfma_f32_16x16x32_f16 v[34:37], v[234:237], v[198:201], v[6:9]
	v_mfma_f32_16x16x32_f16 v[6:9], v[226:229], v[218:221], v[2:5]
	v_mfma_f32_16x16x32_f16 v[2:5], v[230:233], v[202:205], v[186:189]
	v_mfma_f32_16x16x32_f16 v[2:5], v[234:237], v[218:221], v[2:5]
	s_setprio 0
	s_barrier
	s_add_i32 s0, 0, 0x20800
	v_bfe_u32 v166, v0, 4, 2
	v_bfe_u32 v1, v0, 6, 2
	v_lshlrev_b32_e32 v18, 5, v166
	v_lshl_or_b32 v18, v1, 7, v18
	v_add_u32_e32 v19, s0, v18
	s_add_i32 s1, 0, 0x20c00
	v_add_u32_e32 v20, s1, v18
	ds_read_b128 v[54:57], v19
	ds_read_b128 v[46:49], v20
	v_or_b32_e32 v19, 16, v18
	v_add_u32_e32 v20, s0, v19
	v_add_u32_e32 v19, s1, v19
	ds_read_b128 v[42:45], v20
	ds_read_b128 v[38:41], v19
	v_or_b32_e32 v19, 0x200, v18
	v_add_u32_e32 v20, s0, v19
	v_add_u32_e32 v19, s1, v19
	v_or_b32_e32 v18, 0x210, v18
	ds_read_b128 v[30:33], v20
	ds_read_b128 v[26:29], v19
	v_add_u32_e32 v19, s0, v18
	v_and_b32_e32 v114, 15, v0
	v_ashrrev_i32_e32 v0, 2, v0
	s_movk_i32 s0, 0xffc0
	v_and_or_b32 v169, v0, s0, v114
	s_add_i32 s0, 0, 0x20000
	v_add_u32_e32 v18, s1, v18
	v_lshl_add_u32 v168, v169, 3, s0
	ds_read_b128 v[22:25], v19
	ds_read_b128 v[18:21], v18
	s_waitcnt vmcnt(0)
	ds_read2st64_b64 v[114:117], v168 offset1:2
	v_lshlrev_b32_e32 v0, 5, v1
	v_lshlrev_b32_e32 v1, 3, v166
	v_or3_b32 v166, v0, v1, s13
	v_add_u32_e32 v167, s12, v169
	s_waitcnt lgkmcnt(0)
	v_fma_f32 v154, -v114, v42, v154
	v_fma_f32 v154, v115, v154, v38
	v_fma_f32 v1, -v114, v54, v162
	v_fma_f32 v162, -v114, v55, v163
	v_fma_f32 v163, -v114, v56, v164
	v_fma_f32 v164, -v114, v57, v165
	v_max_f32_e32 v165, 0, v154
	v_fma_f32 v154, -v114, v43, v155
	v_fma_f32 v154, v115, v154, v39
	v_max_f32_e32 v170, 0, v154
	v_fma_f32 v154, -v114, v44, v156
	v_fma_f32 v154, v115, v154, v40
	v_max_f32_e32 v156, 0, v154
	v_fma_f32 v154, -v114, v45, v157
	v_fma_f32 v1, v115, v1, v46
	v_fma_f32 v162, v115, v162, v47
	v_fma_f32 v163, v115, v163, v48
	v_fma_f32 v164, v115, v164, v49
	v_fma_f32 v154, v115, v154, v41
	v_mul_lo_u32 v0, v167, s6
	v_max_f32_e32 v1, 0, v1
	v_max_f32_e32 v162, 0, v162
	v_max_f32_e32 v163, 0, v163
	v_max_f32_e32 v164, 0, v164
	v_max_f32_e32 v157, 0, v154
	s_and_b32 s9, s9, 0xffff
	s_mov_b32 s11, 0x20000
	s_mov_b32 s10, 0x7ffffff0
	v_cvt_pk_f16_f32 v155, v163, v164
	v_cvt_pk_f16_f32 v154, v1, v162
	v_cvt_pk_f16_f32 v157, v156, v157
	v_cvt_pk_f16_f32 v156, v165, v170
	v_add_lshl_u32 v0, v166, v0, 1
	buffer_store_dwordx4 v[154:157], v0, s[8:11], 0 offen sc1
	s_and_saveexec_b64 s[24:25], vcc
	s_cbranch_execz .LBB8_8
	s_barrier
.LBB8_8:
	s_or_b64 exec, exec, s[24:25]
	v_fma_f32 v1, -v114, v30, v158
	v_fma_f32 v150, -v114, v22, v150
	v_fma_f32 v154, -v114, v31, v159
	v_fma_f32 v155, -v114, v32, v160
	v_fma_f32 v156, -v114, v33, v161
	v_fma_f32 v151, -v114, v23, v151
	v_fma_f32 v152, -v114, v24, v152
	v_fma_f32 v114, -v114, v25, v153
	v_fma_f32 v1, v115, v1, v26
	v_fma_f32 v154, v115, v154, v27
	v_fma_f32 v155, v115, v155, v28
	v_fma_f32 v156, v115, v156, v29
	v_fma_f32 v150, v115, v150, v18
	v_fma_f32 v151, v115, v151, v19
	v_fma_f32 v152, v115, v152, v20
	v_fma_f32 v114, v115, v114, v21
	v_max_f32_e32 v1, 0, v1
	v_max_f32_e32 v154, 0, v154
	v_max_f32_e32 v155, 0, v155
	v_max_f32_e32 v156, 0, v156
	v_max_f32_e32 v150, 0, v150
	v_max_f32_e32 v151, 0, v151
	v_max_f32_e32 v152, 0, v152
	v_max_f32_e32 v114, 0, v114
	v_cvt_pk_f16_f32 v153, v152, v114
	v_cvt_pk_f16_f32 v152, v150, v151
	v_cvt_pk_f16_f32 v151, v155, v156
	v_cvt_pk_f16_f32 v150, v1, v154
	buffer_store_dwordx4 v[150:153], v0, s[8:11], 0 offen offset:256 sc1
	v_or_b32_e32 v0, 16, v169
	v_add_u32_e32 v114, s12, v0
	v_lshl_add_u32 v0, v0, 3, s0
	ds_read_b64 v[0:1], v0
	v_or_b32_e32 v155, 32, v169
	v_or_b32_e32 v156, 48, v169
	v_mul_lo_u32 v154, v114, s6
	v_lshl_add_u32 v114, v155, 3, s0
	s_waitcnt lgkmcnt(0)
	v_fma_f32 v146, -v0, v54, v146
	v_fma_f32 v147, -v0, v55, v147
	v_fma_f32 v148, -v0, v56, v148
	v_fma_f32 v149, -v0, v57, v149
	v_fma_f32 v138, -v0, v42, v138
	v_fma_f32 v139, -v0, v43, v139
	v_fma_f32 v140, -v0, v44, v140
	v_fma_f32 v141, -v0, v45, v141
	v_fma_f32 v146, v1, v146, v46
	v_fma_f32 v147, v1, v147, v47
	v_fma_f32 v148, v1, v148, v48
	v_fma_f32 v149, v1, v149, v49
	v_fma_f32 v138, v1, v138, v38
	v_fma_f32 v139, v1, v139, v39
	v_fma_f32 v140, v1, v140, v40
	v_fma_f32 v141, v1, v141, v41
	v_lshl_add_u32 v115, v156, 3, s0
	v_max_f32_e32 v146, 0, v146
	v_max_f32_e32 v147, 0, v147
	v_max_f32_e32 v148, 0, v148
	v_max_f32_e32 v149, 0, v149
	v_max_f32_e32 v138, 0, v138
	v_max_f32_e32 v139, 0, v139
	v_max_f32_e32 v140, 0, v140
	v_max_f32_e32 v141, 0, v141
	ds_read_b64 v[152:153], v114
	ds_read_b64 v[114:115], v115
	ds_read_b64 v[150:151], v168 offset:1408
	v_cvt_pk_f16_f32 v141, v140, v141
	v_cvt_pk_f16_f32 v140, v138, v139
	v_cvt_pk_f16_f32 v139, v148, v149
	v_cvt_pk_f16_f32 v138, v146, v147
	v_add_lshl_u32 v146, v166, v154, 1
	buffer_store_dwordx4 v[138:141], v146, s[8:11], 0 offen sc1
	v_fma_f32 v134, -v0, v22, v134
	v_fma_f32 v135, -v0, v23, v135
	v_fma_f32 v138, -v0, v30, v142
	v_fma_f32 v139, -v0, v31, v143
	v_fma_f32 v140, -v0, v32, v144
	v_fma_f32 v141, -v0, v33, v145
	v_fma_f32 v136, -v0, v24, v136
	v_fma_f32 v0, -v0, v25, v137
	v_fma_f32 v136, v1, v136, v20
	v_fma_f32 v0, v1, v0, v21
	v_fma_f32 v138, v1, v138, v26
	v_fma_f32 v139, v1, v139, v27
	v_fma_f32 v140, v1, v140, v28
	v_fma_f32 v141, v1, v141, v29
	v_fma_f32 v134, v1, v134, v18
	v_fma_f32 v135, v1, v135, v19
	v_max_f32_e32 v136, 0, v136
	v_max_f32_e32 v0, 0, v0
	s_waitcnt lgkmcnt(2)
	v_fma_f32 v1, -v152, v54, v130
	v_fma_f32 v130, -v152, v55, v131
	v_fma_f32 v131, -v152, v56, v132
	v_fma_f32 v132, -v152, v57, v133
	v_fma_f32 v122, -v152, v42, v122
	v_fma_f32 v123, -v152, v43, v123
	v_fma_f32 v124, -v152, v44, v124
	v_fma_f32 v125, -v152, v45, v125
	v_cvt_pk_f16_f32 v137, v136, v0
	v_add_u32_e32 v0, s12, v155
	v_fma_f32 v1, v153, v1, v46
	v_fma_f32 v130, v153, v130, v47
	v_fma_f32 v131, v153, v131, v48
	v_fma_f32 v132, v153, v132, v49
	v_fma_f32 v122, v153, v122, v38
	v_fma_f32 v123, v153, v123, v39
	v_fma_f32 v124, v153, v124, v40
	v_fma_f32 v125, v153, v125, v41
	v_max_f32_e32 v138, 0, v138
	v_max_f32_e32 v139, 0, v139
	v_max_f32_e32 v140, 0, v140
	v_max_f32_e32 v141, 0, v141
	v_max_f32_e32 v134, 0, v134
	v_max_f32_e32 v135, 0, v135
	v_mul_lo_u32 v0, v0, s6
	v_max_f32_e32 v1, 0, v1
	v_max_f32_e32 v130, 0, v130
	v_max_f32_e32 v131, 0, v131
	v_max_f32_e32 v132, 0, v132
	v_max_f32_e32 v122, 0, v122
	v_max_f32_e32 v123, 0, v123
	v_max_f32_e32 v124, 0, v124
	v_max_f32_e32 v125, 0, v125
	v_cvt_pk_f16_f32 v136, v134, v135
	v_cvt_pk_f16_f32 v135, v140, v141
	v_cvt_pk_f16_f32 v134, v138, v139
	v_cvt_pk_f16_f32 v125, v124, v125
	v_cvt_pk_f16_f32 v124, v122, v123
	v_cvt_pk_f16_f32 v123, v131, v132
	v_cvt_pk_f16_f32 v122, v1, v130
	v_add_lshl_u32 v0, v166, v0, 1
	buffer_store_dwordx4 v[134:137], v146, s[8:11], 0 offen offset:256 sc1
	buffer_store_dwordx4 v[122:125], v0, s[8:11], 0 offen sc1
	v_fma_f32 v1, -v152, v30, v126
	v_fma_f32 v118, -v152, v22, v118
	v_fma_f32 v122, -v152, v31, v127
	v_fma_f32 v123, -v152, v32, v128
	v_fma_f32 v124, -v152, v33, v129
	v_fma_f32 v119, -v152, v23, v119
	v_fma_f32 v120, -v152, v24, v120
	v_fma_f32 v121, -v152, v25, v121
	v_fma_f32 v1, v153, v1, v26
	v_fma_f32 v122, v153, v122, v27
	v_fma_f32 v123, v153, v123, v28
	v_fma_f32 v124, v153, v124, v29
	v_fma_f32 v118, v153, v118, v18
	v_fma_f32 v119, v153, v119, v19
	v_fma_f32 v120, v153, v120, v20
	v_fma_f32 v121, v153, v121, v21
	v_max_f32_e32 v1, 0, v1
	v_max_f32_e32 v122, 0, v122
	v_max_f32_e32 v123, 0, v123
	v_max_f32_e32 v124, 0, v124
	v_max_f32_e32 v118, 0, v118
	v_max_f32_e32 v119, 0, v119
	v_max_f32_e32 v120, 0, v120
	v_max_f32_e32 v121, 0, v121
	v_cvt_pk_f16_f32 v121, v120, v121
	v_cvt_pk_f16_f32 v120, v118, v119
	v_cvt_pk_f16_f32 v119, v123, v124
	v_cvt_pk_f16_f32 v118, v1, v122
	s_waitcnt lgkmcnt(1)
	v_fma_f32 v1, -v114, v54, v110
	v_fma_f32 v110, -v114, v55, v111
	v_fma_f32 v111, -v114, v56, v112
	v_fma_f32 v112, -v114, v57, v113
	v_fma_f32 v102, -v114, v42, v102
	v_fma_f32 v103, -v114, v43, v103
	v_fma_f32 v104, -v114, v44, v104
	v_fma_f32 v105, -v114, v45, v105
	buffer_store_dwordx4 v[118:121], v0, s[8:11], 0 offen offset:256 sc1
	v_add_u32_e32 v0, s12, v156
	v_fma_f32 v1, v115, v1, v46
	v_fma_f32 v110, v115, v110, v47
	v_fma_f32 v111, v115, v111, v48
	v_fma_f32 v112, v115, v112, v49
	v_fma_f32 v102, v115, v102, v38
	v_fma_f32 v103, v115, v103, v39
	v_fma_f32 v104, v115, v104, v40
	v_fma_f32 v105, v115, v105, v41
	v_mul_lo_u32 v0, v0, s6
	v_max_f32_e32 v1, 0, v1
	v_max_f32_e32 v110, 0, v110
	v_max_f32_e32 v111, 0, v111
	v_max_f32_e32 v112, 0, v112
	v_max_f32_e32 v102, 0, v102
	v_max_f32_e32 v103, 0, v103
	v_max_f32_e32 v104, 0, v104
	v_max_f32_e32 v105, 0, v105
	v_cvt_pk_f16_f32 v105, v104, v105
	v_cvt_pk_f16_f32 v104, v102, v103
	v_cvt_pk_f16_f32 v103, v111, v112
	v_cvt_pk_f16_f32 v102, v1, v110
	v_add_lshl_u32 v0, v166, v0, 1
	buffer_store_dwordx4 v[102:105], v0, s[8:11], 0 offen sc1
	v_fma_f32 v1, -v114, v30, v106
	v_fma_f32 v98, -v114, v22, v98
	v_fma_f32 v102, -v114, v31, v107
	v_fma_f32 v103, -v114, v32, v108
	v_fma_f32 v104, -v114, v33, v109
	v_fma_f32 v99, -v114, v23, v99
	v_fma_f32 v100, -v114, v24, v100
	v_fma_f32 v101, -v114, v25, v101
	v_fma_f32 v1, v115, v1, v26
	v_fma_f32 v102, v115, v102, v27
	v_fma_f32 v103, v115, v103, v28
	v_fma_f32 v104, v115, v104, v29
	v_fma_f32 v98, v115, v98, v18
	v_fma_f32 v99, v115, v99, v19
	v_fma_f32 v100, v115, v100, v20
	v_fma_f32 v101, v115, v101, v21
	v_max_f32_e32 v1, 0, v1
	v_max_f32_e32 v102, 0, v102
	v_max_f32_e32 v103, 0, v103
	v_max_f32_e32 v104, 0, v104
	v_max_f32_e32 v98, 0, v98
	v_max_f32_e32 v99, 0, v99
	v_max_f32_e32 v100, 0, v100
	v_max_f32_e32 v101, 0, v101
	v_cvt_pk_f16_f32 v101, v100, v101
	v_cvt_pk_f16_f32 v100, v98, v99
	v_cvt_pk_f16_f32 v99, v103, v104
	v_cvt_pk_f16_f32 v98, v1, v102
	v_fma_f32 v1, -v116, v54, v94
	v_fma_f32 v94, -v116, v55, v95
	v_fma_f32 v95, -v116, v56, v96
	v_fma_f32 v96, -v116, v57, v97
	v_fma_f32 v86, -v116, v42, v86
	v_fma_f32 v87, -v116, v43, v87
	v_fma_f32 v88, -v116, v44, v88
	v_fma_f32 v89, -v116, v45, v89
	buffer_store_dwordx4 v[98:101], v0, s[8:11], 0 offen offset:256 sc1
	v_add_u32_e32 v0, 0x80, v167
	v_fma_f32 v1, v117, v1, v46
	v_fma_f32 v94, v117, v94, v47
	v_fma_f32 v95, v117, v95, v48
	v_fma_f32 v96, v117, v96, v49
	v_fma_f32 v86, v117, v86, v38
	v_fma_f32 v87, v117, v87, v39
	v_fma_f32 v88, v117, v88, v40
	v_fma_f32 v89, v117, v89, v41
	v_mul_lo_u32 v0, v0, s6
	v_max_f32_e32 v1, 0, v1
	v_max_f32_e32 v94, 0, v94
	v_max_f32_e32 v95, 0, v95
	v_max_f32_e32 v96, 0, v96
	v_max_f32_e32 v86, 0, v86
	v_max_f32_e32 v87, 0, v87
	v_max_f32_e32 v88, 0, v88
	v_max_f32_e32 v89, 0, v89
	v_cvt_pk_f16_f32 v89, v88, v89
	v_cvt_pk_f16_f32 v88, v86, v87
	v_cvt_pk_f16_f32 v87, v95, v96
	v_cvt_pk_f16_f32 v86, v1, v94
	v_add_lshl_u32 v0, v166, v0, 1
	buffer_store_dwordx4 v[86:89], v0, s[8:11], 0 offen sc1
	v_fma_f32 v1, -v116, v30, v90
	v_fma_f32 v82, -v116, v22, v82
	v_fma_f32 v86, -v116, v31, v91
	v_fma_f32 v86, v117, v86, v27
	v_max_f32_e32 v90, 0, v86
	v_fma_f32 v86, -v116, v32, v92
	v_fma_f32 v87, -v116, v33, v93
	v_fma_f32 v83, -v116, v23, v83
	v_fma_f32 v84, -v116, v24, v84
	v_fma_f32 v85, -v116, v25, v85
	v_fma_f32 v86, v117, v86, v28
	v_fma_f32 v87, v117, v87, v29
	v_fma_f32 v82, v117, v82, v18
	v_fma_f32 v83, v117, v83, v19
	v_fma_f32 v84, v117, v84, v20
	v_fma_f32 v85, v117, v85, v21
	v_max_f32_e32 v86, 0, v86
	v_max_f32_e32 v87, 0, v87
	v_max_f32_e32 v82, 0, v82
	v_max_f32_e32 v83, 0, v83
	v_max_f32_e32 v84, 0, v84
	v_max_f32_e32 v85, 0, v85
	v_cvt_pk_f16_f32 v85, v84, v85
	v_cvt_pk_f16_f32 v84, v82, v83
	v_cvt_pk_f16_f32 v83, v86, v87
	ds_read2_b64 v[86:89], v168 offset0:144 offset1:160
	v_fma_f32 v1, v117, v1, v26
	v_max_f32_e32 v1, 0, v1
	v_cvt_pk_f16_f32 v82, v1, v90
	buffer_store_dwordx4 v[82:85], v0, s[8:11], 0 offen offset:256 sc1
	s_waitcnt lgkmcnt(0)
	v_fma_f32 v1, -v86, v54, v78
	v_fma_f32 v78, -v86, v55, v79
	v_fma_f32 v79, -v86, v56, v80
	v_fma_f32 v80, -v86, v57, v81
	v_fma_f32 v70, -v86, v42, v70
	v_fma_f32 v71, -v86, v43, v71
	v_fma_f32 v72, -v86, v44, v72
	v_fma_f32 v73, -v86, v45, v73
	v_add_u32_e32 v0, 0x90, v167
	v_fma_f32 v1, v87, v1, v46
	v_fma_f32 v78, v87, v78, v47
	v_fma_f32 v79, v87, v79, v48
	v_fma_f32 v80, v87, v80, v49
	v_fma_f32 v70, v87, v70, v38
	v_fma_f32 v71, v87, v71, v39
	v_fma_f32 v72, v87, v72, v40
	v_fma_f32 v73, v87, v73, v41
	v_mul_lo_u32 v0, v0, s6
	v_max_f32_e32 v1, 0, v1
	v_max_f32_e32 v78, 0, v78
	v_max_f32_e32 v79, 0, v79
	v_max_f32_e32 v80, 0, v80
	v_max_f32_e32 v70, 0, v70
	v_max_f32_e32 v71, 0, v71
	v_max_f32_e32 v72, 0, v72
	v_max_f32_e32 v73, 0, v73
	v_cvt_pk_f16_f32 v73, v72, v73
	v_cvt_pk_f16_f32 v72, v70, v71
	v_cvt_pk_f16_f32 v71, v79, v80
	v_cvt_pk_f16_f32 v70, v1, v78
	v_add_lshl_u32 v0, v166, v0, 1
	buffer_store_dwordx4 v[70:73], v0, s[8:11], 0 offen sc1
	v_fma_f32 v1, -v86, v30, v74
	v_fma_f32 v66, -v86, v22, v66
	v_fma_f32 v70, -v86, v31, v75
	v_fma_f32 v71, -v86, v32, v76
	v_fma_f32 v72, -v86, v33, v77
	v_fma_f32 v67, -v86, v23, v67
	v_fma_f32 v68, -v86, v24, v68
	v_fma_f32 v69, -v86, v25, v69
	v_fma_f32 v1, v87, v1, v26
	v_fma_f32 v70, v87, v70, v27
	v_fma_f32 v71, v87, v71, v28
	v_fma_f32 v72, v87, v72, v29
	v_fma_f32 v66, v87, v66, v18
	v_fma_f32 v67, v87, v67, v19
	v_fma_f32 v68, v87, v68, v20
	v_fma_f32 v69, v87, v69, v21
	v_max_f32_e32 v1, 0, v1
	v_max_f32_e32 v70, 0, v70
	v_max_f32_e32 v71, 0, v71
	v_max_f32_e32 v72, 0, v72
	v_max_f32_e32 v66, 0, v66
	v_max_f32_e32 v67, 0, v67
	v_max_f32_e32 v68, 0, v68
	v_max_f32_e32 v69, 0, v69
	v_cvt_pk_f16_f32 v69, v68, v69
	v_cvt_pk_f16_f32 v68, v66, v67
	v_cvt_pk_f16_f32 v67, v71, v72
	v_cvt_pk_f16_f32 v66, v1, v70
	v_fma_f32 v1, -v88, v54, v62
	v_fma_f32 v62, -v88, v55, v63
	v_fma_f32 v63, -v88, v56, v64
	v_fma_f32 v64, -v88, v57, v65
	v_fma_f32 v50, -v88, v42, v50
	v_fma_f32 v51, -v88, v43, v51
	v_fma_f32 v52, -v88, v44, v52
	v_fma_f32 v53, -v88, v45, v53
	buffer_store_dwordx4 v[66:69], v0, s[8:11], 0 offen offset:256 sc1
	v_add_u32_e32 v0, 0xa0, v167
	v_fma_f32 v1, v89, v1, v46
	v_fma_f32 v62, v89, v62, v47
	v_fma_f32 v63, v89, v63, v48
	v_fma_f32 v64, v89, v64, v49
	v_fma_f32 v50, v89, v50, v38
	v_fma_f32 v51, v89, v51, v39
	v_fma_f32 v52, v89, v52, v40
	v_fma_f32 v53, v89, v53, v41
	v_mul_lo_u32 v0, v0, s6
	v_max_f32_e32 v1, 0, v1
	v_max_f32_e32 v62, 0, v62
	v_max_f32_e32 v63, 0, v63
	v_max_f32_e32 v64, 0, v64
	v_max_f32_e32 v50, 0, v50
	v_max_f32_e32 v51, 0, v51
	v_max_f32_e32 v52, 0, v52
	v_max_f32_e32 v53, 0, v53
	v_cvt_pk_f16_f32 v53, v52, v53
	v_cvt_pk_f16_f32 v52, v50, v51
	v_cvt_pk_f16_f32 v51, v63, v64
	v_cvt_pk_f16_f32 v50, v1, v62
	v_add_lshl_u32 v0, v166, v0, 1
	buffer_store_dwordx4 v[50:53], v0, s[8:11], 0 offen sc1
	v_fma_f32 v1, -v88, v30, v58
	v_fma_f32 v34, -v88, v22, v34
	v_fma_f32 v50, -v88, v31, v59
	v_fma_f32 v35, -v88, v23, v35
	v_fma_f32 v36, -v88, v24, v36
	v_fma_f32 v37, -v88, v25, v37
	v_fma_f32 v1, v89, v1, v26
	v_fma_f32 v50, v89, v50, v27
	v_fma_f32 v34, v89, v34, v18
	v_fma_f32 v35, v89, v35, v19
	v_fma_f32 v36, v89, v36, v20
	v_fma_f32 v37, v89, v37, v21
	v_max_f32_e32 v1, 0, v1
	v_max_f32_e32 v50, 0, v50
	v_fma_f32 v51, -v88, v32, v60
	v_fma_f32 v52, -v88, v33, v61
	v_max_f32_e32 v34, 0, v34
	v_max_f32_e32 v35, 0, v35
	v_max_f32_e32 v36, 0, v36
	v_max_f32_e32 v37, 0, v37
	v_fma_f32 v51, v89, v51, v28
	v_fma_f32 v52, v89, v52, v29
	v_cvt_pk_f16_f32 v37, v36, v37
	v_cvt_pk_f16_f32 v36, v34, v35
	v_cvt_pk_f16_f32 v34, v1, v50
	v_fma_f32 v1, -v150, v54, v14
	v_fma_f32 v14, -v150, v55, v15
	v_fma_f32 v10, -v150, v42, v10
	v_fma_f32 v11, -v150, v43, v11
	v_fma_f32 v12, -v150, v44, v12
	v_fma_f32 v13, -v150, v45, v13
	v_max_f32_e32 v51, 0, v51
	v_max_f32_e32 v52, 0, v52
	v_fma_f32 v1, v151, v1, v46
	v_fma_f32 v14, v151, v14, v47
	v_fma_f32 v10, v151, v10, v38
	v_fma_f32 v11, v151, v11, v39
	v_fma_f32 v12, v151, v12, v40
	v_fmac_f32_e32 v41, v151, v13
	v_cvt_pk_f16_f32 v35, v51, v52
	v_max_f32_e32 v1, 0, v1
	v_max_f32_e32 v14, 0, v14
	v_max_f32_e32 v10, 0, v10
	v_max_f32_e32 v11, 0, v11
	v_max_f32_e32 v12, 0, v12
	v_max_f32_e32 v13, 0, v41
	buffer_store_dwordx4 v[34:37], v0, s[8:11], 0 offen offset:256 sc1
	v_add_u32_e32 v0, 0xb0, v167
	v_cvt_pk_f16_f32 v13, v12, v13
	v_cvt_pk_f16_f32 v12, v10, v11
	v_cvt_pk_f16_f32 v10, v1, v14
	v_fma_f32 v1, -v150, v31, v7
	v_fma_f32 v3, -v150, v23, v3
	v_mul_lo_u32 v0, v0, s6
	v_fma_f32 v1, v151, v1, v27
	v_fma_f32 v3, v151, v3, v19
	v_fma_f32 v15, -v150, v56, v16
	v_fma_f32 v16, -v150, v57, v17
	v_add_lshl_u32 v14, v166, v0, 1
	v_fma_f32 v0, -v150, v30, v6
	v_max_f32_e32 v6, 0, v1
	v_fma_f32 v1, -v150, v32, v8
	v_fma_f32 v7, -v150, v33, v9
	v_fma_f32 v2, -v150, v22, v2
	v_max_f32_e32 v8, 0, v3
	v_fma_f32 v3, -v150, v24, v4
	v_fma_f32 v4, -v150, v25, v5
	v_fma_f32 v15, v151, v15, v48
	v_fmac_f32_e32 v49, v151, v16
	v_fma_f32 v0, v151, v0, v26
	v_fma_f32 v1, v151, v1, v28
	v_fmac_f32_e32 v29, v151, v7
	v_fma_f32 v2, v151, v2, v18
	v_fma_f32 v3, v151, v3, v20
	v_fmac_f32_e32 v21, v151, v4
	v_max_f32_e32 v15, 0, v15
	v_max_f32_e32 v16, 0, v49
	v_max_f32_e32 v0, 0, v0
	v_max_f32_e32 v1, 0, v1
	v_max_f32_e32 v7, 0, v29
	v_max_f32_e32 v2, 0, v2
	v_max_f32_e32 v3, 0, v3
	v_max_f32_e32 v4, 0, v21
	v_cvt_pk_f16_f32 v11, v15, v16
	v_cvt_pk_f16_f32 v3, v3, v4
	v_cvt_pk_f16_f32 v2, v2, v8
	v_cvt_pk_f16_f32 v1, v1, v7
	v_cvt_pk_f16_f32 v0, v0, v6
	buffer_store_dwordx4 v[10:13], v14, s[8:11], 0 offen sc1
	buffer_store_dwordx4 v[0:3], v14, s[8:11], 0 offen offset:256 sc1
	s_endpgm

	.amdhsa_kernel _Z6gemm_qILi1ELi0EEvPKDF16_S1_iiiiiiPKfS3_S3_S3_PDF16_8ConvArgs
		.amdhsa_group_segment_fixed_size 0
		.amdhsa_private_segment_fixed_size 0
		.amdhsa_kernarg_size 224
		.amdhsa_user_sgpr_count 2
		.amdhsa_user_sgpr_dispatch_ptr 0
		.amdhsa_user_sgpr_queue_ptr 0
		.amdhsa_user_sgpr_kernarg_segment_ptr 1
		.amdhsa_user_sgpr_dispatch_id 0
		.amdhsa_user_sgpr_kernarg_preload_length 0
		.amdhsa_user_sgpr_kernarg_preload_offset 0
		.amdhsa_user_sgpr_private_segment_size 0
		.amdhsa_uses_dynamic_stack 0
		.amdhsa_enable_private_segment 0
		.amdhsa_system_sgpr_workgroup_id_x 1
		.amdhsa_system_sgpr_workgroup_id_y 0
		.amdhsa_system_sgpr_workgroup_id_z 0
		.amdhsa_system_sgpr_workgroup_info 0
		.amdhsa_system_vgpr_workitem_id 0
		.amdhsa_next_free_vgpr 244
		.amdhsa_next_free_sgpr 26
		.amdhsa_accum_offset 244
		.amdhsa_reserve_vcc 1
		.amdhsa_float_round_mode_32 0
		.amdhsa_float_round_mode_16_64 0
		.amdhsa_float_denorm_mode_32 3
		.amdhsa_float_denorm_mode_16_64 3
		.amdhsa_dx10_clamp 1
		.amdhsa_ieee_mode 1
		.amdhsa_fp16_overflow 0
		.amdhsa_tg_split 0
		.amdhsa_exception_fp_ieee_invalid_op 0
		.amdhsa_exception_fp_denorm_src 0
		.amdhsa_exception_fp_ieee_div_zero 0
		.amdhsa_exception_fp_ieee_overflow 0
		.amdhsa_exception_fp_ieee_underflow 0
		.amdhsa_exception_fp_ieee_inexact 0
		.amdhsa_exception_int_div_zero 0
	.end_amdhsa_kernel
